# v36 + instruction-cache scouts: during the grid barriers before out-proj, MoE1, MoE2 and final, waves 1-7 hop through s_cbranch_execz stones planted every 128-192 B in the next phase's once-executed c
# baseline (speedup 1.0000x reference)
.LBB0_1000:
	s_waitcnt vmcnt(0)
	v_cmp_eq_u32_e32 vcc, 0, v0
	s_barrier
	s_cmp_eq_u32 s80, 0
	s_cbranch_scc1 .Lct_op
	s_cmp_gt_u32 s80, 2
	s_cbranch_scc1 .Lct_op
	s_getpc_b64 s[0:1]
	s_add_u32 s0, s0, 0x2524
	s_addc_u32 s1, s1, 0
	s_lshl_b32 s32, s80, 13
	v_lshl_add_u32 v2, v170, 7, s32
	global_load_dword v3, v2, s[0:1]

.LBB0_1033:
	s_cbranch_execz .Lsc_disp_op

.LBB0_1123:
.Lst_op_0:
	s_cbranch_execz .Lst_op_7
	s_cmp_lt_i32 s92, 9
	s_cselect_b64 s[2:3], -1, 0
	s_and_b64 s[0:1], s[2:3], s[4:5]
	s_andn2_b64 vcc, exec, s[0:1]
	s_cbranch_vccnz .LBB0_1137
	s_and_b32 s1, s96, 7
	s_ashr_i32 s4, s72, 3
	s_mul_i32 s1, s1, s4
	s_ashr_i32 s4, s96, 3
	s_and_b32 s0, s72, 7
	s_add_i32 s4, s4, s1
	s_cmp_eq_u32 s0, 0
	s_cselect_b32 s21, s4, s96
	s_cmpk_gt_i32 s21, 0xff
	s_mov_b32 s9, 0
	s_cbranch_scc1 .LBB0_1136
	s_add_u32 s10, s70, 0xc038000
	s_addc_u32 s11, s71, 0
	s_add_u32 s14, s70, 0xa038000
	v_lshrrev_b32_e32 v166, 4, v170
	s_waitcnt vmcnt(23)
	v_lshrrev_b32_e32 v2, 1, v0
	s_addc_u32 s15, s71, 0
	v_bfe_u32 v3, v0, 1, 3
	v_bitop3_b32 v2, v166, v2, 7 bitop3:0x78
	s_add_u32 s16, s70, 0xa058000
	v_lshlrev_b32_e32 v169, 4, v2
.Lst_op_1:
	s_cbranch_execz .Lst_op_8
	v_bitop3_b32 v2, v166, v3, 4 bitop3:0x36
	s_addc_u32 s17, s71, 0
	v_lshlrev_b32_e32 v171, 4, v2
	v_bfe_u32 v2, v0, 2, 2
	v_lshrrev_b32_e32 v3, 2, v170
	s_add_u32 s27, s70, 0x20368000
	v_and_or_b32 v3, v3, 4, v2
	v_lshlrev_b32_e32 v5, 9, v2
	v_lshlrev_b32_e32 v2, 3, v0
	s_waitcnt vmcnt(7)
	v_and_b32_e32 v6, 31, v0
	s_addc_u32 s28, s71, 0
	v_lshlrev_b32_e32 v172, 5, v3
	v_and_b32_e32 v3, 24, v2
	v_lshlrev_b32_e32 v2, 3, v6
	s_add_u32 s18, s70, 0xe038000
	s_movk_i32 s0, 0x70
	s_addc_u32 s19, s71, 0
	v_lshlrev_b32_e32 v146, 1, v2
	v_mbcnt_lo_u32_b32 v2, -1, 0
	v_lshrrev_b32_e32 v149, 3, v0
	v_bitop3_b32 v159, v158, s0, v0 bitop3:0x48
	v_lshrrev_b32_e32 v167, 5, v170
	v_and_b32_e32 v168, 0x1f0, v158
.Lst_op_2:
	s_cbranch_execz .Lst_op_9
	v_lshlrev_b32_e32 v4, 12, v166
	s_add_u32 s29, s70, 0x6200
	s_mov_b32 s4, 0x358637bd
	v_mbcnt_hi_u32_b32 v2, -1, v2
	v_and_b32_e32 v1, 15, v0
	v_lshl_or_b32 v173, v167, 12, v168
	v_mov_b32_e32 v147, 0
	v_or_b32_e32 v174, 0x40000, v159
	v_or_b32_e32 v175, 0xc0000, v159
	v_lshl_add_u32 v148, v6, 4, 0
	v_cmp_eq_u32_e64 s[0:1], 0, v0
	s_addc_u32 s30, s71, 0
	v_or3_b32 v176, v4, v5, v3
	v_or_b32_e32 v177, 0xc0100, v159
	v_or_b32_e32 v178, 0xc0900, v159
	s_mov_b32 s20, 0x3a800000
	s_waitcnt vmcnt(4)
	v_mov_b64_e32 v[150:151], s[4:5]
	s_mov_b32 s31, 0x800000
.Lst_op_3:
	s_cbranch_execz .Lst_op_10
	s_mov_b32 s33, 0xf800000
	v_mov_b32_e32 v179, 0x260
	v_lshlrev_b32_e32 v180, 12, v149
	s_add_i32 s34, 0, 0x20000
	s_movk_i32 s35, 0x210
	v_and_b32_e32 v181, 64, v2
	s_mov_b32 s4, s21
	s_mov_b32 s36, 0
	s_branch .LBB0_1128

.Lst_op_4:
	s_cbranch_execz .Lst_op_11
	s_mul_i32 s4, s72, s36
	s_add_i32 s4, s4, s21
	s_cmpk_lt_i32 s4, 0x100
	s_cbranch_scc0 .LBB0_1136

.Lst_op_5:
	s_cbranch_execz .Lst_op_12
	s_add_i32 s43, s44, 0
	s_mov_b32 s4, m0
	s_mov_b32 m0, s43
	s_nop 0
	global_load_lds_dwordx4 v18, s[10:11]
	s_mov_b32 m0, s4
	s_add_i32 s45, s44, 0x2000
	s_add_i32 s4, s45, 0
	s_add_i32 s46, s44, 0x4000
	v_add_u32_e32 v19, v2, v174
	s_bfe_u32 s42, s26, 0x20006
	s_mov_b32 s5, m0
	s_mov_b32 m0, s4
	s_nop 0
	global_load_lds_dwordx4 v19, s[10:11]
	s_mov_b32 m0, s5
	s_add_i32 s4, s46, 0
	s_add_i32 s47, s44, 0x6000
	v_or_b32_e32 v3, 0x80000, v18
	v_add_u32_e32 v20, v2, v175
	s_lshl_b32 s8, s38, 1
	s_lshl_b32 s40, s42, 7
	s_mov_b32 s5, m0
	s_mov_b32 m0, s4
	s_nop 0
.Lst_op_6:
	s_cbranch_execz .Lst_op_13
	global_load_lds_dwordx4 v3, s[10:11]
	s_mov_b32 m0, s5
	s_add_i32 s4, s47, 0
	s_mov_b32 s5, m0
	s_mov_b32 m0, s4
	s_nop 0
	global_load_lds_dwordx4 v20, s[10:11]
	s_mov_b32 m0, s5
	s_and_b32 s6, s38, 4
	s_or_b32 s7, s40, 32
	s_or_b32 s51, s40, 64
	s_or_b32 s52, s40, 0x60
	s_lshl_b64 s[4:5], s[8:9], 12
	s_add_u32 s4, s49, s4
	s_addc_u32 s5, s50, s5
	global_load_dwordx4 v[2:5], v173, s[4:5]
	s_add_i32 s4, s8, 16
	s_mov_b32 s5, s9
	s_lshl_b64 s[4:5], s[4:5], 12
	s_add_u32 s4, s49, s4
	s_addc_u32 s5, s50, s5
	global_load_dwordx4 v[6:9], v173, s[4:5]
	s_add_i32 s4, s8, 32
	s_mov_b32 s5, s9
	s_lshl_b64 s[4:5], s[4:5], 12
	s_add_u32 s4, s49, s4
	s_addc_u32 s5, s50, s5
.Lst_op_7:
	s_cbranch_execz .Lst_op_14
	global_load_dwordx4 v[10:13], v173, s[4:5]
	s_add_i32 s4, s8, 48
	s_mov_b32 s5, s9
	s_lshl_b64 s[4:5], s[4:5], 12
	s_add_u32 s4, s49, s4
	s_addc_u32 s5, s50, s5
	global_load_dwordx4 v[14:17], v173, s[4:5]
	s_add_i32 s4, s43, 0x8000
	v_or_b32_e32 v21, 0x80, v18
	s_mov_b32 s5, m0
	s_mov_b32 m0, s4
	s_nop 0
	global_load_lds_dwordx4 v21, s[10:11]
	s_mov_b32 m0, s5
	s_add_i32 s4, s43, 0xa000
	v_or_b32_e32 v19, 0x80, v19
	s_mov_b32 s5, m0
	s_mov_b32 m0, s4
	s_nop 0
	global_load_lds_dwordx4 v19, s[10:11]
	s_mov_b32 m0, s5
	v_or_b32_e32 v18, 0x80080, v18
	s_add_i32 s4, s43, 0xc000
.Lst_op_8:
	s_cbranch_execz .Lst_op_15
	s_add_i32 s43, s43, 0xe000
	s_mov_b32 s5, m0
	s_mov_b32 m0, s4
	s_nop 0
	global_load_lds_dwordx4 v18, s[10:11]
	s_mov_b32 m0, s5
	v_or_b32_e32 v18, 0x80, v20
	s_mov_b32 s4, m0
	s_mov_b32 m0, s43
	s_nop 0
	global_load_lds_dwordx4 v18, s[10:11]
	s_mov_b32 m0, s4
	s_add_i32 s43, s39, s25
	s_waitcnt vmcnt(1)
	v_or_b32_e32 v38, s43, v170
	v_ashrrev_i32_e32 v39, 31, v38
	v_lshlrev_b64 v[18:19], 6, v[38:39]
	v_lshl_add_u64 v[30:31], s[16:17], 0, v[18:19]
	global_load_dwordx4 v[18:21], v[30:31], off
	global_load_dwordx4 v[22:25], v[30:31], off offset:32
	global_load_dwordx4 v[26:29], v[30:31], off offset:16
	s_nop 0
	global_load_dwordx4 v[30:33], v[30:31], off offset:48
.Lst_op_9:
	s_cbranch_execz .Lst_op_16
	v_lshl_add_u64 v[34:35], v[38:39], 4, s[14:15]
	global_load_dwordx4 v[34:37], v[34:35], off
	v_or_b32_e32 v54, 64, v38
	v_ashrrev_i32_e32 v55, 31, v54
	v_lshlrev_b64 v[38:39], 6, v[54:55]
	v_lshl_add_u64 v[50:51], s[16:17], 0, v[38:39]
	global_load_dwordx4 v[38:41], v[50:51], off
	global_load_dwordx4 v[42:45], v[50:51], off offset:32
	global_load_dwordx4 v[46:49], v[50:51], off offset:16
	s_nop 0
	global_load_dwordx4 v[50:53], v[50:51], off offset:48
	v_or_b32_e32 v58, s8, v167
	v_and_or_b32 v56, v58, 3, s6
	v_lshl_add_u64 v[54:55], v[54:55], 4, s[14:15]
	v_lshlrev_b32_e32 v60, 5, v56
	global_load_dwordx4 v[54:57], v[54:55], off
	v_lshlrev_b32_e32 v62, 9, v58
	v_bitop3_b32 v156, s7, v176, v172 bitop3:0xde
	v_bitop3_b32 v160, v60, v62, v168 bitop3:0xde
.Lst_op_10:
	s_cbranch_execz .Lst_op_17
	v_or_b32_e32 v61, s39, v1
	v_bitop3_b32 v157, s40, v176, v172 bitop3:0xde
	v_bitop3_b32 v155, s51, v176, v172 bitop3:0xde
	v_bitop3_b32 v153, s52, v176, v172 bitop3:0xde
	v_mov_b32_e32 v60, v147
	v_mov_b32_e32 v62, 0
	v_mov_b32_e32 v63, v147
	v_mov_b32_e32 v64, v147
	v_mov_b32_e32 v65, v147
	v_mov_b32_e32 v66, 0
	v_mov_b32_e32 v67, v147
	v_mov_b32_e32 v68, v147
	v_mov_b32_e32 v69, v147
	v_mov_b32_e32 v70, 0
	v_mov_b32_e32 v71, v147
	v_mov_b32_e32 v72, v147
	v_mov_b32_e32 v73, v147
	v_mov_b32_e32 v74, 0
	v_mov_b32_e32 v75, v147
	s_waitcnt vmcnt(10)
	v_mov_b32_e32 v76, v147
	v_mov_b32_e32 v77, v147
	v_mov_b32_e32 v78, 0
	v_mov_b32_e32 v79, v147
	v_mov_b32_e32 v80, v147
	v_mov_b32_e32 v81, v147
	v_mov_b32_e32 v82, 0
	v_mov_b32_e32 v83, v147
	v_mov_b32_e32 v84, v147
.Lst_op_11:
	s_cbranch_execz .Lst_op_18
	v_mov_b32_e32 v85, v147
	v_mov_b32_e32 v86, 0
	v_mov_b32_e32 v87, v147
	v_mov_b32_e32 v88, v147
	v_mov_b32_e32 v89, v147
	v_mov_b32_e32 v90, 0
	v_mov_b32_e32 v91, v147
	v_mov_b32_e32 v92, v147
	v_mov_b32_e32 v93, v147
	v_mov_b32_e32 v94, 0
	v_mov_b32_e32 v95, v147
	v_mov_b32_e32 v96, v147
	v_mov_b32_e32 v97, v147
	v_mov_b32_e32 v98, 0
	v_mov_b32_e32 v99, v147
	v_mov_b32_e32 v100, v147
	v_mov_b32_e32 v101, v147
	v_mov_b32_e32 v102, 0
	v_mov_b32_e32 v103, v147
	v_mov_b32_e32 v104, v147
	v_mov_b32_e32 v105, v147
	v_mov_b32_e32 v106, 0
	v_mov_b32_e32 v107, v147
	v_mov_b32_e32 v108, v147
	v_mov_b32_e32 v109, v147
	v_mov_b32_e32 v110, 0
	v_mov_b32_e32 v111, v147
	v_mov_b32_e32 v112, v147
	v_mov_b32_e32 v113, v147
	v_mov_b32_e32 v114, 0
	v_mov_b32_e32 v115, v147
	v_mov_b32_e32 v116, v147
.Lst_op_12:
	s_cbranch_execz .Lst_op_19
	v_mov_b32_e32 v117, v147
	s_waitcnt vmcnt(9)
	v_mov_b32_e32 v58, v18
	s_waitcnt vmcnt(8)
	v_mov_b32_e32 v59, v22
	v_mov_b32_e32 v22, v19
	v_pk_add_f32 v[18:19], v[58:59], v[22:23]
	v_mov_b32_e32 v22, v20
	v_mov_b32_e32 v23, v24
	v_mov_b32_e32 v24, v21
	v_pk_add_f32 v[20:21], v[22:23], v[24:25]
	s_waitcnt vmcnt(7)
	v_mov_b32_e32 v22, v28
	v_pk_add_f32 v[18:19], v[18:19], v[20:21]
	v_mov_b32_e32 v20, v26
	s_waitcnt vmcnt(6)
	v_mov_b32_e32 v21, v30
	v_mov_b32_e32 v30, v27
	v_mov_b32_e32 v23, v32
	v_mov_b32_e32 v32, v29
	v_pk_add_f32 v[20:21], v[20:21], v[30:31]
	v_pk_add_f32 v[22:23], v[22:23], v[32:33]
	v_mov_b32_e32 v58, 0
	v_pk_add_f32 v[20:21], v[20:21], v[22:23]
	v_mov_b32_e32 v59, v147
	v_pk_add_f32 v[18:19], v[18:19], v[20:21]
.Lst_op_13:
	s_cbranch_execz .Lst_op_20
	s_waitcnt vmcnt(5)
	v_mov_b32_e32 v20, v35
	v_mov_b32_e32 v21, v36
	v_mov_b32_e32 v35, v37
	v_pk_add_f32 v[20:21], v[20:21], v[34:35]
	v_mov_b32_e32 v23, v18
	v_mov_b32_e32 v22, v20
	v_mov_b32_e32 v18, v21
	v_pk_add_f32 v[18:19], v[22:23], v[18:19]
	s_waitcnt vmcnt(1)
	v_mov_b32_e32 v23, v52
	v_pk_fma_f32 v[18:19], v[18:19], s[20:21], v[150:151] op_sel_hi:[1,0,0]
	v_mov_b32_e32 v52, v49
	v_mul_f32_e32 v20, 0x4b800000, v19
	v_cmp_gt_f32_e32 vcc, s31, v19
	v_mul_f32_e32 v22, 0x4b800000, v18
	v_cmp_gt_f32_e64 s[4:5], s31, v18
	v_cndmask_b32_e32 v20, v19, v20, vcc
	v_rsq_f32_e32 v20, v20
	v_cndmask_b32_e64 v18, v18, v22, s[4:5]
	v_mul_f32_e32 v22, 0x4f800000, v19
	v_cmp_gt_f32_e64 s[6:7], s33, v19
	v_rsq_f32_e32 v18, v18
.Lst_op_14:
	s_cbranch_execz .Lst_op_21
	v_mul_f32_e32 v21, 0x45800000, v20
	v_cndmask_b32_e64 v24, v19, v22, s[6:7]
	v_sqrt_f32_e32 v19, v24
	v_cndmask_b32_e32 v183, v20, v21, vcc
	v_mul_f32_e32 v20, 0x45800000, v18
	v_cndmask_b32_e64 v25, v18, v20, s[4:5]
	v_add_u32_e32 v18, -1, v19
	v_fma_f32 v20, -v18, v19, v24
	v_cmp_ge_f32_e32 vcc, 0, v20
	v_add_u32_e32 v20, 1, v19
	v_mov_b32_e32 v21, v44
	v_cndmask_b32_e32 v18, v19, v18, vcc
	v_fma_f32 v19, -v20, v19, v24
	v_cmp_lt_f32_e32 vcc, 0, v19
	v_mov_b32_e32 v44, v41
	v_mov_b32_e32 v22, v48
	v_cndmask_b32_e32 v18, v18, v20, vcc
	v_mul_f32_e32 v19, 0x37800000, v18
	v_cndmask_b32_e64 v26, v18, v19, s[6:7]
	v_mov_b32_e32 v18, v38
	v_mov_b32_e32 v19, v42
	v_mov_b32_e32 v42, v39
	v_mov_b32_e32 v20, v40
	v_pk_add_f32 v[18:19], v[18:19], v[42:43]
.Lst_op_15:
	s_cbranch_execz .Lst_op_22
	v_pk_add_f32 v[20:21], v[20:21], v[44:45]
	v_pk_add_f32 v[22:23], v[22:23], v[52:53]
	v_pk_add_f32 v[18:19], v[18:19], v[20:21]
	v_mov_b32_e32 v20, v46
	v_mov_b32_e32 v21, v50
	v_mov_b32_e32 v50, v47
	v_pk_add_f32 v[20:21], v[20:21], v[50:51]
	v_cmp_class_f32_e64 s[4:5], v24, v179
	v_pk_add_f32 v[20:21], v[20:21], v[22:23]
	v_lshlrev_b32_e32 v34, 7, v61
	v_pk_add_f32 v[18:19], v[18:19], v[20:21]
	s_waitcnt vmcnt(0)
	v_mov_b32_e32 v20, v55
	v_mov_b32_e32 v21, v56
	v_mov_b32_e32 v55, v57
	v_pk_add_f32 v[20:21], v[20:21], v[54:55]
	v_mov_b32_e32 v23, v18
	v_mov_b32_e32 v22, v20
	v_mov_b32_e32 v18, v21
	v_pk_add_f32 v[18:19], v[22:23], v[18:19]
	v_cndmask_b32_e64 v21, v26, v24, s[4:5]
	v_pk_fma_f32 v[18:19], v[18:19], s[20:21], v[150:151] op_sel_hi:[1,0,0]
.Lst_op_16:
	s_cbranch_execz .Lst_op_23
	v_mul_f32_e32 v165, v21, v25
	v_mul_f32_e32 v20, 0x4b800000, v19
	v_cmp_gt_f32_e32 vcc, s31, v19
	v_mul_f32_e32 v22, 0x4b800000, v18
	v_cmp_gt_f32_e64 s[4:5], s31, v18
	v_cndmask_b32_e32 v20, v19, v20, vcc
	v_rsq_f32_e32 v20, v20
	v_cndmask_b32_e64 v18, v18, v22, s[4:5]
	v_mul_f32_e32 v22, 0x4f800000, v19
	v_cmp_gt_f32_e64 s[6:7], s33, v19
	v_rsq_f32_e32 v18, v18
	v_mul_f32_e32 v21, 0x45800000, v20
	v_cndmask_b32_e64 v19, v19, v22, s[6:7]
	v_sqrt_f32_e32 v22, v19
	v_cndmask_b32_e32 v182, v20, v21, vcc
	v_mul_f32_e32 v20, 0x45800000, v18
	v_cndmask_b32_e64 v18, v18, v20, s[4:5]
	v_add_u32_e32 v20, -1, v22
	v_fma_f32 v21, -v20, v22, v19
	v_cmp_ge_f32_e32 vcc, 0, v21
	v_add_u32_e32 v21, 1, v22
.Lst_op_17:
	s_cbranch_execz .Lst_op_24
	s_add_i32 s4, s8, 64
	v_cndmask_b32_e32 v20, v22, v20, vcc
	v_fma_f32 v22, -v21, v22, v19
	v_cmp_lt_f32_e32 vcc, 0, v22
	s_mov_b32 s5, s9
	s_lshl_b64 s[4:5], s[4:5], 12
	v_cndmask_b32_e32 v20, v20, v21, vcc
	v_mul_f32_e32 v21, 0x37800000, v20
	v_cndmask_b32_e64 v20, v20, v21, s[6:7]
	v_cmp_class_f32_e32 vcc, v19, v179
	s_add_u32 s4, s49, s4
	s_addc_u32 s5, s50, s5
	v_cndmask_b32_e32 v19, v20, v19, vcc
	v_mul_f32_e32 v184, v19, v18
	s_waitcnt vmcnt(4)
	v_or_b32_e32 v161, v34, v169
	v_add_u32_e32 v18, 0, v160
	v_add_u32_e32 v163, 0x18000, v18
	ds_write_b128 v163, v[2:5]
	ds_write_b128 v163, v[6:9] offset:8192
	ds_write_b128 v163, v[10:13] offset:16384
	ds_write_b128 v163, v[14:17] offset:24576
	global_load_dwordx4 v[14:17], v173, s[4:5]
.Lst_op_18:
	s_cbranch_execz .Lst_op_25
	s_add_i32 s4, s8, 0x50
	s_mov_b32 s5, s9
	s_lshl_b64 s[4:5], s[4:5], 12
	s_add_u32 s4, s49, s4
	s_addc_u32 s5, s50, s5
	global_load_dwordx4 v[10:13], v173, s[4:5]
	s_add_i32 s4, s8, 0x60
	s_mov_b32 s5, s9
	s_lshl_b64 s[4:5], s[4:5], 12
	s_add_u32 s4, s49, s4
	s_addc_u32 s5, s50, s5
	s_addk_i32 s8, 0x70
	global_load_dwordx4 v[6:9], v173, s[4:5]
	s_lshl_b64 s[4:5], s[8:9], 12
	s_add_u32 s4, s49, s4
	s_addc_u32 s5, s50, s5
	global_load_dwordx4 v[2:5], v173, s[4:5]
	s_lshl_b64 s[4:5], s[26:27], 7
	s_waitcnt lgkmcnt(0)
	s_barrier
	s_and_b32 s5, s5, 0x7f
	s_and_b32 s4, s4, 0xffffe000
	v_lshl_or_b32 v18, s41, 23, v180
	s_add_u32 s6, s49, s4
.Lst_op_19:
	s_cbranch_execz .Lst_op_26
	v_lshl_or_b32 v164, s48, 20, v18
	v_or_b32_e32 v162, v34, v171
	s_addc_u32 s7, s50, s5
	v_add_u32_e32 v152, v177, v164
	s_mov_b32 s8, 0
	s_mov_b64 s[4:5], 0
	s_mov_b32 s26, 0x8000
	s_mov_b32 s48, 0x10000
	v_mov_b32_e32 v18, 0
	v_mov_b32_e32 v19, v147
	v_mov_b32_e32 v20, v147
	v_mov_b32_e32 v21, v147
	v_mov_b32_e32 v22, 0
	v_mov_b32_e32 v23, v147
	v_mov_b32_e32 v24, v147
	v_mov_b32_e32 v25, v147
	v_mov_b32_e32 v26, 0
	v_mov_b32_e32 v27, v147
	v_mov_b32_e32 v28, v147
	v_mov_b32_e32 v29, v147
	v_mov_b32_e32 v30, 0
	v_mov_b32_e32 v31, v147
	v_mov_b32_e32 v32, v147
	v_mov_b32_e32 v33, v147
	v_mov_b32_e32 v34, 0
	v_mov_b32_e32 v35, v147
	v_mov_b32_e32 v36, v147
	v_mov_b32_e32 v37, v147
	v_mov_b32_e32 v38, 0
.Lst_op_20:
	s_cbranch_execz .Lst_op_27
	v_mov_b32_e32 v39, v147
	v_mov_b32_e32 v40, v147
	v_mov_b32_e32 v41, v147
	v_mov_b32_e32 v42, 0
	v_mov_b32_e32 v43, v147
	v_mov_b32_e32 v44, v147
	v_mov_b32_e32 v45, v147
	v_mov_b32_e32 v46, 0
	v_mov_b32_e32 v47, v147
	v_mov_b32_e32 v48, v147
	v_mov_b32_e32 v49, v147
	v_mov_b32_e32 v50, 0
	v_mov_b32_e32 v51, v147
	v_mov_b32_e32 v52, v147
	v_mov_b32_e32 v53, v147
	v_mov_b32_e32 v54, 0
	v_mov_b32_e32 v55, v147
	v_mov_b32_e32 v56, v147
	v_mov_b32_e32 v57, v147
	v_mov_b32_e32 v61, v147
	v_mov_b32_e32 v118, 0
	v_mov_b32_e32 v119, v147
	v_mov_b32_e32 v120, v147
	v_mov_b32_e32 v121, v147
	v_mov_b32_e32 v122, 0
	v_mov_b32_e32 v123, v147
	v_mov_b32_e32 v124, v147
	v_mov_b32_e32 v125, v147
	v_mov_b32_e32 v126, 0
	v_mov_b32_e32 v127, v147
	v_mov_b32_e32 v128, v147
	v_mov_b32_e32 v129, v147
.Lst_op_21:
	s_cbranch_execz .Lst_op_28
	v_mov_b32_e32 v130, 0
	v_mov_b32_e32 v131, v147
	v_mov_b32_e32 v132, v147
	v_mov_b32_e32 v133, v147
	v_mov_b32_e32 v134, 0
	v_mov_b32_e32 v135, v147
	v_mov_b32_e32 v136, v147
	v_mov_b32_e32 v137, v147
	v_mov_b32_e32 v138, 0
	v_mov_b32_e32 v139, v147
	v_mov_b32_e32 v140, v147
	v_mov_b32_e32 v141, v147
	v_mov_b32_e32 v142, 0
	v_mov_b32_e32 v143, v147
	v_mov_b32_e32 v144, v147
	v_mov_b32_e32 v145, v147

.Lst_op_22:
	s_cbranch_execz .Lst_op_29
	v_or_b32_e32 v152, v181, v1
	v_lshlrev_b32_e32 v185, 2, v152
	ds_bpermute_b32 v152, v185, v165
	ds_bpermute_b32 v154, v185, v165 offset:64
	ds_bpermute_b32 v186, v185, v165 offset:128
	ds_bpermute_b32 v188, v185, v184 offset:192
	ds_bpermute_b32 v190, v185, v165 offset:192
	ds_bpermute_b32 v192, v185, v184
	ds_bpermute_b32 v194, v185, v184 offset:64
	ds_bpermute_b32 v184, v185, v184 offset:128
	s_mov_b32 s8, 0
	s_waitcnt lgkmcnt(4)
	v_pk_mul_f32 v[144:145], v[144:145], v[188:189] op_sel_hi:[1,0]
	v_pk_mul_f32 v[142:143], v[142:143], v[188:189] op_sel_hi:[1,0]
	v_pk_mul_f32 v[140:141], v[140:141], v[188:189] op_sel_hi:[1,0]
	v_pk_mul_f32 v[138:139], v[138:139], v[188:189] op_sel_hi:[1,0]
	v_pk_mul_f32 v[136:137], v[136:137], v[188:189] op_sel_hi:[1,0]
	v_pk_mul_f32 v[134:135], v[134:135], v[188:189] op_sel_hi:[1,0]
.Lst_op_23:
	s_cbranch_execz .Lst_op_30
	v_pk_mul_f32 v[132:133], v[132:133], v[188:189] op_sel_hi:[1,0]
	v_pk_mul_f32 v[130:131], v[130:131], v[188:189] op_sel_hi:[1,0]
	s_waitcnt lgkmcnt(0)
	v_pk_mul_f32 v[128:129], v[128:129], v[184:185] op_sel_hi:[1,0]
	v_pk_mul_f32 v[126:127], v[126:127], v[184:185] op_sel_hi:[1,0]
	v_pk_mul_f32 v[124:125], v[124:125], v[184:185] op_sel_hi:[1,0]
	v_pk_mul_f32 v[122:123], v[122:123], v[184:185] op_sel_hi:[1,0]
	v_pk_mul_f32 v[120:121], v[120:121], v[184:185] op_sel_hi:[1,0]
	v_pk_mul_f32 v[118:119], v[118:119], v[184:185] op_sel_hi:[1,0]
	v_pk_mul_f32 v[116:117], v[116:117], v[184:185] op_sel_hi:[1,0]
	v_pk_mul_f32 v[114:115], v[114:115], v[184:185] op_sel_hi:[1,0]
	v_pk_mul_f32 v[112:113], v[112:113], v[194:195] op_sel_hi:[1,0]
	v_pk_mul_f32 v[110:111], v[110:111], v[194:195] op_sel_hi:[1,0]
	v_pk_mul_f32 v[108:109], v[108:109], v[194:195] op_sel_hi:[1,0]
	v_pk_mul_f32 v[106:107], v[106:107], v[194:195] op_sel_hi:[1,0]
	v_pk_mul_f32 v[104:105], v[104:105], v[194:195] op_sel_hi:[1,0]
	v_pk_mul_f32 v[102:103], v[102:103], v[194:195] op_sel_hi:[1,0]
.Lst_op_24:
	s_cbranch_execz .Lst_op_31
	v_pk_mul_f32 v[100:101], v[100:101], v[194:195] op_sel_hi:[1,0]
	v_pk_mul_f32 v[98:99], v[98:99], v[194:195] op_sel_hi:[1,0]
	v_pk_mul_f32 v[96:97], v[96:97], v[192:193] op_sel_hi:[1,0]
	v_pk_mul_f32 v[94:95], v[94:95], v[192:193] op_sel_hi:[1,0]
	v_pk_mul_f32 v[92:93], v[92:93], v[192:193] op_sel_hi:[1,0]
	v_pk_mul_f32 v[90:91], v[90:91], v[192:193] op_sel_hi:[1,0]
	v_pk_mul_f32 v[88:89], v[88:89], v[192:193] op_sel_hi:[1,0]
	v_pk_mul_f32 v[86:87], v[86:87], v[192:193] op_sel_hi:[1,0]
	v_pk_mul_f32 v[84:85], v[84:85], v[192:193] op_sel_hi:[1,0]
	v_pk_mul_f32 v[82:83], v[82:83], v[192:193] op_sel_hi:[1,0]
	v_pk_mul_f32 v[80:81], v[80:81], v[190:191] op_sel_hi:[1,0]
	v_pk_mul_f32 v[78:79], v[78:79], v[190:191] op_sel_hi:[1,0]
	v_pk_mul_f32 v[76:77], v[76:77], v[190:191] op_sel_hi:[1,0]
	v_pk_mul_f32 v[74:75], v[74:75], v[190:191] op_sel_hi:[1,0]
	v_pk_mul_f32 v[72:73], v[72:73], v[190:191] op_sel_hi:[1,0]
	v_pk_mul_f32 v[70:71], v[70:71], v[190:191] op_sel_hi:[1,0]
.Lst_op_25:
	s_cbranch_execz .Lst_op_32
	v_pk_mul_f32 v[68:69], v[68:69], v[190:191] op_sel_hi:[1,0]
	v_pk_mul_f32 v[66:67], v[66:67], v[190:191] op_sel_hi:[1,0]
	v_pk_mul_f32 v[64:65], v[64:65], v[186:187] op_sel_hi:[1,0]
	v_pk_mul_f32 v[62:63], v[62:63], v[186:187] op_sel_hi:[1,0]
	v_pk_mul_f32 v[60:61], v[60:61], v[186:187] op_sel_hi:[1,0]
	v_pk_mul_f32 v[58:59], v[58:59], v[186:187] op_sel_hi:[1,0]
	v_pk_mul_f32 v[56:57], v[56:57], v[186:187] op_sel_hi:[1,0]
	v_pk_mul_f32 v[54:55], v[54:55], v[186:187] op_sel_hi:[1,0]
	v_pk_mul_f32 v[52:53], v[52:53], v[186:187] op_sel_hi:[1,0]
	v_pk_mul_f32 v[50:51], v[50:51], v[186:187] op_sel_hi:[1,0]
	v_pk_mul_f32 v[48:49], v[48:49], v[154:155] op_sel_hi:[1,0]
	v_pk_mul_f32 v[46:47], v[46:47], v[154:155] op_sel_hi:[1,0]
	v_pk_mul_f32 v[44:45], v[44:45], v[154:155] op_sel_hi:[1,0]
	v_pk_mul_f32 v[42:43], v[42:43], v[154:155] op_sel_hi:[1,0]
	v_pk_mul_f32 v[40:41], v[40:41], v[154:155] op_sel_hi:[1,0]
	v_pk_mul_f32 v[38:39], v[38:39], v[154:155] op_sel_hi:[1,0]
.Lst_op_26:
	s_cbranch_execz .Lst_op_33
	v_pk_mul_f32 v[36:37], v[36:37], v[154:155] op_sel_hi:[1,0]
	v_pk_mul_f32 v[34:35], v[34:35], v[154:155] op_sel_hi:[1,0]
	v_pk_mul_f32 v[32:33], v[32:33], v[152:153] op_sel_hi:[1,0]
	v_pk_mul_f32 v[30:31], v[30:31], v[152:153] op_sel_hi:[1,0]
	v_pk_mul_f32 v[28:29], v[28:29], v[152:153] op_sel_hi:[1,0]
	v_pk_mul_f32 v[26:27], v[26:27], v[152:153] op_sel_hi:[1,0]
	v_pk_mul_f32 v[24:25], v[24:25], v[152:153] op_sel_hi:[1,0]
	v_pk_mul_f32 v[22:23], v[22:23], v[152:153] op_sel_hi:[1,0]
	v_pk_mul_f32 v[20:21], v[20:21], v[152:153] op_sel_hi:[1,0]
	v_pk_mul_f32 v[18:19], v[18:19], v[152:153] op_sel_hi:[1,0]
	v_add_u32_e32 v152, v178, v164
	s_mov_b32 s26, 0x8000
	s_mov_b64 s[4:5], 0
	s_mov_b32 s48, 0x88000

.Lst_op_27:
	s_cbranch_execz .Lst_op_34
	s_add_i32 s4, 0, 0x18000
	v_add_u32_e32 v152, s4, v157
	v_add_u32_e32 v220, 0, v161
	v_add_u32_e32 v161, s4, v155
	v_add_u32_e32 v221, s4, v153
	ds_read_b64_tr_b16 v[184:185], v152
	ds_read_b64_tr_b16 v[186:187], v152 offset:2048
	v_add_u32_e32 v154, s4, v156
	ds_read_b128 v[188:191], v220
	ds_read_b64_tr_b16 v[192:193], v154
	ds_read_b64_tr_b16 v[194:195], v154 offset:2048
	ds_read_b128 v[196:199], v220 offset:2048
	ds_read_b64_tr_b16 v[200:201], v161
	ds_read_b64_tr_b16 v[202:203], v161 offset:2048
	ds_read_b64_tr_b16 v[204:205], v221
	ds_read_b64_tr_b16 v[206:207], v221 offset:2048
	ds_read_b128 v[208:211], v220 offset:4096
	s_waitcnt lgkmcnt(8)
	v_mfma_f32_16x16x32_bf16 v[18:21], v[184:187], v[188:191], v[18:21]
.Lst_op_28:
	s_cbranch_execz .Lst_op_35
	s_waitcnt lgkmcnt(6)
	v_mfma_f32_16x16x32_bf16 v[22:25], v[192:195], v[188:191], v[22:25]
	s_waitcnt lgkmcnt(3)
	v_mfma_f32_16x16x32_bf16 v[26:29], v[200:203], v[188:191], v[26:29]
	s_waitcnt lgkmcnt(1)
	v_mfma_f32_16x16x32_bf16 v[30:33], v[204:207], v[188:191], v[30:33]
	ds_read_b128 v[188:191], v220 offset:6144
	v_mfma_f32_16x16x32_bf16 v[34:37], v[184:187], v[196:199], v[34:37]
	v_mfma_f32_16x16x32_bf16 v[38:41], v[192:195], v[196:199], v[38:41]
	v_mfma_f32_16x16x32_bf16 v[42:45], v[200:203], v[196:199], v[42:45]
	v_mfma_f32_16x16x32_bf16 v[46:49], v[204:207], v[196:199], v[46:49]
	ds_read_b128 v[196:199], v220 offset:8192
	s_waitcnt lgkmcnt(2)
	v_mfma_f32_16x16x32_bf16 v[50:53], v[184:187], v[208:211], v[50:53]
	v_mfma_f32_16x16x32_bf16 v[54:57], v[192:195], v[208:211], v[54:57]
	v_mfma_f32_16x16x32_bf16 v[58:61], v[200:203], v[208:211], v[58:61]
	v_mfma_f32_16x16x32_bf16 v[62:65], v[204:207], v[208:211], v[62:65]
	ds_read_b128 v[208:211], v220 offset:10240
.Lst_op_29:
	s_cbranch_execz .Lst_op_36
	s_waitcnt lgkmcnt(2)
	v_mfma_f32_16x16x32_bf16 v[66:69], v[184:187], v[188:191], v[66:69]
	v_mfma_f32_16x16x32_bf16 v[70:73], v[192:195], v[188:191], v[70:73]
	v_mfma_f32_16x16x32_bf16 v[74:77], v[200:203], v[188:191], v[74:77]
	v_mfma_f32_16x16x32_bf16 v[78:81], v[204:207], v[188:191], v[78:81]
	ds_read_b128 v[188:191], v220 offset:12288
	ds_read_b64_tr_b16 v[212:213], v152 offset:16384
	ds_read_b64_tr_b16 v[214:215], v152 offset:18432
	s_waitcnt lgkmcnt(4)
	v_mfma_f32_16x16x32_bf16 v[82:85], v[184:187], v[196:199], v[82:85]
	v_mfma_f32_16x16x32_bf16 v[86:89], v[192:195], v[196:199], v[86:89]
	v_mfma_f32_16x16x32_bf16 v[90:93], v[200:203], v[196:199], v[90:93]
	v_mfma_f32_16x16x32_bf16 v[94:97], v[204:207], v[196:199], v[94:97]
	ds_read_b128 v[196:199], v220 offset:14336
	ds_read_b64_tr_b16 v[216:217], v154 offset:16384
	ds_read_b64_tr_b16 v[218:219], v154 offset:18432
	s_waitcnt lgkmcnt(6)
	v_mfma_f32_16x16x32_bf16 v[98:101], v[184:187], v[208:211], v[98:101]
.Lst_op_30:
	s_cbranch_execz .Lst_op_37
	v_mfma_f32_16x16x32_bf16 v[102:105], v[192:195], v[208:211], v[102:105]
	v_mfma_f32_16x16x32_bf16 v[106:109], v[200:203], v[208:211], v[106:109]
	v_mfma_f32_16x16x32_bf16 v[110:113], v[204:207], v[208:211], v[110:113]
	v_add_u32_e32 v236, 0, v162
	ds_read_b128 v[162:165], v236
	ds_read_b64_tr_b16 v[208:209], v161 offset:16384
	ds_read_b64_tr_b16 v[210:211], v161 offset:18432
	s_waitcnt lgkmcnt(8)
	v_mfma_f32_16x16x32_bf16 v[114:117], v[184:187], v[188:191], v[114:117]
	v_mfma_f32_16x16x32_bf16 v[118:121], v[192:195], v[188:191], v[118:121]
	v_mfma_f32_16x16x32_bf16 v[122:125], v[200:203], v[188:191], v[122:125]
	v_mfma_f32_16x16x32_bf16 v[126:129], v[204:207], v[188:191], v[126:129]
	s_waitcnt lgkmcnt(5)
	v_mfma_f32_16x16x32_bf16 v[130:133], v[184:187], v[196:199], v[130:133]
	ds_read_b128 v[184:187], v236 offset:2048
	ds_read_b64_tr_b16 v[188:189], v221 offset:16384
	ds_read_b64_tr_b16 v[190:191], v221 offset:18432
	v_mfma_f32_16x16x32_bf16 v[134:137], v[192:195], v[196:199], v[134:137]
.Lst_op_31:
	s_cbranch_execz .Lst_op_38
	v_mfma_f32_16x16x32_bf16 v[138:141], v[200:203], v[196:199], v[138:141]
	v_mfma_f32_16x16x32_bf16 v[142:145], v[204:207], v[196:199], v[142:145]
	ds_read_b128 v[192:195], v236 offset:4096
	s_waitcnt vmcnt(3)
	v_add_u32_e32 v152, s34, v160
	s_waitcnt lgkmcnt(6)
	v_mfma_f32_16x16x32_bf16 v[18:21], v[212:215], v[162:165], v[18:21]
	ds_write_b128 v152, v[14:17]
	v_mfma_f32_16x16x32_bf16 v[22:25], v[216:219], v[162:165], v[22:25]
	s_waitcnt lgkmcnt(5)
	v_mfma_f32_16x16x32_bf16 v[26:29], v[208:211], v[162:165], v[26:29]
	s_waitcnt lgkmcnt(2)
	v_mfma_f32_16x16x32_bf16 v[14:17], v[188:191], v[162:165], v[30:33]
	v_mfma_f32_16x16x32_bf16 v[30:33], v[212:215], v[184:187], v[34:37]
	v_mfma_f32_16x16x32_bf16 v[34:37], v[216:219], v[184:187], v[38:41]
	v_mfma_f32_16x16x32_bf16 v[38:41], v[208:211], v[184:187], v[42:45]
	s_nop 2
	ds_read_b128 v[42:45], v236 offset:6144
	s_waitcnt vmcnt(2)
	ds_write_b128 v152, v[10:13] offset:8192
.Lst_op_32:
	s_cbranch_execz .Lst_op_39
	v_mfma_f32_16x16x32_bf16 v[10:13], v[188:191], v[184:187], v[46:49]
	s_waitcnt lgkmcnt(3)
	v_mfma_f32_16x16x32_bf16 v[46:49], v[212:215], v[192:195], v[50:53]
	v_mfma_f32_16x16x32_bf16 v[50:53], v[216:219], v[192:195], v[54:57]
	v_mfma_f32_16x16x32_bf16 v[54:57], v[208:211], v[192:195], v[58:61]
	s_nop 2
	ds_read_b128 v[58:61], v236 offset:8192
	s_waitcnt vmcnt(1)
	ds_write_b128 v152, v[6:9] offset:16384
	v_mfma_f32_16x16x32_bf16 v[6:9], v[188:191], v[192:195], v[62:65]
	s_waitcnt lgkmcnt(3)
	v_mfma_f32_16x16x32_bf16 v[62:65], v[212:215], v[42:45], v[66:69]
	v_mfma_f32_16x16x32_bf16 v[66:69], v[216:219], v[42:45], v[70:73]
	v_mfma_f32_16x16x32_bf16 v[70:73], v[208:211], v[42:45], v[74:77]
	s_nop 2
	ds_read_b128 v[74:77], v236 offset:10240
	s_waitcnt vmcnt(0)
	ds_write_b128 v152, v[2:5] offset:24576
	v_mfma_f32_16x16x32_bf16 v[2:5], v[188:191], v[42:45], v[78:81]
.Lst_op_33:
	s_cbranch_execz .Lst_op_40
	s_waitcnt lgkmcnt(3)
	v_mfma_f32_16x16x32_bf16 v[78:81], v[216:219], v[58:61], v[86:89]
	s_nop 2
	ds_read_b128 v[86:89], v236 offset:12288
	v_mfma_f32_16x16x32_bf16 v[42:45], v[212:215], v[58:61], v[82:85]
	v_mfma_f32_16x16x32_bf16 v[82:85], v[208:211], v[58:61], v[90:93]
	v_mfma_f32_16x16x32_bf16 v[58:61], v[188:191], v[58:61], v[94:97]
	s_waitcnt lgkmcnt(2)
	v_mfma_f32_16x16x32_bf16 v[94:97], v[216:219], v[74:77], v[102:105]
	s_nop 2
	ds_read_b128 v[102:105], v236 offset:14336
	v_mfma_f32_16x16x32_bf16 v[90:93], v[212:215], v[74:77], v[98:101]
	v_mfma_f32_16x16x32_bf16 v[98:101], v[208:211], v[74:77], v[106:109]
	v_mfma_f32_16x16x32_bf16 v[74:77], v[188:191], v[74:77], v[110:113]
	s_waitcnt lgkmcnt(1)
	v_mfma_f32_16x16x32_bf16 v[106:109], v[212:215], v[86:89], v[114:117]
	v_mfma_f32_16x16x32_bf16 v[110:113], v[216:219], v[86:89], v[118:121]
	v_mfma_f32_16x16x32_bf16 v[114:117], v[208:211], v[86:89], v[122:125]
	v_mfma_f32_16x16x32_bf16 v[86:89], v[188:191], v[86:89], v[126:129]
.Lst_op_34:
	s_cbranch_execz .Lst_op_41
	s_waitcnt lgkmcnt(0)
	v_mfma_f32_16x16x32_bf16 v[118:121], v[212:215], v[102:105], v[130:133]
	v_mfma_f32_16x16x32_bf16 v[122:125], v[216:219], v[102:105], v[134:137]
	v_mfma_f32_16x16x32_bf16 v[126:129], v[208:211], v[102:105], v[138:141]
	v_mfma_f32_16x16x32_bf16 v[102:105], v[188:191], v[102:105], v[142:145]
	s_waitcnt lgkmcnt(0)
	s_barrier
	v_add_u32_e32 v164, s34, v157
	v_add_u32_e32 v165, s34, v156
	v_add_u32_e32 v198, s34, v155
	ds_read_b64_tr_b16 v[130:131], v164
	ds_read_b64_tr_b16 v[132:133], v164 offset:2048
	ds_read_b64_tr_b16 v[134:135], v165
	ds_read_b64_tr_b16 v[136:137], v165 offset:2048
	ds_read_b128 v[138:141], v220 offset:32768
	ds_read_b64_tr_b16 v[142:143], v198
	ds_read_b128 v[154:157], v220 offset:34816
	ds_read_b128 v[160:163], v220 offset:36864
	ds_read_b64_tr_b16 v[144:145], v198 offset:2048
.Lst_op_35:
	s_cbranch_execz .Lst_op_42
	v_add_u32_e32 v200, s34, v153
	ds_read_b64_tr_b16 v[184:185], v200
	ds_read_b64_tr_b16 v[186:187], v200 offset:2048
	s_waitcnt lgkmcnt(6)
	v_mfma_f32_16x16x32_bf16 v[18:21], v[130:133], v[138:141], v[18:21]
	v_mfma_f32_16x16x32_bf16 v[22:25], v[134:137], v[138:141], v[22:25]
	s_waitcnt lgkmcnt(2)
	v_mfma_f32_16x16x32_bf16 v[26:29], v[142:145], v[138:141], v[26:29]
	s_waitcnt lgkmcnt(0)
	v_mfma_f32_16x16x32_bf16 v[14:17], v[184:187], v[138:141], v[14:17]
	ds_read_b128 v[138:141], v220 offset:38912
	v_mfma_f32_16x16x32_bf16 v[30:33], v[130:133], v[154:157], v[30:33]
	v_mfma_f32_16x16x32_bf16 v[34:37], v[134:137], v[154:157], v[34:37]
	v_mfma_f32_16x16x32_bf16 v[38:41], v[142:145], v[154:157], v[38:41]
	v_mfma_f32_16x16x32_bf16 v[10:13], v[184:187], v[154:157], v[10:13]
	ds_read_b128 v[152:155], v220 offset:40960
	v_mfma_f32_16x16x32_bf16 v[46:49], v[130:133], v[160:163], v[46:49]
	v_mfma_f32_16x16x32_bf16 v[50:53], v[134:137], v[160:163], v[50:53]
.Lst_op_36:
	s_cbranch_execz .Lst_op_43
	v_mfma_f32_16x16x32_bf16 v[54:57], v[142:145], v[160:163], v[54:57]
	v_mfma_f32_16x16x32_bf16 v[6:9], v[184:187], v[160:163], v[6:9]
	ds_read_b128 v[160:163], v220 offset:43008
	s_waitcnt lgkmcnt(2)
	v_mfma_f32_16x16x32_bf16 v[62:65], v[130:133], v[138:141], v[62:65]
	v_mfma_f32_16x16x32_bf16 v[66:69], v[134:137], v[138:141], v[66:69]
	v_mfma_f32_16x16x32_bf16 v[70:73], v[142:145], v[138:141], v[70:73]
	v_mfma_f32_16x16x32_bf16 v[2:5], v[184:187], v[138:141], v[2:5]
	s_waitcnt lgkmcnt(1)
	v_mfma_f32_16x16x32_bf16 v[138:141], v[134:137], v[152:155], v[78:81]
	s_nop 2
	ds_read_b128 v[78:81], v220 offset:45056
	ds_read_b64_tr_b16 v[188:189], v164 offset:16384
	ds_read_b64_tr_b16 v[190:191], v164 offset:18432
	v_mfma_f32_16x16x32_bf16 v[42:45], v[130:133], v[152:155], v[42:45]
	v_mfma_f32_16x16x32_bf16 v[82:85], v[142:145], v[152:155], v[82:85]
	v_mfma_f32_16x16x32_bf16 v[152:155], v[184:187], v[152:155], v[58:61]
	s_nop 2
.Lst_op_37:
	s_cbranch_execz .Lst_op_44
	ds_read_b128 v[58:61], v220 offset:47104
	ds_read_b64_tr_b16 v[192:193], v165 offset:16384
	ds_read_b64_tr_b16 v[194:195], v165 offset:18432
	s_waitcnt lgkmcnt(6)
	v_mfma_f32_16x16x32_bf16 v[90:93], v[130:133], v[160:163], v[90:93]
	v_mfma_f32_16x16x32_bf16 v[94:97], v[134:137], v[160:163], v[94:97]
	v_mfma_f32_16x16x32_bf16 v[98:101], v[142:145], v[160:163], v[98:101]
	v_mfma_f32_16x16x32_bf16 v[160:163], v[184:187], v[160:163], v[74:77]
	s_nop 2
	ds_read_b128 v[74:77], v236 offset:32768
	ds_read_b64_tr_b16 v[196:197], v198 offset:16384
	ds_read_b64_tr_b16 v[198:199], v198 offset:18432
	s_waitcnt lgkmcnt(8)
	v_mfma_f32_16x16x32_bf16 v[106:109], v[130:133], v[78:81], v[106:109]
	v_mfma_f32_16x16x32_bf16 v[110:113], v[134:137], v[78:81], v[110:113]
	v_mfma_f32_16x16x32_bf16 v[114:117], v[142:145], v[78:81], v[114:117]
	v_mfma_f32_16x16x32_bf16 v[86:89], v[184:187], v[78:81], v[86:89]
	s_waitcnt lgkmcnt(5)
.Lst_op_38:
	s_cbranch_execz .Lst_op_45
	v_mfma_f32_16x16x32_bf16 v[118:121], v[130:133], v[58:61], v[118:121]
	ds_read_b128 v[78:81], v236 offset:34816
	ds_read_b64_tr_b16 v[130:131], v200 offset:16384
	ds_read_b64_tr_b16 v[132:133], v200 offset:18432
	v_mfma_f32_16x16x32_bf16 v[122:125], v[134:137], v[58:61], v[122:125]
	v_mfma_f32_16x16x32_bf16 v[126:129], v[142:145], v[58:61], v[126:129]
	v_mfma_f32_16x16x32_bf16 v[102:105], v[184:187], v[58:61], v[102:105]
	s_waitcnt lgkmcnt(5)
	v_mfma_f32_16x16x32_bf16 v[134:137], v[188:191], v[74:77], v[18:21]
	s_nop 2
	ds_read_b128 v[18:21], v236 offset:36864
	v_mfma_f32_16x16x32_bf16 v[142:145], v[192:195], v[74:77], v[22:25]
	s_waitcnt lgkmcnt(4)
	v_mfma_f32_16x16x32_bf16 v[184:187], v[196:199], v[74:77], v[26:29]
	s_waitcnt lgkmcnt(1)
	v_mfma_f32_16x16x32_bf16 v[14:17], v[130:133], v[74:77], v[14:17]
	ds_read_b128 v[22:25], v236 offset:38912
	v_mfma_f32_16x16x32_bf16 v[200:203], v[188:191], v[78:81], v[30:33]
.Lst_op_39:
	s_cbranch_execz .Lst_op_46
	v_mfma_f32_16x16x32_bf16 v[204:207], v[192:195], v[78:81], v[34:37]
	v_mfma_f32_16x16x32_bf16 v[208:211], v[196:199], v[78:81], v[38:41]
	v_mfma_f32_16x16x32_bf16 v[10:13], v[130:133], v[78:81], v[10:13]
	ds_read_b128 v[26:29], v236 offset:40960
	s_waitcnt lgkmcnt(2)
	v_mfma_f32_16x16x32_bf16 v[212:215], v[188:191], v[18:21], v[46:49]
	v_mfma_f32_16x16x32_bf16 v[216:219], v[192:195], v[18:21], v[50:53]
	v_mfma_f32_16x16x32_bf16 v[220:223], v[196:199], v[18:21], v[54:57]
	v_mfma_f32_16x16x32_bf16 v[6:9], v[130:133], v[18:21], v[6:9]
	ds_read_b128 v[18:21], v236 offset:43008
	s_waitcnt lgkmcnt(2)
	v_mfma_f32_16x16x32_bf16 v[224:227], v[188:191], v[22:25], v[62:65]
	v_mfma_f32_16x16x32_bf16 v[228:231], v[192:195], v[22:25], v[66:69]
	v_mfma_f32_16x16x32_bf16 v[232:235], v[196:199], v[22:25], v[70:73]
	v_mfma_f32_16x16x32_bf16 v[2:5], v[130:133], v[22:25], v[2:5]
	ds_read_b128 v[22:25], v236 offset:45056
	s_waitcnt lgkmcnt(2)
	v_mfma_f32_16x16x32_bf16 v[78:81], v[188:191], v[26:29], v[42:45]
.Lst_op_40:
	s_cbranch_execz .Lst_op_47
	v_mfma_f32_16x16x32_bf16 v[74:77], v[192:195], v[26:29], v[138:141]
	v_mfma_f32_16x16x32_bf16 v[58:61], v[196:199], v[26:29], v[82:85]
	v_mfma_f32_16x16x32_bf16 v[62:65], v[130:133], v[26:29], v[152:155]
	s_nop 1
	ds_read_b128 v[82:85], v236 offset:47104
	s_waitcnt lgkmcnt(2)
	v_mfma_f32_16x16x32_bf16 v[70:73], v[188:191], v[18:21], v[90:93]
	v_mfma_f32_16x16x32_bf16 v[66:69], v[192:195], v[18:21], v[94:97]
	v_mfma_f32_16x16x32_bf16 v[50:53], v[196:199], v[18:21], v[98:101]
	v_mfma_f32_16x16x32_bf16 v[54:57], v[130:133], v[18:21], v[160:163]
	s_waitcnt lgkmcnt(1)
	v_mfma_f32_16x16x32_bf16 v[46:49], v[188:191], v[22:25], v[106:109]
	v_mfma_f32_16x16x32_bf16 v[42:45], v[192:195], v[22:25], v[110:113]
	v_mfma_f32_16x16x32_bf16 v[38:41], v[196:199], v[22:25], v[114:117]
	v_mfma_f32_16x16x32_bf16 v[30:33], v[130:133], v[22:25], v[86:89]
	s_waitcnt lgkmcnt(0)
	v_mfma_f32_16x16x32_bf16 v[34:37], v[188:191], v[82:85], v[118:121]
	v_mfma_f32_16x16x32_bf16 v[26:29], v[192:195], v[82:85], v[122:125]
.Lst_op_41:
	s_cbranch_execz .Lst_op_48
	v_mfma_f32_16x16x32_bf16 v[22:25], v[196:199], v[82:85], v[126:129]
	v_mfma_f32_16x16x32_bf16 v[18:21], v[130:133], v[82:85], v[102:105]
	v_mov_b32_e32 v236, v1
	v_mov_b32_e32 v237, v166
	s_waitcnt lgkmcnt(0)
	s_barrier
	s_lshl_b32 s4, s42, 6
	v_and_or_b32 v82, v236, 63, v181
	v_lshlrev_b32_e32 v122, 2, v82
	ds_bpermute_b32 v82, v122, v183
	v_xor_b32_e32 v239, 0x80, v122
	s_or_b32 s4, s4, s24
	v_lshlrev_b32_e32 v240, 3, v237
	s_waitcnt lgkmcnt(0)
	v_pk_mul_f32 v[162:163], v[136:137], v[82:83] op_sel_hi:[1,0]
	v_pk_mul_f32 v[164:165], v[134:135], v[82:83] op_sel_hi:[1,0]
	v_pk_mul_f32 v[152:153], v[144:145], v[82:83] op_sel_hi:[1,0]
	v_pk_mul_f32 v[154:155], v[142:143], v[82:83] op_sel_hi:[1,0]
	v_add_u32_e32 v83, 16, v236
	v_and_or_b32 v83, v83, 63, v181
	v_lshlrev_b32_e32 v238, 2, v83
	ds_bpermute_b32 v84, v238, v183
.Lst_op_42:
	s_cbranch_execz .Lst_op_49
	v_pk_mul_f32 v[138:139], v[14:15], v[82:83] op_sel_hi:[1,0]
	ds_bpermute_b32 v14, v239, v183
	v_add_u32_e32 v144, s43, v236
	v_ashrrev_i32_e32 v145, 31, v144
	s_waitcnt lgkmcnt(1)
	v_pk_mul_f32 v[116:117], v[10:11], v[84:85] op_sel_hi:[1,0]
	v_add_u32_e32 v10, 48, v236
	v_and_or_b32 v10, v10, 63, v181
	s_waitcnt lgkmcnt(0)
	v_pk_mul_f32 v[112:113], v[212:213], v[14:15] op_sel_hi:[1,0]
	v_lshlrev_b32_e32 v213, 2, v10
	ds_bpermute_b32 v10, v213, v183
	v_pk_mul_f32 v[98:99], v[8:9], v[14:15] op_sel_hi:[1,0]
	v_lshlrev_b64 v[8:9], 13, v[144:145]
	v_pk_mul_f32 v[118:119], v[208:209], v[84:85] op_sel_hi:[1,0]
	v_pk_mul_f32 v[100:101], v[6:7], v[14:15] op_sel_hi:[1,0]
	s_waitcnt lgkmcnt(0)
	v_pk_mul_f32 v[86:87], v[2:3], v[10:11] op_sel_hi:[1,0]
	v_lshl_add_u32 v2, v237, 2, s4
	s_mul_i32 s4, s41, 0x3000
.Lst_op_43:
	s_cbranch_execz .Lst_op_50
	s_ashr_i32 s5, s4, 31
	s_lshl_b64 s[4:5], s[4:5], 2
	s_add_u32 s4, s70, s4
	s_addc_u32 s5, s71, s5
	s_add_u32 s4, s4, 0xc000
	v_ashrrev_i32_e32 v3, 31, v2
	ds_bpermute_b32 v208, v122, v182
	s_addc_u32 s5, s5, 0
	v_lshlrev_b64 v[122:123], 2, v[2:3]
	v_add_u32_e32 v6, 16, v2
	v_lshl_add_u64 v[8:9], s[12:13], 0, v[8:9]
	v_pk_mul_f32 v[128:129], v[202:203], v[84:85] op_sel_hi:[1,0]
	v_pk_mul_f32 v[130:131], v[200:201], v[84:85] op_sel_hi:[1,0]
	v_pk_mul_f32 v[124:125], v[206:207], v[84:85] op_sel_hi:[1,0]
	v_pk_mul_f32 v[126:127], v[204:205], v[84:85] op_sel_hi:[1,0]
	v_pk_mul_f32 v[120:121], v[210:211], v[84:85] op_sel_hi:[1,0]
	v_pk_mul_f32 v[114:115], v[12:13], v[84:85] op_sel_hi:[1,0]
	v_pk_mul_f32 v[84:85], v[4:5], v[10:11] op_sel_hi:[1,0]
	v_lshl_add_u64 v[4:5], s[4:5], 0, v[122:123]
	v_ashrrev_i32_e32 v7, 31, v6
.Lst_op_44:
	s_cbranch_execz .Lst_op_51
	v_lshl_add_u64 v[132:133], v[8:9], 0, v[122:123]
	v_pk_mul_f32 v[156:157], v[186:187], v[82:83] op_sel_hi:[1,0]
	v_pk_mul_f32 v[160:161], v[184:185], v[82:83] op_sel_hi:[1,0]
	v_pk_mul_f32 v[136:137], v[16:17], v[82:83] op_sel_hi:[1,0]
	v_pk_mul_f32 v[110:111], v[214:215], v[14:15] op_sel_hi:[1,0]
	v_pk_mul_f32 v[106:107], v[218:219], v[14:15] op_sel_hi:[1,0]
	v_pk_mul_f32 v[108:109], v[216:217], v[14:15] op_sel_hi:[1,0]
	v_pk_mul_f32 v[102:103], v[222:223], v[14:15] op_sel_hi:[1,0]
	v_pk_mul_f32 v[104:105], v[220:221], v[14:15] op_sel_hi:[1,0]
	v_pk_mul_f32 v[94:95], v[226:227], v[10:11] op_sel_hi:[1,0]
	v_pk_mul_f32 v[96:97], v[224:225], v[10:11] op_sel_hi:[1,0]
	v_pk_mul_f32 v[90:91], v[230:231], v[10:11] op_sel_hi:[1,0]
	v_pk_mul_f32 v[92:93], v[228:229], v[10:11] op_sel_hi:[1,0]
	v_pk_mul_f32 v[88:89], v[234:235], v[10:11] op_sel_hi:[1,0]
	v_pk_mul_f32 v[82:83], v[232:233], v[10:11] op_sel_hi:[1,0]
	v_lshl_add_u64 v[6:7], v[6:7], 2, s[4:5]
.Lst_op_45:
	s_cbranch_execz .Lst_op_52
	global_load_dwordx4 v[184:187], v[132:133], off nt
	global_load_dwordx4 v[14:17], v[4:5], off
	global_load_dwordx4 v[10:13], v[6:7], off
	v_add_u32_e32 v4, 32, v2
	v_add_u32_e32 v2, 48, v2
	v_ashrrev_i32_e32 v5, 31, v4
	v_ashrrev_i32_e32 v3, 31, v2
	v_lshl_add_u64 v[4:5], v[4:5], 2, s[4:5]
	v_lshl_add_u64 v[2:3], v[2:3], 2, s[4:5]
	global_load_dwordx4 v[188:191], v[132:133], off offset:64 nt
	global_load_dwordx4 v[192:195], v[132:133], off offset:128 nt
	global_load_dwordx4 v[6:9], v[4:5], off
	s_nop 0
	global_load_dwordx4 v[2:5], v[2:3], off
	s_nop 0
	global_load_dwordx4 v[196:199], v[132:133], off offset:192 nt
	v_add_u32_e32 v132, 16, v144
	ds_bpermute_b32 v212, v238, v182
	ds_bpermute_b32 v216, v239, v182
	v_ashrrev_i32_e32 v133, 31, v132
.Lst_op_46:
	s_cbranch_execz .Lst_op_53
	v_lshlrev_b64 v[132:133], 13, v[132:133]
	v_lshl_add_u64 v[132:133], s[12:13], 0, v[132:133]
	v_lshl_add_u64 v[210:211], v[132:133], 0, v[122:123]
	global_load_dwordx4 v[200:203], v[210:211], off nt
	global_load_dwordx4 v[204:207], v[210:211], off offset:64 nt
	s_waitcnt lgkmcnt(2)
	v_pk_mul_f32 v[142:143], v[78:79], v[208:209] op_sel_hi:[1,0]
	v_pk_mul_f32 v[78:79], v[60:61], v[208:209] op_sel_hi:[1,0]
	s_waitcnt lgkmcnt(1)
	v_pk_mul_f32 v[60:61], v[50:51], v[212:213] op_sel_hi:[1,0]
	s_waitcnt lgkmcnt(0)
	v_pk_mul_f32 v[50:51], v[48:49], v[216:217] op_sel_hi:[1,0]
	v_pk_mul_f32 v[48:49], v[42:43], v[216:217] op_sel_hi:[1,0]
	v_add_u32_e32 v42, 32, v144
	ds_bpermute_b32 v182, v213, v182
	v_ashrrev_i32_e32 v43, 31, v42
	v_pk_mul_f32 v[132:133], v[76:77], v[208:209] op_sel_hi:[1,0]
	v_pk_mul_f32 v[134:135], v[74:75], v[208:209] op_sel_hi:[1,0]
	v_pk_mul_f32 v[74:75], v[64:65], v[208:209] op_sel_hi:[1,0]
.Lst_op_47:
	s_cbranch_execz .Lst_op_54
	v_pk_mul_f32 v[76:77], v[62:63], v[208:209] op_sel_hi:[1,0]
	v_pk_mul_f32 v[62:63], v[68:69], v[212:213] op_sel_hi:[1,0]
	v_pk_mul_f32 v[64:65], v[66:67], v[212:213] op_sel_hi:[1,0]
	global_load_dwordx4 v[66:69], v[210:211], off offset:128 nt
	v_lshlrev_b64 v[42:43], 13, v[42:43]
	v_lshl_add_u64 v[42:43], s[12:13], 0, v[42:43]
	v_lshl_add_u64 v[220:221], v[42:43], 0, v[122:123]
	v_pk_mul_f32 v[140:141], v[80:81], v[208:209] op_sel_hi:[1,0]
	v_pk_mul_f32 v[80:81], v[58:59], v[208:209] op_sel_hi:[1,0]
	v_pk_mul_f32 v[72:73], v[72:73], v[212:213] op_sel_hi:[1,0]
	v_pk_mul_f32 v[70:71], v[70:71], v[212:213] op_sel_hi:[1,0]
	v_pk_mul_f32 v[58:59], v[52:53], v[212:213] op_sel_hi:[1,0]
	v_pk_mul_f32 v[56:57], v[56:57], v[212:213] op_sel_hi:[1,0]
	v_pk_mul_f32 v[54:55], v[54:55], v[212:213] op_sel_hi:[1,0]
	global_load_dwordx4 v[212:215], v[220:221], off nt
	v_pk_mul_f32 v[52:53], v[46:47], v[216:217] op_sel_hi:[1,0]
.Lst_op_48:
	s_cbranch_execz .Lst_op_55
	global_load_dwordx4 v[208:211], v[210:211], off offset:192 nt
	v_pk_mul_f32 v[46:47], v[44:45], v[216:217] op_sel_hi:[1,0]
	v_pk_mul_f32 v[42:43], v[32:33], v[216:217] op_sel_hi:[1,0]
	v_pk_mul_f32 v[44:45], v[30:31], v[216:217] op_sel_hi:[1,0]
	s_waitcnt lgkmcnt(0)
	v_pk_mul_f32 v[30:31], v[36:37], v[182:183] op_sel_hi:[1,0]
	v_pk_mul_f32 v[32:33], v[34:35], v[182:183] op_sel_hi:[1,0]
	global_load_dwordx4 v[34:37], v[220:221], off offset:64 nt
	v_pk_mul_f32 v[40:41], v[40:41], v[216:217] op_sel_hi:[1,0]
	v_pk_mul_f32 v[38:39], v[38:39], v[216:217] op_sel_hi:[1,0]
	global_load_dwordx4 v[216:219], v[220:221], off offset:128 nt
	s_nop 0
	global_load_dwordx4 v[220:223], v[220:221], off offset:192 nt
	v_pk_mul_f32 v[28:29], v[28:29], v[182:183] op_sel_hi:[1,0]
	v_pk_mul_f32 v[26:27], v[26:27], v[182:183] op_sel_hi:[1,0]
	v_pk_mul_f32 v[24:25], v[24:25], v[182:183] op_sel_hi:[1,0]
	v_pk_mul_f32 v[22:23], v[22:23], v[182:183] op_sel_hi:[1,0]
.Lst_op_49:
	s_cbranch_execz .Lst_op_56
	v_pk_mul_f32 v[20:21], v[20:21], v[182:183] op_sel_hi:[1,0]
	v_pk_mul_f32 v[18:19], v[18:19], v[182:183] op_sel_hi:[1,0]
	v_add_u32_e32 v182, 48, v144
	v_ashrrev_i32_e32 v183, 31, v182
	v_lshlrev_b64 v[182:183], 13, v[182:183]
	v_lshl_add_u64 v[182:183], s[12:13], 0, v[182:183]
	v_lshl_add_u64 v[182:183], v[182:183], 0, v[122:123]
	v_add_u32_e32 v145, s39, v236
	global_load_dwordx4 v[224:227], v[182:183], off nt
	global_load_dwordx4 v[228:231], v[182:183], off offset:64 nt
	global_load_dwordx4 v[232:235], v[182:183], off offset:128 nt
	global_load_dwordx4 v[236:239], v[182:183], off offset:192 nt
	s_add_i32 s40, s40, 0
	v_mul_lo_u32 v145, v145, s35
	v_add3_u32 v240, s40, v240, v145
	v_add_u32_e32 v145, 0x2000, v240
	s_andn2_b64 vcc, exec, s[76:77]
	s_waitcnt vmcnt(18)
	v_pk_fma_f32 v[162:163], v[162:163], v[16:17], v[186:187]
.Lst_op_50:
	s_cbranch_execz .Lst_op_57
	v_pk_fma_f32 v[164:165], v[164:165], v[14:15], v[184:185]
	s_waitcnt vmcnt(16)
	v_pk_fma_f32 v[152:153], v[152:153], v[12:13], v[190:191]
	v_pk_fma_f32 v[154:155], v[154:155], v[10:11], v[188:189]
	v_cvt_pk_bf16_f32 v164, v164, v165
	v_cvt_pk_bf16_f32 v165, v162, v163
	v_cvt_pk_bf16_f32 v154, v154, v155
	v_cvt_pk_bf16_f32 v155, v152, v153
	ds_write2_b64 v240, v[164:165], v[154:155] offset1:4
	s_waitcnt vmcnt(14)
	v_pk_fma_f32 v[152:153], v[156:157], v[8:9], v[194:195]
	v_pk_fma_f32 v[154:155], v[160:161], v[6:7], v[192:193]
	s_waitcnt vmcnt(12)
	v_pk_fma_f32 v[136:137], v[136:137], v[4:5], v[198:199]
	v_pk_fma_f32 v[138:139], v[138:139], v[2:3], v[196:197]
	s_waitcnt vmcnt(11)
	v_pk_fma_f32 v[128:129], v[128:129], v[16:17], v[202:203]
	v_pk_fma_f32 v[130:131], v[130:131], v[14:15], v[200:201]
.Lst_op_51:
	s_cbranch_execz .Lst_op_58
	s_waitcnt vmcnt(10)
	v_pk_fma_f32 v[124:125], v[124:125], v[12:13], v[206:207]
	v_cvt_pk_bf16_f32 v130, v130, v131
	v_cvt_pk_bf16_f32 v131, v128, v129
	v_cvt_pk_bf16_f32 v129, v124, v125
	v_add_u32_e32 v124, 64, v144
	v_ashrrev_i32_e32 v125, 31, v124
	v_lshlrev_b64 v[124:125], 13, v[124:125]
	v_pk_fma_f32 v[126:127], v[126:127], v[10:11], v[204:205]
	v_lshl_add_u64 v[124:125], s[12:13], 0, v[124:125]
	v_cvt_pk_bf16_f32 v154, v154, v155
	v_cvt_pk_bf16_f32 v155, v152, v153
	v_cvt_pk_bf16_f32 v138, v138, v139
	v_cvt_pk_bf16_f32 v139, v136, v137
	v_cvt_pk_bf16_f32 v128, v126, v127
	s_waitcnt vmcnt(9)
	v_pk_fma_f32 v[66:67], v[118:119], v[6:7], v[66:67]
	v_add_u32_e32 v118, 0x50, v144
.Lst_op_52:
	s_cbranch_execz .Lst_op_59
	v_ashrrev_i32_e32 v119, 31, v118
	v_lshlrev_b64 v[118:119], 13, v[118:119]
	v_lshl_add_u64 v[136:137], v[124:125], 0, v[122:123]
	v_pk_fma_f32 v[68:69], v[120:121], v[8:9], v[68:69]
	v_lshl_add_u64 v[118:119], s[12:13], 0, v[118:119]
	ds_write2_b64 v240, v[154:155], v[138:139] offset0:8 offset1:12
	global_load_dwordx4 v[124:127], v[136:137], off nt
	ds_write2_b64 v145, v[130:131], v[128:129] offset0:32 offset1:36
	global_load_dwordx4 v[128:131], v[136:137], off offset:64 nt
	v_cvt_pk_bf16_f32 v138, v66, v67
	v_cvt_pk_bf16_f32 v139, v68, v69
	s_waitcnt vmcnt(9)
	v_pk_fma_f32 v[114:115], v[114:115], v[4:5], v[210:211]
	v_pk_fma_f32 v[116:117], v[116:117], v[2:3], v[208:209]
	global_load_dwordx4 v[66:69], v[136:137], off offset:128 nt
	v_cvt_pk_bf16_f32 v152, v116, v117
	v_cvt_pk_bf16_f32 v153, v114, v115
.Lst_op_53:
	s_cbranch_execz .Lst_op_60
	global_load_dwordx4 v[114:117], v[136:137], off offset:192 nt
	v_lshl_add_u64 v[136:137], v[118:119], 0, v[122:123]
	s_waitcnt vmcnt(10)
	v_pk_fma_f32 v[106:107], v[106:107], v[12:13], v[36:37]
	v_pk_fma_f32 v[34:35], v[108:109], v[10:11], v[34:35]
	global_load_dwordx4 v[118:121], v[136:137], off nt
	ds_write2_b64 v145, v[138:139], v[152:153] offset0:40 offset1:44
	v_pk_fma_f32 v[138:139], v[110:111], v[16:17], v[214:215]
	v_pk_fma_f32 v[152:153], v[112:113], v[14:15], v[212:213]
	global_load_dwordx4 v[110:113], v[136:137], off offset:64 nt
	v_cvt_pk_bf16_f32 v154, v34, v35
	global_load_dwordx4 v[34:37], v[136:137], off offset:128 nt
	v_cvt_pk_bf16_f32 v155, v106, v107
	global_load_dwordx4 v[106:109], v[136:137], off offset:192 nt
	v_add_u32_e32 v136, 0x60, v144
	v_cvt_pk_bf16_f32 v152, v152, v153
	v_cvt_pk_bf16_f32 v153, v138, v139
.Lst_op_54:
	s_cbranch_execz .Lst_op_61
	v_add_u32_e32 v145, 0x4000, v240
	v_ashrrev_i32_e32 v137, 31, v136
	v_lshlrev_b64 v[136:137], 13, v[136:137]
	ds_write2_b64 v145, v[152:153], v[154:155] offset0:64 offset1:68
	s_waitcnt vmcnt(13)
	v_pk_fma_f32 v[152:153], v[102:103], v[8:9], v[218:219]
	v_pk_fma_f32 v[154:155], v[104:105], v[6:7], v[216:217]
	v_lshl_add_u64 v[136:137], s[12:13], 0, v[136:137]
	v_cvt_pk_bf16_f32 v154, v154, v155
	v_cvt_pk_bf16_f32 v155, v152, v153
	s_waitcnt vmcnt(12)
	v_pk_fma_f32 v[152:153], v[98:99], v[4:5], v[222:223]
	v_pk_fma_f32 v[98:99], v[100:101], v[2:3], v[220:221]
	v_lshl_add_u64 v[156:157], v[136:137], 0, v[122:123]
	v_cvt_pk_bf16_f32 v160, v98, v99
	v_cvt_pk_bf16_f32 v161, v152, v153
	v_add_u32_e32 v144, 0x70, v144
	global_load_dwordx4 v[136:139], v[156:157], off nt
.Lst_op_55:
	s_cbranch_execz .Lst_op_62
	global_load_dwordx4 v[102:105], v[156:157], off offset:64 nt
	ds_write2_b64 v145, v[154:155], v[160:161] offset0:72 offset1:76
	v_ashrrev_i32_e32 v145, 31, v144
	v_lshlrev_b64 v[144:145], 13, v[144:145]
	v_lshl_add_u64 v[144:145], s[12:13], 0, v[144:145]
	global_load_dwordx4 v[98:101], v[156:157], off offset:128 nt
	global_load_dwordx4 v[152:155], v[156:157], off offset:192 nt
	v_lshl_add_u64 v[122:123], v[144:145], 0, v[122:123]
	s_waitcnt vmcnt(15)
	v_pk_fma_f32 v[144:145], v[94:95], v[16:17], v[226:227]
	v_pk_fma_f32 v[94:95], v[96:97], v[14:15], v[224:225]
	s_waitcnt vmcnt(14)
	v_pk_fma_f32 v[90:91], v[90:91], v[12:13], v[230:231]
	v_pk_fma_f32 v[92:93], v[92:93], v[10:11], v[228:229]
	global_load_dwordx4 v[160:163], v[122:123], off nt
	v_cvt_pk_bf16_f32 v156, v94, v95
	global_load_dwordx4 v[94:97], v[122:123], off offset:64 nt
	v_cvt_pk_bf16_f32 v157, v144, v145
.Lst_op_56:
	s_cbranch_execz .Lst_op_63
	v_cvt_pk_bf16_f32 v144, v92, v93
	v_cvt_pk_bf16_f32 v145, v90, v91
	global_load_dwordx4 v[90:93], v[122:123], off offset:128 nt
	global_load_dwordx4 v[182:185], v[122:123], off offset:192 nt
	s_waitcnt vmcnt(17)
	v_pk_fma_f32 v[88:89], v[88:89], v[8:9], v[234:235]
	v_pk_fma_f32 v[82:83], v[82:83], v[6:7], v[232:233]
	s_waitcnt vmcnt(16)
	v_pk_fma_f32 v[84:85], v[84:85], v[4:5], v[238:239]
	v_pk_fma_f32 v[86:87], v[86:87], v[2:3], v[236:237]
	v_add_u32_e32 v164, 0x6000, v240
	v_cvt_pk_bf16_f32 v82, v82, v83
	v_cvt_pk_bf16_f32 v83, v88, v89
	v_cvt_pk_bf16_f32 v86, v86, v87
	v_cvt_pk_bf16_f32 v87, v84, v85
	ds_write2_b64 v164, v[82:83], v[86:87] offset0:104 offset1:108
	ds_write2_b64 v164, v[156:157], v[144:145] offset0:96 offset1:100
.Lst_op_57:
	s_cbranch_execz .Lst_op_64
	s_waitcnt vmcnt(15)
	v_pk_fma_f32 v[82:83], v[140:141], v[16:17], v[126:127]
	v_pk_fma_f32 v[84:85], v[142:143], v[14:15], v[124:125]
	s_waitcnt vmcnt(14)
	v_pk_fma_f32 v[86:87], v[134:135], v[10:11], v[128:129]
	v_cvt_pk_bf16_f32 v84, v84, v85
	v_cvt_pk_bf16_f32 v85, v82, v83
	v_pk_fma_f32 v[82:83], v[132:133], v[12:13], v[130:131]
	v_cvt_pk_bf16_f32 v86, v86, v87
	s_waitcnt vmcnt(13)
	v_pk_fma_f32 v[68:69], v[78:79], v[8:9], v[68:69]
	v_pk_fma_f32 v[66:67], v[80:81], v[6:7], v[66:67]
	v_cvt_pk_bf16_f32 v87, v82, v83
	v_cvt_pk_bf16_f32 v66, v66, v67
	v_cvt_pk_bf16_f32 v67, v68, v69
	s_waitcnt vmcnt(12)
	v_pk_fma_f32 v[68:69], v[74:75], v[4:5], v[116:117]
	v_pk_fma_f32 v[74:75], v[76:77], v[2:3], v[114:115]
.Lst_op_58:
	s_cbranch_execz .Lst_op_65
	v_add_u32_e32 v82, 0x8000, v240
	v_cvt_pk_bf16_f32 v74, v74, v75
	v_cvt_pk_bf16_f32 v75, v68, v69
	ds_write2_b64 v82, v[66:67], v[74:75] offset0:136 offset1:140
	s_waitcnt vmcnt(10)
	v_pk_fma_f32 v[62:63], v[62:63], v[12:13], v[112:113]
	v_pk_fma_f32 v[64:65], v[64:65], v[10:11], v[110:111]
	s_waitcnt vmcnt(9)
	v_pk_fma_f32 v[36:37], v[58:59], v[8:9], v[36:37]
	v_pk_fma_f32 v[34:35], v[60:61], v[6:7], v[34:35]
	s_waitcnt vmcnt(8)
	v_pk_fma_f32 v[54:55], v[54:55], v[2:3], v[106:107]
	v_cvt_pk_bf16_f32 v34, v34, v35
	v_cvt_pk_bf16_f32 v35, v36, v37
	v_pk_fma_f32 v[36:37], v[56:57], v[4:5], v[108:109]
	v_cvt_pk_bf16_f32 v64, v64, v65
	v_cvt_pk_bf16_f32 v65, v62, v63
	v_add_u32_e32 v62, 0xa000, v240
.Lst_op_59:
	s_cbranch_execz .Lst_op_66
	v_cvt_pk_bf16_f32 v54, v54, v55
	v_cvt_pk_bf16_f32 v55, v36, v37
	ds_write2_b64 v62, v[34:35], v[54:55] offset0:168 offset1:172
	v_pk_fma_f32 v[66:67], v[16:17], v[72:73], v[120:121]
	v_pk_fma_f32 v[68:69], v[14:15], v[70:71], v[118:119]
	ds_write2_b64 v82, v[84:85], v[86:87] offset0:128 offset1:132
	v_cvt_pk_bf16_f32 v68, v68, v69
	v_cvt_pk_bf16_f32 v69, v66, v67
	ds_write2_b64 v62, v[68:69], v[64:65] offset0:160 offset1:164
	s_waitcnt vmcnt(7)
	v_pk_fma_f32 v[34:35], v[16:17], v[50:51], v[138:139]
	v_pk_fma_f32 v[36:37], v[14:15], v[52:53], v[136:137]
	s_waitcnt vmcnt(3)
	v_pk_fma_f32 v[16:17], v[16:17], v[30:31], v[162:163]
	v_cvt_pk_bf16_f32 v36, v36, v37
	v_cvt_pk_bf16_f32 v37, v34, v35
	v_pk_fma_f32 v[34:35], v[12:13], v[46:47], v[104:105]
.Lst_op_60:
	s_cbranch_execz .Lst_op_67
	v_pk_fma_f32 v[46:47], v[10:11], v[48:49], v[102:103]
	v_add_u32_e32 v48, 0xc000, v240
	v_cvt_pk_bf16_f32 v46, v46, v47
	v_cvt_pk_bf16_f32 v47, v34, v35
	ds_write2_b64 v48, v[36:37], v[46:47] offset0:192 offset1:196
	v_pk_fma_f32 v[34:35], v[40:41], v[8:9], v[100:101]
	v_pk_fma_f32 v[36:37], v[38:39], v[6:7], v[98:99]
	v_pk_fma_f32 v[38:39], v[44:45], v[2:3], v[152:153]
	v_cvt_pk_bf16_f32 v36, v36, v37
	v_cvt_pk_bf16_f32 v37, v34, v35
	v_pk_fma_f32 v[34:35], v[42:43], v[4:5], v[154:155]
	s_waitcnt vmcnt(2)
	v_pk_fma_f32 v[12:13], v[12:13], v[28:29], v[96:97]
	v_pk_fma_f32 v[10:11], v[10:11], v[26:27], v[94:95]
	s_waitcnt vmcnt(1)
	v_pk_fma_f32 v[8:9], v[8:9], v[24:25], v[92:93]
	v_pk_fma_f32 v[6:7], v[6:7], v[22:23], v[90:91]
.Lst_op_61:
	s_cbranch_execz .Lst_op_68
	s_waitcnt vmcnt(0)
	v_pk_fma_f32 v[4:5], v[20:21], v[4:5], v[184:185]
	v_pk_fma_f32 v[2:3], v[18:19], v[2:3], v[182:183]
	v_cvt_pk_bf16_f32 v10, v10, v11
	v_cvt_pk_bf16_f32 v11, v12, v13
	v_add_u32_e32 v12, 0xe000, v240
	v_cvt_pk_bf16_f32 v6, v6, v7
	v_cvt_pk_bf16_f32 v7, v8, v9
	v_cvt_pk_bf16_f32 v2, v2, v3
	v_cvt_pk_bf16_f32 v3, v4, v5
	v_lshl_or_b32 v8, s38, 5, v167
	v_pk_fma_f32 v[14:15], v[14:15], v[32:33], v[160:161]
	ds_write2_b64 v12, v[6:7], v[2:3] offset0:232 offset1:236
	v_mad_u64_u32 v[6:7], s[4:5], v8, s35, v[148:149]
	v_add_u32_e32 v8, s25, v8
	v_cvt_pk_bf16_f32 v14, v14, v15
	v_cvt_pk_bf16_f32 v15, v16, v17
.Lst_op_62:
	s_cbranch_execz .Lst_op_69
	v_ashrrev_i32_e32 v9, 31, v8
	ds_write2_b64 v12, v[14:15], v[10:11] offset0:224 offset1:228
	v_lshlrev_b64 v[10:11], 12, v[8:9]
	v_cvt_pk_bf16_f32 v38, v38, v39
	v_cvt_pk_bf16_f32 v39, v34, v35
	v_lshl_add_u64 v[10:11], s[18:19], 0, v[10:11]
	ds_write2_b64 v48, v[36:37], v[38:39] offset0:200 offset1:204
	v_lshl_add_u64 v[10:11], v[10:11], 0, s[22:23]
	s_waitcnt lgkmcnt(0)
	s_barrier
	v_lshl_add_u64 v[10:11], v[10:11], 0, v[146:147]
	ds_read_b128 v[2:5], v6
	s_waitcnt lgkmcnt(0)
	global_store_dwordx4 v[10:11], v[2:5], off sc1
	s_nop 1
	v_add_u32_e32 v10, 2, v8
	v_ashrrev_i32_e32 v11, 31, v10
	v_lshlrev_b64 v[10:11], 12, v[10:11]
	v_lshl_add_u64 v[10:11], s[18:19], 0, v[10:11]
	v_lshl_add_u64 v[10:11], v[10:11], 0, s[22:23]
.Lst_op_63:
	s_cbranch_execz .Lst_op_70
	v_lshl_add_u64 v[10:11], v[10:11], 0, v[146:147]
	ds_read_b128 v[2:5], v6 offset:1056
	s_waitcnt lgkmcnt(0)
	global_store_dwordx4 v[10:11], v[2:5], off sc1
	s_nop 1
	v_add_u32_e32 v10, 4, v8
	v_ashrrev_i32_e32 v11, 31, v10
	v_lshlrev_b64 v[10:11], 12, v[10:11]
	v_lshl_add_u64 v[10:11], s[18:19], 0, v[10:11]
	v_lshl_add_u64 v[10:11], v[10:11], 0, s[22:23]
	v_lshl_add_u64 v[10:11], v[10:11], 0, v[146:147]
	ds_read_b128 v[2:5], v6 offset:2112
	s_waitcnt lgkmcnt(0)
	global_store_dwordx4 v[10:11], v[2:5], off sc1
	s_nop 1
	v_add_u32_e32 v10, 6, v8
	v_ashrrev_i32_e32 v11, 31, v10
	v_lshlrev_b64 v[10:11], 12, v[10:11]
	v_lshl_add_u64 v[10:11], s[18:19], 0, v[10:11]
	v_lshl_add_u64 v[10:11], v[10:11], 0, s[22:23]
.Lst_op_64:
	s_cbranch_execz .Lsc_join_op
	v_lshl_add_u64 v[10:11], v[10:11], 0, v[146:147]
	ds_read_b128 v[2:5], v6 offset:3168
	s_waitcnt lgkmcnt(0)
	global_store_dwordx4 v[10:11], v[2:5], off sc1
	s_nop 1
	v_add_u32_e32 v10, 8, v8
	v_ashrrev_i32_e32 v11, 31, v10
	v_lshlrev_b64 v[10:11], 12, v[10:11]
	v_lshl_add_u64 v[10:11], s[18:19], 0, v[10:11]
	v_lshl_add_u64 v[10:11], v[10:11], 0, s[22:23]
	v_lshl_add_u64 v[10:11], v[10:11], 0, v[146:147]
	ds_read_b128 v[2:5], v6 offset:4224
	s_waitcnt lgkmcnt(0)
	global_store_dwordx4 v[10:11], v[2:5], off sc1
	s_nop 1
	v_add_u32_e32 v10, 10, v8
	v_ashrrev_i32_e32 v11, 31, v10
	v_lshlrev_b64 v[10:11], 12, v[10:11]
	v_lshl_add_u64 v[10:11], s[18:19], 0, v[10:11]
	v_lshl_add_u64 v[10:11], v[10:11], 0, s[22:23]
.Lst_op_65:
	s_cbranch_execz .Lsc_join_op
	v_lshl_add_u64 v[10:11], v[10:11], 0, v[146:147]
	ds_read_b128 v[2:5], v6 offset:5280
	s_waitcnt lgkmcnt(0)
	global_store_dwordx4 v[10:11], v[2:5], off sc1
	s_nop 1
	v_add_u32_e32 v10, 12, v8
	v_ashrrev_i32_e32 v11, 31, v10
	v_lshlrev_b64 v[10:11], 12, v[10:11]
	v_lshl_add_u64 v[10:11], s[18:19], 0, v[10:11]
	v_lshl_add_u64 v[10:11], v[10:11], 0, s[22:23]
	v_lshl_add_u64 v[10:11], v[10:11], 0, v[146:147]
	ds_read_b128 v[2:5], v6 offset:6336
	s_waitcnt lgkmcnt(0)
	global_store_dwordx4 v[10:11], v[2:5], off sc1
	s_nop 1
	v_add_u32_e32 v10, 14, v8
	v_ashrrev_i32_e32 v11, 31, v10
	v_lshlrev_b64 v[10:11], 12, v[10:11]
	v_lshl_add_u64 v[10:11], s[18:19], 0, v[10:11]
	v_lshl_add_u64 v[10:11], v[10:11], 0, s[22:23]
.Lst_op_66:
	s_cbranch_execz .Lsc_join_op
	v_lshl_add_u64 v[10:11], v[10:11], 0, v[146:147]
	ds_read_b128 v[2:5], v6 offset:7392
	s_waitcnt lgkmcnt(0)
	global_store_dwordx4 v[10:11], v[2:5], off sc1
	s_nop 1
	v_add_u32_e32 v10, 16, v8
	v_ashrrev_i32_e32 v11, 31, v10
	v_lshlrev_b64 v[10:11], 12, v[10:11]
	v_lshl_add_u64 v[10:11], s[18:19], 0, v[10:11]
	v_lshl_add_u64 v[10:11], v[10:11], 0, s[22:23]
	v_lshl_add_u64 v[10:11], v[10:11], 0, v[146:147]
	ds_read_b128 v[2:5], v6 offset:8448
	s_waitcnt lgkmcnt(0)
	global_store_dwordx4 v[10:11], v[2:5], off sc1
	s_nop 1
	v_add_u32_e32 v10, 18, v8
	v_ashrrev_i32_e32 v11, 31, v10
	v_lshlrev_b64 v[10:11], 12, v[10:11]
	v_lshl_add_u64 v[10:11], s[18:19], 0, v[10:11]
	v_lshl_add_u64 v[10:11], v[10:11], 0, s[22:23]
.Lst_op_67:
	s_cbranch_execz .Lsc_join_op
	v_lshl_add_u64 v[10:11], v[10:11], 0, v[146:147]
	ds_read_b128 v[2:5], v6 offset:9504
	s_waitcnt lgkmcnt(0)
	global_store_dwordx4 v[10:11], v[2:5], off sc1
	s_nop 1
	v_add_u32_e32 v10, 20, v8
	v_ashrrev_i32_e32 v11, 31, v10
	v_lshlrev_b64 v[10:11], 12, v[10:11]
	v_lshl_add_u64 v[10:11], s[18:19], 0, v[10:11]
	v_lshl_add_u64 v[10:11], v[10:11], 0, s[22:23]
	v_lshl_add_u64 v[10:11], v[10:11], 0, v[146:147]
	ds_read_b128 v[2:5], v6 offset:10560
	s_waitcnt lgkmcnt(0)
	global_store_dwordx4 v[10:11], v[2:5], off sc1
	s_nop 1
	v_add_u32_e32 v10, 22, v8
	v_ashrrev_i32_e32 v11, 31, v10
	v_lshlrev_b64 v[10:11], 12, v[10:11]
	v_lshl_add_u64 v[10:11], s[18:19], 0, v[10:11]
	v_lshl_add_u64 v[10:11], v[10:11], 0, s[22:23]
.Lst_op_68:
	s_cbranch_execz .Lsc_join_op
	v_lshl_add_u64 v[10:11], v[10:11], 0, v[146:147]
	ds_read_b128 v[2:5], v6 offset:11616
	s_waitcnt lgkmcnt(0)
	global_store_dwordx4 v[10:11], v[2:5], off sc1
	s_nop 1
	v_add_u32_e32 v10, 24, v8
	v_ashrrev_i32_e32 v11, 31, v10
	v_lshlrev_b64 v[10:11], 12, v[10:11]
	v_lshl_add_u64 v[10:11], s[18:19], 0, v[10:11]
	v_lshl_add_u64 v[10:11], v[10:11], 0, s[22:23]
	v_lshl_add_u64 v[10:11], v[10:11], 0, v[146:147]
	ds_read_b128 v[2:5], v6 offset:12672
	s_waitcnt lgkmcnt(0)
	global_store_dwordx4 v[10:11], v[2:5], off sc1
	s_nop 1
	v_add_u32_e32 v10, 26, v8
	v_ashrrev_i32_e32 v11, 31, v10
	v_lshlrev_b64 v[10:11], 12, v[10:11]
	v_lshl_add_u64 v[10:11], s[18:19], 0, v[10:11]
	v_lshl_add_u64 v[10:11], v[10:11], 0, s[22:23]
.Lst_op_69:
	s_cbranch_execz .Lsc_join_op
	v_lshl_add_u64 v[10:11], v[10:11], 0, v[146:147]
	ds_read_b128 v[2:5], v6 offset:13728
	s_waitcnt lgkmcnt(0)
	global_store_dwordx4 v[10:11], v[2:5], off sc1
	s_nop 1
	v_add_u32_e32 v10, 28, v8
	v_ashrrev_i32_e32 v11, 31, v10
	v_lshlrev_b64 v[10:11], 12, v[10:11]
	v_lshl_add_u64 v[10:11], s[18:19], 0, v[10:11]
	v_lshl_add_u64 v[10:11], v[10:11], 0, s[22:23]
	ds_read_b128 v[2:5], v6 offset:14784
	v_lshl_add_u64 v[10:11], v[10:11], 0, v[146:147]
	s_waitcnt lgkmcnt(0)
	global_store_dwordx4 v[10:11], v[2:5], off sc1
	s_nop 1
	ds_read_b128 v[2:5], v6 offset:15840
	v_add_u32_e32 v6, 30, v8
	v_ashrrev_i32_e32 v7, 31, v6
	v_lshlrev_b64 v[6:7], 12, v[6:7]
	v_lshl_add_u64 v[6:7], s[18:19], 0, v[6:7]
.Lst_op_70:
	s_cbranch_execz .Lsc_join_op
	v_lshl_add_u64 v[6:7], v[6:7], 0, s[22:23]
	v_lshl_add_u64 v[6:7], v[6:7], 0, v[146:147]
	s_waitcnt lgkmcnt(0)
	global_store_dwordx4 v[6:7], v[2:5], off sc1
	s_nop 1
	s_waitcnt lgkmcnt(0)
	s_barrier
	s_cbranch_vccnz .LBB0_1127
	s_waitcnt vmcnt(0)
	s_barrier
	s_and_saveexec_b64 s[4:5], s[0:1]
	s_cbranch_execz .LBB0_1126
	s_mov_b64 s[6:7], exec
	v_mbcnt_lo_u32_b32 v2, s6, 0
	v_mbcnt_hi_u32_b32 v2, s7, v2
	v_cmp_eq_u32_e32 vcc, 0, v2
	s_and_b64 s[22:23], exec, vcc
	s_mov_b64 exec, s[22:23]
	s_cbranch_execz .LBB0_1126
	s_lshl_b32 s22, s37, 4
	s_ashr_i32 s23, s22, 31
	s_lshl_b64 s[22:23], s[22:23], 2
	s_add_u32 s22, s29, s22
	s_addc_u32 s23, s30, s23
	s_bcnt1_i32_b64 s6, s[6:7]
	v_mov_b32_e32 v2, s6
	global_atomic_add v147, v2, s[22:23]
	s_branch .LBB0_1126

.LBB0_1420:
.Lst_m1_0:
	s_cbranch_execz .Lst_m1_7
	s_add_i32 s11, s11, 1

.Lst_m1_1:
	s_cbranch_execz .Lst_m1_8
	v_mov_b32_e32 v207, v211
	v_mov_b64_e32 v[186:187], 0
	v_mov_b64_e32 v[188:189], 0
	s_cbranch_vccnz .LBB0_1425
	s_add_i32 s28, s11, 1
	s_lshl_b32 s4, s28, 8
	s_add_i32 s29, s4, s50
	s_add_i32 s31, s29, 0xffffff80
	s_and_b64 s[4:5], s[14:15], exec
	s_cselect_b32 s4, s29, s31
	s_cmp_eq_u32 s28, 5
	s_cselect_b32 s4, s4, s29
	s_cselect_b32 s28, s42, 0
	s_ashr_i32 s29, s4, 2
	s_mul_hi_i32 s5, s29, 0x2e8ba2e9
	s_lshl_b32 s4, s4, 8
	s_lshr_b32 s31, s5, 31
	s_ashr_i32 s5, s5, 2
	s_and_b32 s4, s4, 0x300
	s_add_i32 s5, s5, s31
	v_add_u32_e32 v2, s4, v195
	s_waitcnt vmcnt(6)
	v_lshrrev_b32_e32 v12, 8, v2
	s_lshl_b32 s31, s5, 8
	s_lshl_b32 s33, s4, 4
	v_add_u32_e32 v10, s4, v202
	v_lshl_add_u32 v2, v12, 12, s31
	s_add_i32 s33, s33, s31
.Lst_m1_2:
	s_cbranch_execz .Lst_m1_9
	v_or_b32_e32 v6, 64, v171
	v_lshrrev_b32_e32 v13, 8, v10
	v_or_b32_e32 v2, v2, v195
	v_or_b32_e32 v4, s33, v171
	v_or_b32_e32 v6, s33, v6
	v_lshl_add_u32 v10, v13, 12, s31
	v_ashrrev_i32_e32 v3, 31, v2
	v_ashrrev_i32_e32 v5, 31, v4
	v_ashrrev_i32_e32 v7, 31, v6
	v_or_b32_e32 v8, s33, v191
	v_or_b32_e32 v10, v10, v202
	v_lshl_add_u64 v[2:3], v[2:3], 2, s[16:17]
	v_lshl_add_u64 v[4:5], v[4:5], 2, s[16:17]
	v_lshl_add_u64 v[6:7], v[6:7], 2, s[16:17]
	v_ashrrev_i32_e32 v9, 31, v8
	v_ashrrev_i32_e32 v11, 31, v10
	v_lshl_add_u64 v[8:9], v[8:9], 2, s[16:17]
	v_lshl_add_u64 v[10:11], v[10:11], 2, s[16:17]
	global_load_dword v14, v[2:3], off
	s_nop 0
	global_load_dword v4, v[4:5], off
	s_nop 0
	global_load_dword v5, v[6:7], off
.Lst_m1_3:
	s_cbranch_execz .Lst_m1_10
	s_nop 0
	global_load_dword v6, v[8:9], off
	global_load_dword v7, v[10:11], off
	v_lshrrev_b32_e32 v2, 2, v0
	v_mov_b32_e32 v3, 0x1600000
	v_lshlrev_b32_e32 v9, 22, v13
	v_add_u32_e32 v8, s28, v2
	s_lshl_b32 s31, s4, 14
	s_mul_i32 s33, s5, 22
	v_mad_i64_i32 v[2:3], s[4:5], s5, v3, v[176:177]
	s_sub_i32 s4, s29, s33
	s_lshl_b32 s4, s4, 7
	s_ashr_i32 s5, s4, 31
	v_mov_b32_e32 v181, v173
	s_waitcnt vmcnt(4)
	v_lshlrev_b32_e32 v10, 11, v14
	s_waitcnt vmcnt(3)
	v_lshl_add_u32 v4, v4, 11, s31
	s_waitcnt vmcnt(2)
	v_lshl_add_u32 v5, v5, 11, s31
	s_waitcnt vmcnt(1)
	v_lshl_add_u32 v6, v6, 11, s31
	s_waitcnt vmcnt(0)
	v_lshl_add_u32 v7, v7, 11, v9
.Lst_m1_4:
	s_cbranch_execz .Lst_m1_11
	v_lshl_add_u32 v9, v12, 22, v10
	v_or_b32_e32 v172, s28, v9
	v_lshl_add_u64 v[184:185], v[172:173], 1, v[174:175]
	v_mul_u32_u24_e32 v172, 0x2c00, v8
	v_lshl_add_u64 v[2:3], v[2:3], 0, v[172:173]
	v_lshl_add_u64 v[2:3], s[4:5], 2, v[2:3]
	v_or3_b32 v4, v4, v201, s28
	v_or3_b32 v5, v5, v201, s28
	v_or3_b32 v6, v6, v201, s28
	v_or3_b32 v7, v7, v201, s28
	v_lshl_add_u64 v[186:187], v[2:3], 0, v[180:181]
	v_lshlrev_b32_e32 v204, 1, v4
	v_lshlrev_b32_e32 v205, 1, v5
	v_lshlrev_b32_e32 v206, 1, v6
	v_lshlrev_b32_e32 v207, 1, v7
	v_lshl_add_u64 v[188:189], v[186:187], 0, s[20:21]

.Lst_m1_5:
	s_cbranch_execz .Lst_m1_12
	s_ashr_i32 s79, s3, 2
	s_add_i32 s79, s79, s28
	s_mul_i32 s3, s79, 22
	s_mul_hi_i32 s35, s79, 0x580000
	s_mul_i32 s34, s79, 0x580000
	s_xor_b64 s[36:37], s[24:25], -1
	s_and_b32 s78, s30, 3
	s_sub_i32 s28, s2, s3
	s_lshl_b64 s[2:3], s[34:35], 2
	s_add_u32 s31, s60, s2
	s_addc_u32 s33, s61, s3
	s_lshl_b32 s28, s28, 7
	s_ashr_i32 s29, s28, 31
	s_lshl_b64 s[38:39], s[28:29], 2
	s_add_u32 s59, s31, s38
	s_addc_u32 s73, s33, s39
	s_add_u32 s2, s62, s2
	s_addc_u32 s3, s63, s3
	s_add_u32 s74, s2, s38
	v_cndmask_b32_e64 v2, 0, 1, s[4:5]
	s_addc_u32 s75, s3, s39
	s_mov_b64 s[2:3], -1
	s_and_b64 vcc, exec, s[36:37]
	v_cmp_ne_u32_e64 s[4:5], 1, v2
	s_cbranch_vccz .LBB0_1437
	v_readfirstlane_b32 s2, v0
	s_lshl_b32 s3, s79, 8
	s_and_b64 vcc, exec, s[4:5]
.Lst_m1_6:
	s_cbranch_execz .Lst_m1_13
	v_mov_b32_e32 v34, v208
	s_cbranch_vccnz .LBB0_1428
	s_lshl_b32 s31, s78, 12
	s_add_i32 s31, s3, s31
	v_or_b32_e32 v2, s31, v171
	v_ashrrev_i32_e32 v3, 31, v2
	v_lshl_add_u64 v[2:3], v[2:3], 2, s[16:17]
	global_load_dword v2, v[2:3], off
	v_lshl_or_b32 v3, s78, 23, v190
	s_waitcnt vmcnt(0)
	v_lshl_add_u32 v34, v2, 12, v3

.Lst_m1_7:
	s_cbranch_execz .Lst_m1_14
	s_waitcnt vmcnt(0)
	v_lshl_add_u32 v35, v3, 12, v4
	s_and_b64 vcc, exec, s[4:5]
	v_mov_b32_e32 v36, v210
	s_cbranch_vccz .LBB0_1459

.Lst_m1_8:
	s_cbranch_execz .Lst_m1_15
	v_and_or_b32 v3, v2, 3, s36
	s_lshr_b32 s36, s2, 1
	s_or_b32 s2, s37, 32
	v_bitop3_b32 v183, s2, v203, v198 bitop3:0xde
	s_or_b32 s2, s37, 0x100
	v_bitop3_b32 v181, s2, v203, v198 bitop3:0xde
	s_or_b32 s2, s37, 0x120
	s_lshl_b32 s38, s33, 10
	v_bitop3_b32 v172, s2, v203, v198 bitop3:0xde
	s_add_i32 s38, s38, 0
	s_mov_b32 s2, m0
	s_mov_b32 m0, s38
	s_nop 0
	global_load_lds_dwordx4 v34, s[18:19]
	s_mov_b32 m0, s2
	s_add_i32 s2, s38, 0x2000
	s_mov_b32 s39, m0
	s_mov_b32 m0, s2
	s_nop 0
	global_load_lds_dwordx4 v35, s[18:19]
	s_mov_b32 m0, s39
	s_add_i32 s2, s38, 0x4000
.Lst_m1_9:
	s_cbranch_execz .Lst_m1_16
	s_mov_b32 s39, m0
	s_mov_b32 m0, s2
	s_nop 0
	global_load_lds_dwordx4 v36, s[18:19]
	s_mov_b32 m0, s39
	s_add_i32 s2, s38, 0x6000
	v_lshlrev_b32_e32 v2, 9, v2
	v_lshlrev_b32_e32 v3, 5, v3
	s_and_b32 s36, s36, 0x7fffff80
	s_mov_b32 s39, m0
	s_mov_b32 m0, s2
	s_nop 0
	global_load_lds_dwordx4 v37, s[18:19]
	s_mov_b32 m0, s39
	s_mul_i32 s2, s33, 0x5800
	v_bitop3_b32 v214, v3, v2, v194 bitop3:0xde
	v_or_b32_e32 v2, s36, v1
	s_mul_hi_u32 s39, s3, 0x2c00
	s_add_u32 s40, s59, s2
	s_waitcnt vmcnt(1)
	v_lshlrev_b32_e32 v38, 7, v2
	s_addc_u32 s41, s73, s39
	global_load_dwordx4 v[2:5], v199, s[40:41] nt
	s_add_i32 s40, s3, 16
.Lst_m1_10:
	s_cbranch_execz .Lst_m1_17
	s_add_i32 s83, s2, 0x2c000
	s_mul_hi_u32 s84, s40, 0x2c00
	s_add_u32 s40, s59, s83
	s_addc_u32 s41, s73, s84
	global_load_dwordx4 v[6:9], v199, s[40:41] nt
	s_add_i32 s40, s3, 32
	s_add_i32 s85, s2, 0x58000
	s_mul_hi_u32 s86, s40, 0x2c00
	s_add_u32 s40, s59, s85
	s_addc_u32 s41, s73, s86
	global_load_dwordx4 v[10:13], v199, s[40:41] nt
	s_add_i32 s40, s3, 48
	s_add_i32 s87, s2, 0x84000
	s_mul_hi_u32 s88, s40, 0x2c00
	s_add_u32 s40, s59, s87
	s_addc_u32 s41, s73, s88
	global_load_dwordx4 v[14:17], v199, s[40:41] nt
	s_add_u32 s40, s74, s2
	s_addc_u32 s41, s75, s39
	global_load_dwordx4 v[18:21], v199, s[40:41] nt
	s_add_u32 s40, s74, s83
	s_addc_u32 s41, s75, s84
.Lst_m1_11:
	s_cbranch_execz .Lst_m1_18
	global_load_dwordx4 v[22:25], v199, s[40:41] nt
	s_add_u32 s40, s74, s85
	s_addc_u32 s41, s75, s86
	global_load_dwordx4 v[26:29], v199, s[40:41] nt
	s_add_u32 s40, s74, s87
	s_addc_u32 s41, s75, s88
	global_load_dwordx4 v[30:33], v199, s[40:41] nt
	s_add_i32 s40, s38, 0x8000
	v_add_u32_e32 v39, 0x80, v34
	s_mov_b32 s41, m0
	s_mov_b32 m0, s40
	s_nop 0
	global_load_lds_dwordx4 v39, s[18:19]
	s_mov_b32 m0, s41
	v_add_u32_e32 v39, 0x80, v35
	s_add_i32 s40, s38, 0xa000
	s_mov_b32 s41, m0
	s_mov_b32 m0, s40
	s_nop 0
	global_load_lds_dwordx4 v39, s[18:19]
	s_mov_b32 m0, s41
	v_add_u32_e32 v39, 0x80, v36
.Lst_m1_12:
	s_cbranch_execz .Lst_m1_19
	s_add_i32 s40, s38, 0xc000
	s_mov_b32 s41, m0
	s_mov_b32 m0, s40
	s_nop 0
	global_load_lds_dwordx4 v39, s[18:19]
	s_mov_b32 m0, s41
	v_add_u32_e32 v39, 0x80, v37
	s_add_i32 s40, s38, 0xe000
	s_mov_b32 s41, m0
	s_mov_b32 m0, s40
	s_nop 0
	global_load_lds_dwordx4 v39, s[18:19]
	s_mov_b32 m0, s41
	s_waitcnt vmcnt(4)
	v_add_u32_e32 v217, s52, v214
	v_cvt_pk_bf16_f32 v2, v2, v3
	v_cvt_pk_bf16_f32 v3, v4, v5
	v_cvt_pk_bf16_f32 v4, v6, v7
	v_cvt_pk_bf16_f32 v5, v8, v9
	v_or_b32_e32 v213, 0x100, v214
	ds_write2st64_b64 v217, v[2:3], v[4:5] offset1:16
.Lst_m1_13:
	s_cbranch_execz .Lst_m1_20
	v_cvt_pk_bf16_f32 v2, v10, v11
	v_cvt_pk_bf16_f32 v3, v12, v13
	v_cvt_pk_bf16_f32 v4, v14, v15
	v_cvt_pk_bf16_f32 v5, v16, v17
	ds_write2st64_b64 v217, v[2:3], v[4:5] offset0:32 offset1:48
	v_cvt_pk_bf16_f32 v2, v18, v19
	v_cvt_pk_bf16_f32 v3, v20, v21
	v_add_u32_e32 v6, s52, v213
	v_cvt_pk_bf16_f32 v4, v22, v23
	v_cvt_pk_bf16_f32 v5, v24, v25
	s_add_i32 s40, s3, 64
	s_add_i32 s83, s2, 0xb0000
	ds_write2st64_b64 v6, v[2:3], v[4:5] offset1:16
	v_cvt_pk_bf16_f32 v2, v26, v27
	v_cvt_pk_bf16_f32 v3, v28, v29
	v_cvt_pk_bf16_f32 v4, v30, v31
	v_cvt_pk_bf16_f32 v5, v32, v33
.Lst_m1_14:
	s_cbranch_execz .Lst_m1_21
	s_mul_hi_u32 s84, s40, 0x2c00
	s_add_u32 s40, s59, s83
	ds_write2st64_b64 v6, v[2:3], v[4:5] offset0:32 offset1:48
	s_addc_u32 s41, s73, s84
	global_load_dwordx4 v[30:33], v199, s[40:41] nt
	s_add_i32 s40, s3, 0x50
	s_add_i32 s85, s2, 0xdc000
	s_mul_hi_u32 s86, s40, 0x2c00
	s_add_u32 s40, s59, s85
	s_addc_u32 s41, s73, s86
	global_load_dwordx4 v[26:29], v199, s[40:41] nt
	s_add_i32 s40, s3, 0x60
	s_add_i32 s87, s2, 0x108000
	s_mul_hi_u32 s88, s40, 0x2c00
	s_add_u32 s40, s59, s87
	s_addc_u32 s41, s73, s88
	s_addk_i32 s3, 0x70
	s_add_i32 s89, s2, 0x134000
	global_load_dwordx4 v[22:25], v199, s[40:41] nt
	s_mul_hi_u32 s3, s3, 0x2c00
.Lst_m1_15:
	s_cbranch_execz .Lst_m1_22
	s_add_u32 s40, s59, s89
	s_addc_u32 s41, s73, s3
	global_load_dwordx4 v[18:21], v199, s[40:41] nt
	s_add_u32 s40, s74, s83
	s_addc_u32 s41, s75, s84
	global_load_dwordx4 v[14:17], v199, s[40:41] nt
	s_add_u32 s40, s74, s85
	s_addc_u32 s41, s75, s86
	global_load_dwordx4 v[10:13], v199, s[40:41] nt
	s_add_u32 s40, s74, s87
	s_addc_u32 s41, s75, s88
	global_load_dwordx4 v[6:9], v199, s[40:41] nt
	s_add_u32 s40, s74, s89
	s_addc_u32 s41, s75, s3
	global_load_dwordx4 v[2:5], v199, s[40:41] nt
	s_mul_hi_u32 s3, s33, 0x5800
	s_add_u32 s40, s74, s2
	s_waitcnt lgkmcnt(0)
	s_barrier
	s_addc_u32 s41, s75, s3
	s_add_u32 s83, s59, s2
	v_add_u32_e32 v221, 0x100, v34
	v_mov_b32_e32 v34, 0
	v_bitop3_b32 v212, s37, v203, v198 bitop3:0xde
.Lst_m1_16:
	s_cbranch_execz .Lst_m1_23
	v_or_b32_e32 v215, v38, v196
	s_mov_b32 s39, 0x8000
	v_or_b32_e32 v216, v38, v197
	s_addc_u32 s84, s73, s3
	v_add_u32_e32 v218, 0x100, v37
	v_add_u32_e32 v219, 0x100, v36
	v_add_u32_e32 v220, 0x100, v35
	s_mov_b32 s85, 0x10000
	s_mov_b32 s86, 0
	s_mov_b64 s[2:3], 0
	v_mov_b32_e32 v35, v34
	v_mov_b32_e32 v36, v34
	v_mov_b32_e32 v37, v34
	v_mov_b32_e32 v38, v34
	v_mov_b32_e32 v39, v34
	v_mov_b32_e32 v40, v34
	v_mov_b32_e32 v41, v34
	v_mov_b32_e32 v46, v34
	v_mov_b32_e32 v47, v34
	v_mov_b32_e32 v48, v34
	v_mov_b32_e32 v49, v34
	v_mov_b32_e32 v50, v34
	v_mov_b32_e32 v51, v34
	v_mov_b32_e32 v52, v34
	v_mov_b32_e32 v53, v34
	s_waitcnt vmcnt(0)
	v_mov_b32_e32 v42, v34
.Lst_m1_17:
	s_cbranch_execz .Lst_m1_24
	v_mov_b32_e32 v43, v34
	v_mov_b32_e32 v44, v34
	v_mov_b32_e32 v45, v34
	v_mov_b32_e32 v54, v34
	v_mov_b32_e32 v55, v34
	v_mov_b32_e32 v56, v34
	v_mov_b32_e32 v57, v34
	v_mov_b32_e32 v58, v34
	v_mov_b32_e32 v59, v34
	v_mov_b32_e32 v60, v34
	v_mov_b32_e32 v61, v34
	v_mov_b32_e32 v62, v34
	v_mov_b32_e32 v63, v34
	v_mov_b32_e32 v64, v34
	v_mov_b32_e32 v65, v34
	v_mov_b32_e32 v66, v34
	v_mov_b32_e32 v67, v34
	v_mov_b32_e32 v68, v34
	v_mov_b32_e32 v69, v34
	v_mov_b32_e32 v70, v34
	v_mov_b32_e32 v71, v34
	v_mov_b32_e32 v72, v34
	v_mov_b32_e32 v73, v34
	v_mov_b32_e32 v74, v34
	v_mov_b32_e32 v75, v34
	v_mov_b32_e32 v76, v34
	v_mov_b32_e32 v77, v34
	v_mov_b32_e32 v78, v34
	v_mov_b32_e32 v79, v34
	v_mov_b32_e32 v80, v34
	v_mov_b32_e32 v81, v34
	v_mov_b32_e32 v82, v34
.Lst_m1_18:
	s_cbranch_execz .Lst_m1_25
	v_mov_b32_e32 v83, v34
	v_mov_b32_e32 v84, v34
	v_mov_b32_e32 v85, v34
	v_mov_b32_e32 v86, v34
	v_mov_b32_e32 v87, v34
	v_mov_b32_e32 v88, v34
	v_mov_b32_e32 v89, v34
	v_mov_b32_e32 v90, v34
	v_mov_b32_e32 v91, v34
	v_mov_b32_e32 v92, v34
	v_mov_b32_e32 v93, v34
	v_mov_b32_e32 v94, v34
	v_mov_b32_e32 v95, v34
	v_mov_b32_e32 v96, v34
	v_mov_b32_e32 v97, v34
	v_mov_b32_e32 v98, v34
	v_mov_b32_e32 v99, v34
	v_mov_b32_e32 v100, v34
	v_mov_b32_e32 v101, v34
	v_mov_b32_e32 v102, v34
	v_mov_b32_e32 v103, v34
	v_mov_b32_e32 v104, v34
	v_mov_b32_e32 v105, v34
	v_mov_b32_e32 v106, v34
	v_mov_b32_e32 v107, v34
	v_mov_b32_e32 v108, v34
	v_mov_b32_e32 v109, v34
	v_mov_b32_e32 v110, v34
	v_mov_b32_e32 v111, v34
	v_mov_b32_e32 v112, v34
	v_mov_b32_e32 v113, v34
	v_mov_b32_e32 v114, v34
.Lst_m1_19:
	s_cbranch_execz .Lst_m1_26
	v_mov_b32_e32 v115, v34
	v_mov_b32_e32 v116, v34
	v_mov_b32_e32 v117, v34
	v_mov_b32_e32 v118, v34
	v_mov_b32_e32 v119, v34
	v_mov_b32_e32 v120, v34
	v_mov_b32_e32 v121, v34
	v_mov_b32_e32 v122, v34
	v_mov_b32_e32 v123, v34
	v_mov_b32_e32 v124, v34
	v_mov_b32_e32 v125, v34
	v_mov_b32_e32 v126, v34
	v_mov_b32_e32 v127, v34
	v_mov_b32_e32 v128, v34
	v_mov_b32_e32 v129, v34
	v_mov_b32_e32 v130, v34
	v_mov_b32_e32 v131, v34
	v_mov_b32_e32 v132, v34
	v_mov_b32_e32 v133, v34
	v_mov_b32_e32 v134, v34
	v_mov_b32_e32 v135, v34
	v_mov_b32_e32 v136, v34
	v_mov_b32_e32 v137, v34
	v_mov_b32_e32 v138, v34
	v_mov_b32_e32 v139, v34
	v_mov_b32_e32 v140, v34
	v_mov_b32_e32 v141, v34
	v_mov_b32_e32 v142, v34
	v_mov_b32_e32 v143, v34
	v_mov_b32_e32 v144, v34
	v_mov_b32_e32 v145, v34
	v_mov_b32_e32 v146, v34
.Lst_m1_20:
	s_cbranch_execz .Lst_m1_27
	v_mov_b32_e32 v147, v34
	v_mov_b32_e32 v148, v34
	v_mov_b32_e32 v149, v34
	v_mov_b32_e32 v150, v34
	v_mov_b32_e32 v151, v34
	v_mov_b32_e32 v152, v34
	v_mov_b32_e32 v153, v34
	v_mov_b32_e32 v154, v34
	v_mov_b32_e32 v155, v34
	v_mov_b32_e32 v156, v34
	v_mov_b32_e32 v157, v34
	v_mov_b32_e32 v158, v34
	v_mov_b32_e32 v159, v34
	v_mov_b32_e32 v160, v34
	v_mov_b32_e32 v161, v34

.Lst_m1_21:
	s_cbranch_execz .Lst_m1_28
	v_add_u32_e32 v200, s52, v212
	v_add_u32_e32 v250, 0, v215
	v_add_u32_e32 v215, s52, v181
	v_add_u32_e32 v251, s52, v172
	v_add_u32_e32 v217, s52, v183
	ds_read_b64_tr_b16 v[162:163], v200
	ds_read_b64_tr_b16 v[164:165], v200 offset:2048
	ds_read_b64_tr_b16 v[166:167], v217
	ds_read_b64_tr_b16 v[168:169], v217 offset:2048
	ds_read_b128 v[218:221], v250
	ds_read_b128 v[222:225], v250 offset:2048
	ds_read_b64_tr_b16 v[226:227], v215
	ds_read_b64_tr_b16 v[228:229], v215 offset:2048
	ds_read_b64_tr_b16 v[230:231], v251
	ds_read_b64_tr_b16 v[232:233], v251 offset:2048
	s_waitcnt lgkmcnt(5)
	v_mfma_f32_16x16x32_bf16 v[62:65], v[162:165], v[218:221], v[62:65]
	ds_read_b128 v[234:237], v250 offset:4096
	v_mfma_f32_16x16x32_bf16 v[58:61], v[166:169], v[218:221], v[58:61]
.Lst_m1_22:
	s_cbranch_execz .Lst_m1_29
	s_waitcnt lgkmcnt(3)
	v_mfma_f32_16x16x32_bf16 v[54:57], v[226:229], v[218:221], v[54:57]
	s_waitcnt lgkmcnt(1)
	v_mfma_f32_16x16x32_bf16 v[42:45], v[230:233], v[218:221], v[42:45]
	v_mfma_f32_16x16x32_bf16 v[50:53], v[162:165], v[222:225], v[50:53]
	ds_read_b128 v[218:221], v250 offset:6144
	v_mfma_f32_16x16x32_bf16 v[46:49], v[166:169], v[222:225], v[46:49]
	v_mfma_f32_16x16x32_bf16 v[38:41], v[226:229], v[222:225], v[38:41]
	v_mfma_f32_16x16x32_bf16 v[34:37], v[230:233], v[222:225], v[34:37]
	s_waitcnt lgkmcnt(1)
	v_mfma_f32_16x16x32_bf16 v[66:69], v[162:165], v[234:237], v[66:69]
	ds_read_b128 v[222:225], v250 offset:8192
	v_mfma_f32_16x16x32_bf16 v[70:73], v[166:169], v[234:237], v[70:73]
	v_mfma_f32_16x16x32_bf16 v[74:77], v[226:229], v[234:237], v[74:77]
	v_mfma_f32_16x16x32_bf16 v[78:81], v[230:233], v[234:237], v[78:81]
	s_waitcnt lgkmcnt(1)
	v_mfma_f32_16x16x32_bf16 v[82:85], v[162:165], v[218:221], v[82:85]
	ds_read_b128 v[234:237], v250 offset:10240
.Lst_m1_23:
	s_cbranch_execz .Lst_m1_30
	v_mfma_f32_16x16x32_bf16 v[86:89], v[166:169], v[218:221], v[86:89]
	v_mfma_f32_16x16x32_bf16 v[90:93], v[226:229], v[218:221], v[90:93]
	v_mfma_f32_16x16x32_bf16 v[94:97], v[230:233], v[218:221], v[94:97]
	ds_read_b128 v[218:221], v250 offset:12288
	ds_read_b64_tr_b16 v[238:239], v200 offset:16384
	ds_read_b64_tr_b16 v[240:241], v200 offset:18432
	s_waitcnt lgkmcnt(4)
	v_mfma_f32_16x16x32_bf16 v[98:101], v[162:165], v[222:225], v[98:101]
	v_mfma_f32_16x16x32_bf16 v[102:105], v[166:169], v[222:225], v[102:105]
	v_mfma_f32_16x16x32_bf16 v[106:109], v[226:229], v[222:225], v[106:109]
	v_mfma_f32_16x16x32_bf16 v[110:113], v[230:233], v[222:225], v[110:113]
	ds_read_b128 v[222:225], v250 offset:14336
	ds_read_b64_tr_b16 v[242:243], v217 offset:16384
	ds_read_b64_tr_b16 v[244:245], v217 offset:18432
	s_waitcnt lgkmcnt(6)
	v_mfma_f32_16x16x32_bf16 v[114:117], v[162:165], v[234:237], v[114:117]
	v_mfma_f32_16x16x32_bf16 v[118:121], v[166:169], v[234:237], v[118:121]
.Lst_m1_24:
	s_cbranch_execz .Lst_m1_31
	v_mfma_f32_16x16x32_bf16 v[122:125], v[226:229], v[234:237], v[122:125]
	v_mfma_f32_16x16x32_bf16 v[126:129], v[230:233], v[234:237], v[126:129]
	v_add_u32_e32 v200, 0, v216
	ds_read_b128 v[234:237], v200
	ds_read_b64_tr_b16 v[246:247], v215 offset:16384
	ds_read_b64_tr_b16 v[248:249], v215 offset:18432
	s_waitcnt lgkmcnt(8)
	v_mfma_f32_16x16x32_bf16 v[130:133], v[162:165], v[218:221], v[130:133]
	v_mfma_f32_16x16x32_bf16 v[134:137], v[166:169], v[218:221], v[134:137]
	v_mfma_f32_16x16x32_bf16 v[138:141], v[226:229], v[218:221], v[138:141]
	v_mfma_f32_16x16x32_bf16 v[142:145], v[230:233], v[218:221], v[142:145]
	s_waitcnt lgkmcnt(5)
	v_mfma_f32_16x16x32_bf16 v[146:149], v[162:165], v[222:225], v[146:149]
	v_mfma_f32_16x16x32_bf16 v[150:153], v[166:169], v[222:225], v[150:153]
	ds_read_b128 v[162:165], v200 offset:2048
	ds_read_b64_tr_b16 v[166:167], v251 offset:16384
	ds_read_b64_tr_b16 v[168:169], v251 offset:18432
	v_mfma_f32_16x16x32_bf16 v[154:157], v[226:229], v[222:225], v[154:157]
.Lst_m1_25:
	s_cbranch_execz .Lst_m1_32
	v_mfma_f32_16x16x32_bf16 v[158:161], v[230:233], v[222:225], v[158:161]
	ds_read_b128 v[216:219], v200 offset:4096
	s_waitcnt vmcnt(7)
	v_add_u32_e32 v214, s56, v214
	v_cvt_pk_bf16_f32 v30, v30, v31
	v_cvt_pk_bf16_f32 v31, v32, v33
	s_waitcnt lgkmcnt(6)
	v_mfma_f32_16x16x32_bf16 v[62:65], v[238:241], v[234:237], v[62:65]
	ds_write_b64 v214, v[30:31]
	v_mfma_f32_16x16x32_bf16 v[58:61], v[242:245], v[234:237], v[58:61]
	s_waitcnt lgkmcnt(5)
	v_mfma_f32_16x16x32_bf16 v[54:57], v[246:249], v[234:237], v[54:57]
	s_waitcnt lgkmcnt(2)
	v_mfma_f32_16x16x32_bf16 v[30:33], v[166:169], v[234:237], v[42:45]
	v_mfma_f32_16x16x32_bf16 v[42:45], v[238:241], v[162:165], v[50:53]
	s_nop 2
	ds_read_b128 v[50:53], v200 offset:6144
	s_waitcnt vmcnt(6)
	v_mfma_f32_16x16x32_bf16 v[46:49], v[242:245], v[162:165], v[46:49]
	v_cvt_pk_bf16_f32 v26, v26, v27
.Lst_m1_26:
	s_cbranch_execz .Lst_m1_33
	v_cvt_pk_bf16_f32 v27, v28, v29
	ds_write_b64 v214, v[26:27] offset:8192
	v_mfma_f32_16x16x32_bf16 v[38:41], v[246:249], v[162:165], v[38:41]
	v_mfma_f32_16x16x32_bf16 v[26:29], v[166:169], v[162:165], v[34:37]
	s_waitcnt lgkmcnt(3)
	v_mfma_f32_16x16x32_bf16 v[34:37], v[238:241], v[216:219], v[66:69]
	v_mfma_f32_16x16x32_bf16 v[66:69], v[242:245], v[216:219], v[70:73]
	s_nop 2
	ds_read_b128 v[70:73], v200 offset:8192
	s_waitcnt vmcnt(5)
	v_mfma_f32_16x16x32_bf16 v[74:77], v[246:249], v[216:219], v[74:77]
	v_cvt_pk_bf16_f32 v22, v22, v23
	v_cvt_pk_bf16_f32 v23, v24, v25
	ds_write_b64 v214, v[22:23] offset:16384
	v_mfma_f32_16x16x32_bf16 v[22:25], v[166:169], v[216:219], v[78:81]
	s_waitcnt lgkmcnt(3)
	v_mfma_f32_16x16x32_bf16 v[78:81], v[238:241], v[50:53], v[82:85]
	v_mfma_f32_16x16x32_bf16 v[82:85], v[242:245], v[50:53], v[86:89]
.Lst_m1_27:
	s_cbranch_execz .Lst_m1_34
	s_nop 2
	ds_read_b128 v[86:89], v200 offset:10240
	s_waitcnt vmcnt(4)
	v_mfma_f32_16x16x32_bf16 v[90:93], v[246:249], v[50:53], v[90:93]
	v_cvt_pk_bf16_f32 v18, v18, v19
	v_cvt_pk_bf16_f32 v19, v20, v21
	ds_write_b64 v214, v[18:19] offset:24576
	v_mfma_f32_16x16x32_bf16 v[18:21], v[166:169], v[50:53], v[94:97]
	s_waitcnt lgkmcnt(3)
	v_mfma_f32_16x16x32_bf16 v[50:53], v[238:241], v[70:73], v[98:101]
	v_add_u32_e32 v162, s56, v213
	s_nop 1
	ds_read_b128 v[98:101], v200 offset:12288
	s_waitcnt vmcnt(3)
	v_mfma_f32_16x16x32_bf16 v[94:97], v[242:245], v[70:73], v[102:105]
	v_cvt_pk_bf16_f32 v14, v14, v15
	v_cvt_pk_bf16_f32 v15, v16, v17
	ds_write_b64 v162, v[14:15]
	v_mfma_f32_16x16x32_bf16 v[102:105], v[246:249], v[70:73], v[106:109]
.Lst_m1_28:
	s_cbranch_execz .Lst_m1_35
	v_mfma_f32_16x16x32_bf16 v[14:17], v[166:169], v[70:73], v[110:113]
	s_nop 2
	ds_read_b128 v[110:113], v200 offset:14336
	s_waitcnt vmcnt(2)
	s_waitcnt lgkmcnt(4)
	v_mfma_f32_16x16x32_bf16 v[70:73], v[238:241], v[86:89], v[114:117]
	v_cvt_pk_bf16_f32 v10, v10, v11
	v_cvt_pk_bf16_f32 v11, v12, v13
	ds_write_b64 v162, v[10:11] offset:8192
	v_mfma_f32_16x16x32_bf16 v[106:109], v[242:245], v[86:89], v[118:121]
	v_mfma_f32_16x16x32_bf16 v[114:117], v[246:249], v[86:89], v[122:125]
	v_mfma_f32_16x16x32_bf16 v[10:13], v[166:169], v[86:89], v[126:129]
	s_waitcnt vmcnt(1)
	s_waitcnt lgkmcnt(3)
	v_mfma_f32_16x16x32_bf16 v[86:89], v[238:241], v[98:101], v[130:133]
	v_cvt_pk_bf16_f32 v6, v6, v7
	v_cvt_pk_bf16_f32 v7, v8, v9
	ds_write_b64 v162, v[6:7] offset:16384
	v_mfma_f32_16x16x32_bf16 v[118:121], v[242:245], v[98:101], v[134:137]
.Lst_m1_29:
	s_cbranch_execz .Lst_m1_36
	v_mfma_f32_16x16x32_bf16 v[122:125], v[246:249], v[98:101], v[138:141]
	v_mfma_f32_16x16x32_bf16 v[6:9], v[166:169], v[98:101], v[142:145]
	s_waitcnt vmcnt(0)
	s_waitcnt lgkmcnt(2)
	v_mfma_f32_16x16x32_bf16 v[98:101], v[238:241], v[110:113], v[146:149]
	v_cvt_pk_bf16_f32 v2, v2, v3
	v_cvt_pk_bf16_f32 v3, v4, v5
	ds_write_b64 v162, v[2:3] offset:24576
	v_mfma_f32_16x16x32_bf16 v[126:129], v[242:245], v[110:113], v[150:153]
	v_mfma_f32_16x16x32_bf16 v[130:133], v[246:249], v[110:113], v[154:157]
	v_mfma_f32_16x16x32_bf16 v[2:5], v[166:169], v[110:113], v[158:161]
	s_waitcnt lgkmcnt(0)
	s_barrier
	v_add_u32_e32 v168, s56, v212
	v_add_u32_e32 v183, s56, v183
	v_add_u32_e32 v181, s56, v181
	ds_read_b64_tr_b16 v[110:111], v168
	ds_read_b64_tr_b16 v[112:113], v168 offset:2048
	ds_read_b64_tr_b16 v[134:135], v183
	ds_read_b64_tr_b16 v[136:137], v183 offset:2048
.Lst_m1_30:
	s_cbranch_execz .Lst_m1_37
	ds_read_b128 v[138:141], v250 offset:32768
	ds_read_b64_tr_b16 v[142:143], v181
	ds_read_b128 v[146:149], v250 offset:34816
	ds_read_b128 v[150:153], v250 offset:36864
	ds_read_b64_tr_b16 v[144:145], v181 offset:2048
	v_add_u32_e32 v172, s56, v172
	ds_read_b64_tr_b16 v[154:155], v172
	ds_read_b64_tr_b16 v[156:157], v172 offset:2048
	s_waitcnt lgkmcnt(6)
	v_mfma_f32_16x16x32_bf16 v[62:65], v[110:113], v[138:141], v[62:65]
	v_mfma_f32_16x16x32_bf16 v[58:61], v[134:137], v[138:141], v[58:61]
	s_waitcnt lgkmcnt(2)
	v_mfma_f32_16x16x32_bf16 v[54:57], v[142:145], v[138:141], v[54:57]
	s_waitcnt lgkmcnt(0)
	v_mfma_f32_16x16x32_bf16 v[30:33], v[154:157], v[138:141], v[30:33]
	v_mfma_f32_16x16x32_bf16 v[42:45], v[110:113], v[146:149], v[42:45]
	ds_read_b128 v[138:141], v250 offset:38912
	v_mfma_f32_16x16x32_bf16 v[46:49], v[134:137], v[146:149], v[46:49]
.Lst_m1_31:
	s_cbranch_execz .Lst_m1_38
	v_mfma_f32_16x16x32_bf16 v[38:41], v[142:145], v[146:149], v[38:41]
	v_mfma_f32_16x16x32_bf16 v[26:29], v[154:157], v[146:149], v[26:29]
	v_mfma_f32_16x16x32_bf16 v[34:37], v[110:113], v[150:153], v[34:37]
	ds_read_b128 v[146:149], v250 offset:40960
	v_mfma_f32_16x16x32_bf16 v[66:69], v[134:137], v[150:153], v[66:69]
	v_mfma_f32_16x16x32_bf16 v[74:77], v[142:145], v[150:153], v[74:77]
	v_mfma_f32_16x16x32_bf16 v[22:25], v[154:157], v[150:153], v[22:25]
	s_waitcnt lgkmcnt(1)
	v_mfma_f32_16x16x32_bf16 v[150:153], v[134:137], v[138:141], v[82:85]
	s_nop 2
	ds_read_b128 v[82:85], v250 offset:43008
	v_mfma_f32_16x16x32_bf16 v[78:81], v[110:113], v[138:141], v[78:81]
	v_mfma_f32_16x16x32_bf16 v[18:21], v[154:157], v[138:141], v[18:21]
	v_mfma_f32_16x16x32_bf16 v[158:161], v[142:145], v[138:141], v[90:93]
	s_nop 2
	ds_read_b128 v[90:93], v250 offset:45056
	ds_read_b64_tr_b16 v[166:167], v168 offset:16384
	ds_read_b64_tr_b16 v[168:169], v168 offset:18432
.Lst_m1_32:
	s_cbranch_execz .Lst_m1_39
	s_waitcnt lgkmcnt(4)
	v_mfma_f32_16x16x32_bf16 v[50:53], v[110:113], v[146:149], v[50:53]
	v_mfma_f32_16x16x32_bf16 v[14:17], v[154:157], v[146:149], v[14:17]
	v_mfma_f32_16x16x32_bf16 v[138:141], v[134:137], v[146:149], v[94:97]
	v_mfma_f32_16x16x32_bf16 v[162:165], v[142:145], v[146:149], v[102:105]
	s_waitcnt lgkmcnt(3)
	v_mfma_f32_16x16x32_bf16 v[146:149], v[110:113], v[82:85], v[70:73]
	s_nop 2
	ds_read_b128 v[70:73], v250 offset:47104
	ds_read_b64_tr_b16 v[220:221], v183 offset:16384
	ds_read_b64_tr_b16 v[222:223], v183 offset:18432
	v_mfma_f32_16x16x32_bf16 v[10:13], v[154:157], v[82:85], v[10:13]
	v_mfma_f32_16x16x32_bf16 v[212:215], v[134:137], v[82:85], v[106:109]
	v_mfma_f32_16x16x32_bf16 v[216:219], v[142:145], v[82:85], v[114:117]
	ds_read_b128 v[82:85], v200 offset:32768
	ds_read_b64_tr_b16 v[236:237], v181 offset:16384
	ds_read_b64_tr_b16 v[238:239], v181 offset:18432
	s_waitcnt lgkmcnt(8)
.Lst_m1_33:
	s_cbranch_execz .Lst_m1_40
	v_mfma_f32_16x16x32_bf16 v[6:9], v[154:157], v[90:93], v[6:9]
	v_mfma_f32_16x16x32_bf16 v[224:227], v[110:113], v[90:93], v[86:89]
	v_mfma_f32_16x16x32_bf16 v[228:231], v[134:137], v[90:93], v[118:121]
	v_mfma_f32_16x16x32_bf16 v[232:235], v[142:145], v[90:93], v[122:125]
	s_waitcnt lgkmcnt(5)
	v_mfma_f32_16x16x32_bf16 v[130:133], v[142:145], v[70:73], v[130:133]
	ds_read_b128 v[86:89], v200 offset:34816
	ds_read_b64_tr_b16 v[142:143], v172 offset:16384
	ds_read_b64_tr_b16 v[144:145], v172 offset:18432
	v_mfma_f32_16x16x32_bf16 v[240:243], v[110:113], v[70:73], v[98:101]
	v_mfma_f32_16x16x32_bf16 v[134:137], v[134:137], v[70:73], v[126:129]
	v_mfma_f32_16x16x32_bf16 v[154:157], v[154:157], v[70:73], v[2:5]
	s_nop 2
	ds_read_b128 v[2:5], v200 offset:36864
	s_waitcnt lgkmcnt(6)
	v_mfma_f32_16x16x32_bf16 v[122:125], v[166:169], v[82:85], v[62:65]
	v_mfma_f32_16x16x32_bf16 v[114:117], v[220:223], v[82:85], v[58:61]
	s_waitcnt lgkmcnt(4)
.Lst_m1_34:
	s_cbranch_execz .Lst_m1_41
	v_mfma_f32_16x16x32_bf16 v[126:129], v[236:239], v[82:85], v[54:57]
	s_waitcnt lgkmcnt(1)
	v_mfma_f32_16x16x32_bf16 v[118:121], v[142:145], v[82:85], v[30:33]
	s_nop 2
	ds_read_b128 v[30:33], v200 offset:38912
	v_mfma_f32_16x16x32_bf16 v[106:109], v[166:169], v[86:89], v[42:45]
	v_mfma_f32_16x16x32_bf16 v[98:101], v[220:223], v[86:89], v[46:49]
	v_mfma_f32_16x16x32_bf16 v[110:113], v[236:239], v[86:89], v[38:41]
	v_mfma_f32_16x16x32_bf16 v[102:105], v[142:145], v[86:89], v[26:29]
	s_nop 2
	ds_read_b128 v[26:29], v200 offset:40960
	s_waitcnt lgkmcnt(2)
	v_mfma_f32_16x16x32_bf16 v[90:93], v[166:169], v[2:5], v[34:37]
	v_mfma_f32_16x16x32_bf16 v[82:85], v[220:223], v[2:5], v[66:69]
	v_mfma_f32_16x16x32_bf16 v[94:97], v[236:239], v[2:5], v[74:77]
	v_mfma_f32_16x16x32_bf16 v[86:89], v[142:145], v[2:5], v[22:25]
	ds_read_b128 v[2:5], v200 offset:43008
	s_waitcnt lgkmcnt(2)
	v_mfma_f32_16x16x32_bf16 v[74:77], v[166:169], v[30:33], v[78:81]
.Lst_m1_35:
	s_cbranch_execz .Lst_m1_42
	v_mfma_f32_16x16x32_bf16 v[66:69], v[220:223], v[30:33], v[150:153]
	v_mfma_f32_16x16x32_bf16 v[78:81], v[236:239], v[30:33], v[158:161]
	v_mfma_f32_16x16x32_bf16 v[70:73], v[142:145], v[30:33], v[18:21]
	ds_read_b128 v[22:25], v200 offset:45056
	s_waitcnt lgkmcnt(2)
	v_mfma_f32_16x16x32_bf16 v[58:61], v[166:169], v[26:29], v[50:53]
	v_mfma_f32_16x16x32_bf16 v[50:53], v[220:223], v[26:29], v[138:141]
	v_mfma_f32_16x16x32_bf16 v[62:65], v[236:239], v[26:29], v[162:165]
	v_mfma_f32_16x16x32_bf16 v[54:57], v[142:145], v[26:29], v[14:17]
	s_waitcnt lgkmcnt(1)
	v_mfma_f32_16x16x32_bf16 v[42:45], v[166:169], v[2:5], v[146:149]
	ds_read_b128 v[138:141], v200 offset:47104
	v_mfma_f32_16x16x32_bf16 v[34:37], v[220:223], v[2:5], v[212:215]
	v_mfma_f32_16x16x32_bf16 v[46:49], v[236:239], v[2:5], v[216:219]
	v_mfma_f32_16x16x32_bf16 v[38:41], v[142:145], v[2:5], v[10:13]
	s_waitcnt lgkmcnt(1)
	v_mfma_f32_16x16x32_bf16 v[26:29], v[166:169], v[22:25], v[224:227]
	v_mfma_f32_16x16x32_bf16 v[18:21], v[220:223], v[22:25], v[228:231]
.Lst_m1_36:
	s_cbranch_execz .Lst_m1_43
	v_mfma_f32_16x16x32_bf16 v[30:33], v[236:239], v[22:25], v[232:235]
	v_mfma_f32_16x16x32_bf16 v[22:25], v[142:145], v[22:25], v[6:9]
	s_waitcnt lgkmcnt(0)
	v_mfma_f32_16x16x32_bf16 v[10:13], v[166:169], v[138:141], v[240:243]
	v_mfma_f32_16x16x32_bf16 v[2:5], v[220:223], v[138:141], v[134:137]
	v_mfma_f32_16x16x32_bf16 v[14:17], v[236:239], v[138:141], v[130:133]
	v_mfma_f32_16x16x32_bf16 v[6:9], v[142:145], v[138:141], v[154:157]
	s_waitcnt lgkmcnt(0)
	s_barrier
	s_nop 0
	v_mov_b32_e32 v130, 0
	s_and_b64 vcc, exec, s[6:7]
	v_mov_b32_e32 v131, 0
	v_mov_b32_e32 v132, 0
	s_cbranch_vccnz .LBB0_1436
	global_load_dword v130, v[184:185], off
	global_load_dword v131, v[186:187], off
	global_load_dword v132, v[188:189], off

.Lst_m1_37:
	s_cbranch_execz .Lst_m1_44
	v_pk_mul_f32 v[134:135], v[122:123], s[10:11] op_sel_hi:[1,0]
	v_exp_f32_e32 v136, v136
	v_exp_f32_e32 v134, v134
	v_exp_f32_e32 v135, v135
	v_exp_f32_e32 v137, v137
	s_add_u32 s2, s43, s34
	v_add_u32_e32 v133, s36, v133
	v_pk_add_f32 v[134:135], v[134:135], 1.0 op_sel_hi:[1,0]
	v_pk_add_f32 v[136:137], v[136:137], 1.0 op_sel_hi:[1,0]
	v_rcp_f32_e32 v134, v134
	v_rcp_f32_e32 v135, v135
	v_rcp_f32_e32 v136, v136
	v_rcp_f32_e32 v137, v137
	s_addc_u32 s3, s44, s35
	v_pk_mul_f32 v[122:123], v[122:123], v[134:135]
	s_add_i32 s37, s37, 0
	v_pk_mul_f32 v[124:125], v[124:125], v[136:137]
	v_pk_mul_f32 v[122:123], v[126:127], v[122:123]
	v_pk_mul_f32 v[124:125], v[128:129], v[124:125]
	v_pk_mul_f32 v[126:127], v[114:115], s[10:11] op_sel_hi:[1,0]
	v_pk_mul_f32 v[128:129], v[116:117], s[10:11] op_sel_hi:[1,0]
	v_exp_f32_e32 v126, v126
	v_exp_f32_e32 v127, v127
.Lst_m1_38:
	s_cbranch_execz .Lst_m1_45
	v_exp_f32_e32 v128, v128
	v_exp_f32_e32 v129, v129
	v_mul_lo_u32 v133, v133, s57
	v_pk_add_f32 v[126:127], v[126:127], 1.0 op_sel_hi:[1,0]
	v_add3_u32 v133, s37, v138, v133
	v_pk_add_f32 v[128:129], v[128:129], 1.0 op_sel_hi:[1,0]
	v_rcp_f32_e32 v126, v126
	v_rcp_f32_e32 v127, v127
	v_rcp_f32_e32 v128, v128
	v_rcp_f32_e32 v129, v129
	s_lshl_b64 s[6:7], s[28:29], 1
	v_pk_mul_f32 v[114:115], v[114:115], v[126:127]
	s_add_u32 s2, s2, s6
	v_pk_mul_f32 v[116:117], v[116:117], v[128:129]
	v_pk_mul_f32 v[114:115], v[118:119], v[114:115]
	v_pk_mul_f32 v[116:117], v[120:121], v[116:117]
	v_cvt_pk_bf16_f32 v114, v114, v115
	v_cvt_pk_bf16_f32 v115, v116, v117
	v_pk_mul_f32 v[116:117], v[106:107], s[10:11] op_sel_hi:[1,0]
	v_pk_mul_f32 v[118:119], v[108:109], s[10:11] op_sel_hi:[1,0]
.Lst_m1_39:
	s_cbranch_execz .Lst_m1_46
	v_exp_f32_e32 v116, v116
	v_exp_f32_e32 v117, v117
	v_exp_f32_e32 v118, v118
	v_exp_f32_e32 v119, v119
	v_cvt_pk_bf16_f32 v122, v122, v123
	v_pk_add_f32 v[116:117], v[116:117], 1.0 op_sel_hi:[1,0]
	v_cvt_pk_bf16_f32 v123, v124, v125
	v_pk_add_f32 v[118:119], v[118:119], 1.0 op_sel_hi:[1,0]
	v_rcp_f32_e32 v116, v116
	v_rcp_f32_e32 v117, v117
	v_rcp_f32_e32 v118, v118
	v_rcp_f32_e32 v119, v119
	s_addc_u32 s3, s3, s7
	v_pk_mul_f32 v[106:107], v[106:107], v[116:117]
	v_mov_b32_e32 v183, v173
	v_pk_mul_f32 v[108:109], v[108:109], v[118:119]
	v_pk_mul_f32 v[106:107], v[110:111], v[106:107]
	v_pk_mul_f32 v[108:109], v[112:113], v[108:109]
	v_pk_mul_f32 v[110:111], v[98:99], s[10:11] op_sel_hi:[1,0]
	v_pk_mul_f32 v[112:113], v[100:101], s[10:11] op_sel_hi:[1,0]
	v_exp_f32_e32 v110, v110
	v_exp_f32_e32 v111, v111
.Lst_m1_40:
	s_cbranch_execz .Lst_m1_47
	v_exp_f32_e32 v112, v112
	v_exp_f32_e32 v113, v113
	v_cvt_pk_bf16_f32 v106, v106, v107
	v_pk_add_f32 v[110:111], v[110:111], 1.0 op_sel_hi:[1,0]
	v_cvt_pk_bf16_f32 v107, v108, v109
	v_pk_add_f32 v[112:113], v[112:113], 1.0 op_sel_hi:[1,0]
	v_rcp_f32_e32 v110, v110
	v_rcp_f32_e32 v111, v111
	v_rcp_f32_e32 v112, v112
	v_rcp_f32_e32 v113, v113
	ds_write2_b64 v133, v[122:123], v[114:115] offset1:4
	v_pk_mul_f32 v[98:99], v[98:99], v[110:111]
	v_pk_mul_f32 v[100:101], v[100:101], v[112:113]
	v_pk_mul_f32 v[98:99], v[102:103], v[98:99]
	v_pk_mul_f32 v[100:101], v[104:105], v[100:101]
	v_cvt_pk_bf16_f32 v98, v98, v99
	v_cvt_pk_bf16_f32 v99, v100, v101
	v_pk_mul_f32 v[100:101], v[90:91], s[10:11] op_sel_hi:[1,0]
	v_pk_mul_f32 v[102:103], v[92:93], s[10:11] op_sel_hi:[1,0]
.Lst_m1_41:
	s_cbranch_execz .Lst_m1_48
	v_exp_f32_e32 v100, v100
	v_exp_f32_e32 v101, v101
	v_exp_f32_e32 v102, v102
	v_exp_f32_e32 v103, v103
	v_add_u32_e32 v104, 0x1000, v133
	v_pk_add_f32 v[100:101], v[100:101], 1.0 op_sel_hi:[1,0]
	ds_write2_b64 v104, v[106:107], v[98:99] offset0:32 offset1:36
	v_pk_add_f32 v[102:103], v[102:103], 1.0 op_sel_hi:[1,0]
	v_rcp_f32_e32 v100, v100
	v_rcp_f32_e32 v101, v101
	v_rcp_f32_e32 v102, v102
	v_rcp_f32_e32 v103, v103
	v_pk_mul_f32 v[90:91], v[90:91], v[100:101]
	s_nop 0
	v_pk_mul_f32 v[90:91], v[94:95], v[90:91]
	v_pk_mul_f32 v[92:93], v[92:93], v[102:103]
	v_pk_mul_f32 v[94:95], v[82:83], s[10:11] op_sel_hi:[1,0]
	v_pk_mul_f32 v[92:93], v[96:97], v[92:93]
	v_pk_mul_f32 v[96:97], v[84:85], s[10:11] op_sel_hi:[1,0]
	v_exp_f32_e32 v94, v94
	v_exp_f32_e32 v95, v95
	v_exp_f32_e32 v96, v96
.Lst_m1_42:
	s_cbranch_execz .Lst_m1_49
	v_exp_f32_e32 v97, v97
	v_cvt_pk_bf16_f32 v90, v90, v91
	v_pk_add_f32 v[94:95], v[94:95], 1.0 op_sel_hi:[1,0]
	v_cvt_pk_bf16_f32 v91, v92, v93
	v_pk_add_f32 v[96:97], v[96:97], 1.0 op_sel_hi:[1,0]
	v_rcp_f32_e32 v94, v94
	v_rcp_f32_e32 v95, v95
	v_rcp_f32_e32 v96, v96
	v_rcp_f32_e32 v97, v97
	v_pk_mul_f32 v[82:83], v[82:83], v[94:95]
	s_nop 0
	v_pk_mul_f32 v[82:83], v[86:87], v[82:83]
	v_pk_mul_f32 v[84:85], v[84:85], v[96:97]
	v_cvt_pk_bf16_f32 v82, v82, v83
	v_pk_mul_f32 v[84:85], v[88:89], v[84:85]
	v_pk_mul_f32 v[86:87], v[76:77], s[10:11] op_sel_hi:[1,0]
	v_cvt_pk_bf16_f32 v83, v84, v85
	v_pk_mul_f32 v[84:85], v[74:75], s[10:11] op_sel_hi:[1,0]
	v_exp_f32_e32 v86, v86
	v_exp_f32_e32 v84, v84
.Lst_m1_43:
	s_cbranch_execz .Lst_m1_50
	v_exp_f32_e32 v85, v85
	v_exp_f32_e32 v87, v87
	v_add_u32_e32 v88, 0x2000, v133
	ds_write2_b64 v88, v[90:91], v[82:83] offset0:64 offset1:68
	v_pk_add_f32 v[84:85], v[84:85], 1.0 op_sel_hi:[1,0]
	v_pk_add_f32 v[86:87], v[86:87], 1.0 op_sel_hi:[1,0]
	v_rcp_f32_e32 v84, v84
	v_rcp_f32_e32 v85, v85
	v_rcp_f32_e32 v86, v86
	v_rcp_f32_e32 v87, v87
	v_pk_mul_f32 v[74:75], v[74:75], v[84:85]
	s_nop 0
	v_pk_mul_f32 v[74:75], v[78:79], v[74:75]
	v_pk_mul_f32 v[76:77], v[76:77], v[86:87]
	v_pk_mul_f32 v[78:79], v[66:67], s[10:11] op_sel_hi:[1,0]
	v_pk_mul_f32 v[76:77], v[80:81], v[76:77]
	v_pk_mul_f32 v[80:81], v[68:69], s[10:11] op_sel_hi:[1,0]
	v_exp_f32_e32 v78, v78
	v_exp_f32_e32 v79, v79
	v_exp_f32_e32 v80, v80
	v_exp_f32_e32 v81, v81
	v_cvt_pk_bf16_f32 v74, v74, v75
.Lst_m1_44:
	s_cbranch_execz .Lst_m1_51
	v_pk_add_f32 v[78:79], v[78:79], 1.0 op_sel_hi:[1,0]
	v_cvt_pk_bf16_f32 v75, v76, v77
	v_pk_add_f32 v[80:81], v[80:81], 1.0 op_sel_hi:[1,0]
	v_rcp_f32_e32 v78, v78
	v_rcp_f32_e32 v79, v79
	v_rcp_f32_e32 v80, v80
	v_rcp_f32_e32 v81, v81
	v_pk_mul_f32 v[66:67], v[66:67], v[78:79]
	s_nop 0
	v_pk_mul_f32 v[66:67], v[70:71], v[66:67]
	v_pk_mul_f32 v[68:69], v[68:69], v[80:81]
	v_cvt_pk_bf16_f32 v66, v66, v67
	v_pk_mul_f32 v[68:69], v[72:73], v[68:69]
	v_pk_mul_f32 v[70:71], v[60:61], s[10:11] op_sel_hi:[1,0]
	v_cvt_pk_bf16_f32 v67, v68, v69
	v_pk_mul_f32 v[68:69], v[58:59], s[10:11] op_sel_hi:[1,0]
	v_exp_f32_e32 v70, v70
	v_exp_f32_e32 v68, v68
	v_exp_f32_e32 v69, v69
	v_exp_f32_e32 v71, v71
	v_add_u32_e32 v72, 0x3000, v133
.Lst_m1_45:
	s_cbranch_execz .Lst_m1_52
	ds_write2_b64 v72, v[74:75], v[66:67] offset0:96 offset1:100
	v_pk_add_f32 v[68:69], v[68:69], 1.0 op_sel_hi:[1,0]
	v_pk_add_f32 v[70:71], v[70:71], 1.0 op_sel_hi:[1,0]
	v_rcp_f32_e32 v68, v68
	v_rcp_f32_e32 v69, v69
	v_rcp_f32_e32 v70, v70
	v_rcp_f32_e32 v71, v71
	v_pk_mul_f32 v[58:59], v[58:59], v[68:69]
	s_nop 0
	v_pk_mul_f32 v[58:59], v[62:63], v[58:59]
	v_pk_mul_f32 v[60:61], v[60:61], v[70:71]
	v_pk_mul_f32 v[62:63], v[50:51], s[10:11] op_sel_hi:[1,0]
	v_pk_mul_f32 v[60:61], v[64:65], v[60:61]
	v_pk_mul_f32 v[64:65], v[52:53], s[10:11] op_sel_hi:[1,0]
	v_exp_f32_e32 v62, v62
	v_exp_f32_e32 v63, v63
	v_exp_f32_e32 v64, v64
	v_exp_f32_e32 v65, v65
	v_cvt_pk_bf16_f32 v58, v58, v59
	v_pk_add_f32 v[62:63], v[62:63], 1.0 op_sel_hi:[1,0]
	v_cvt_pk_bf16_f32 v59, v60, v61
.Lst_m1_46:
	s_cbranch_execz .Lst_m1_53
	v_pk_add_f32 v[64:65], v[64:65], 1.0 op_sel_hi:[1,0]
	v_rcp_f32_e32 v62, v62
	v_rcp_f32_e32 v63, v63
	v_rcp_f32_e32 v64, v64
	v_rcp_f32_e32 v65, v65
	v_pk_mul_f32 v[50:51], v[50:51], v[62:63]
	s_nop 0
	v_pk_mul_f32 v[50:51], v[54:55], v[50:51]
	v_pk_mul_f32 v[52:53], v[52:53], v[64:65]
	v_cvt_pk_bf16_f32 v50, v50, v51
	v_pk_mul_f32 v[52:53], v[56:57], v[52:53]
	v_pk_mul_f32 v[54:55], v[44:45], s[10:11] op_sel_hi:[1,0]
	v_cvt_pk_bf16_f32 v51, v52, v53
	v_pk_mul_f32 v[52:53], v[42:43], s[10:11] op_sel_hi:[1,0]
	v_exp_f32_e32 v54, v54
	v_exp_f32_e32 v52, v52
	v_exp_f32_e32 v53, v53
	v_exp_f32_e32 v55, v55
	v_add_u32_e32 v56, 0x4000, v133
	ds_write2_b64 v56, v[58:59], v[50:51] offset0:128 offset1:132
	v_pk_add_f32 v[52:53], v[52:53], 1.0 op_sel_hi:[1,0]
.Lst_m1_47:
	s_cbranch_execz .Lst_m1_54
	v_pk_add_f32 v[54:55], v[54:55], 1.0 op_sel_hi:[1,0]
	v_rcp_f32_e32 v52, v52
	v_rcp_f32_e32 v53, v53
	v_rcp_f32_e32 v54, v54
	v_rcp_f32_e32 v55, v55
	v_pk_mul_f32 v[42:43], v[42:43], v[52:53]
	s_nop 0
	v_pk_mul_f32 v[42:43], v[46:47], v[42:43]
	v_pk_mul_f32 v[44:45], v[44:45], v[54:55]
	v_pk_mul_f32 v[46:47], v[34:35], s[10:11] op_sel_hi:[1,0]
	v_pk_mul_f32 v[44:45], v[48:49], v[44:45]
	v_pk_mul_f32 v[48:49], v[36:37], s[10:11] op_sel_hi:[1,0]
	v_exp_f32_e32 v46, v46
	v_exp_f32_e32 v47, v47
	v_exp_f32_e32 v48, v48
	v_exp_f32_e32 v49, v49
	v_cvt_pk_bf16_f32 v42, v42, v43
	v_pk_add_f32 v[46:47], v[46:47], 1.0 op_sel_hi:[1,0]
	v_cvt_pk_bf16_f32 v43, v44, v45
	v_pk_add_f32 v[48:49], v[48:49], 1.0 op_sel_hi:[1,0]
	v_rcp_f32_e32 v46, v46
.Lst_m1_48:
	s_cbranch_execz .Lst_m1_55
	v_rcp_f32_e32 v47, v47
	v_rcp_f32_e32 v48, v48
	v_rcp_f32_e32 v49, v49
	v_pk_mul_f32 v[34:35], v[34:35], v[46:47]
	s_nop 0
	v_pk_mul_f32 v[34:35], v[38:39], v[34:35]
	v_pk_mul_f32 v[36:37], v[36:37], v[48:49]
	v_cvt_pk_bf16_f32 v34, v34, v35
	v_pk_mul_f32 v[36:37], v[40:41], v[36:37]
	v_pk_mul_f32 v[38:39], v[28:29], s[10:11] op_sel_hi:[1,0]
	v_cvt_pk_bf16_f32 v35, v36, v37
	v_pk_mul_f32 v[36:37], v[26:27], s[10:11] op_sel_hi:[1,0]
	v_exp_f32_e32 v38, v38
	v_exp_f32_e32 v36, v36
	v_exp_f32_e32 v37, v37
	v_exp_f32_e32 v39, v39
	v_add_u32_e32 v40, 0x5000, v133
	ds_write2_b64 v40, v[42:43], v[34:35] offset0:160 offset1:164
	v_pk_add_f32 v[36:37], v[36:37], 1.0 op_sel_hi:[1,0]
	v_pk_add_f32 v[38:39], v[38:39], 1.0 op_sel_hi:[1,0]
.Lst_m1_49:
	s_cbranch_execz .Lst_m1_56
	v_rcp_f32_e32 v36, v36
	v_rcp_f32_e32 v37, v37
	v_rcp_f32_e32 v38, v38
	v_rcp_f32_e32 v39, v39
	v_pk_mul_f32 v[26:27], v[26:27], v[36:37]
	s_nop 0
	v_pk_mul_f32 v[26:27], v[30:31], v[26:27]
	v_pk_mul_f32 v[28:29], v[28:29], v[38:39]
	v_pk_mul_f32 v[30:31], v[18:19], s[10:11] op_sel_hi:[1,0]
	v_pk_mul_f32 v[28:29], v[32:33], v[28:29]
	v_pk_mul_f32 v[32:33], v[20:21], s[10:11] op_sel_hi:[1,0]
	v_exp_f32_e32 v30, v30
	v_exp_f32_e32 v31, v31
	v_exp_f32_e32 v32, v32
	v_exp_f32_e32 v33, v33
	v_cvt_pk_bf16_f32 v26, v26, v27
	v_pk_add_f32 v[30:31], v[30:31], 1.0 op_sel_hi:[1,0]
	v_cvt_pk_bf16_f32 v27, v28, v29
	v_pk_add_f32 v[32:33], v[32:33], 1.0 op_sel_hi:[1,0]
	v_rcp_f32_e32 v30, v30
	v_rcp_f32_e32 v31, v31
	v_rcp_f32_e32 v32, v32
.Lst_m1_50:
	s_cbranch_execz .Lst_m1_57
	v_rcp_f32_e32 v33, v33
	v_pk_mul_f32 v[18:19], v[18:19], v[30:31]
	s_nop 0
	v_pk_mul_f32 v[18:19], v[22:23], v[18:19]
	v_pk_mul_f32 v[20:21], v[20:21], v[32:33]
	v_cvt_pk_bf16_f32 v18, v18, v19
	v_pk_mul_f32 v[20:21], v[24:25], v[20:21]
	v_pk_mul_f32 v[22:23], v[12:13], s[10:11] op_sel_hi:[1,0]
	v_cvt_pk_bf16_f32 v19, v20, v21
	v_pk_mul_f32 v[20:21], v[10:11], s[10:11] op_sel_hi:[1,0]
	v_exp_f32_e32 v22, v22
	v_exp_f32_e32 v20, v20
	v_exp_f32_e32 v21, v21
	v_exp_f32_e32 v23, v23
	v_add_u32_e32 v24, 0x6000, v133
	ds_write2_b64 v24, v[26:27], v[18:19] offset0:192 offset1:196
	v_pk_add_f32 v[20:21], v[20:21], 1.0 op_sel_hi:[1,0]
	v_pk_add_f32 v[22:23], v[22:23], 1.0 op_sel_hi:[1,0]
	v_rcp_f32_e32 v20, v20
	v_rcp_f32_e32 v21, v21
.Lst_m1_51:
	s_cbranch_execz .Lst_m1_58
	v_rcp_f32_e32 v22, v22
	v_rcp_f32_e32 v23, v23
	v_pk_mul_f32 v[10:11], v[10:11], v[20:21]
	s_nop 0
	v_pk_mul_f32 v[10:11], v[14:15], v[10:11]
	v_pk_mul_f32 v[12:13], v[12:13], v[22:23]
	v_pk_mul_f32 v[14:15], v[2:3], s[10:11] op_sel_hi:[1,0]
	v_pk_mul_f32 v[12:13], v[16:17], v[12:13]
	v_pk_mul_f32 v[16:17], v[4:5], s[10:11] op_sel_hi:[1,0]
	v_exp_f32_e32 v14, v14
	v_exp_f32_e32 v15, v15
	v_exp_f32_e32 v16, v16
	v_exp_f32_e32 v17, v17
	v_cvt_pk_bf16_f32 v10, v10, v11
	v_pk_add_f32 v[14:15], v[14:15], 1.0 op_sel_hi:[1,0]
	v_cvt_pk_bf16_f32 v11, v12, v13
	v_pk_add_f32 v[16:17], v[16:17], 1.0 op_sel_hi:[1,0]
	v_rcp_f32_e32 v14, v14
	v_rcp_f32_e32 v15, v15
	v_rcp_f32_e32 v16, v16
	v_rcp_f32_e32 v17, v17
	v_pk_mul_f32 v[2:3], v[2:3], v[14:15]
.Lst_m1_52:
	s_cbranch_execz .Lst_m1_59
	s_nop 0
	v_pk_mul_f32 v[2:3], v[6:7], v[2:3]
	v_pk_mul_f32 v[4:5], v[4:5], v[16:17]
	v_cvt_pk_bf16_f32 v2, v2, v3
	v_pk_mul_f32 v[4:5], v[8:9], v[4:5]
	v_lshl_add_u64 v[8:9], s[2:3], 0, v[182:183]
	v_cvt_pk_bf16_f32 v3, v4, v5
	v_add_u32_e32 v4, 0x7000, v133
	ds_write2_b64 v4, v[10:11], v[2:3] offset0:224 offset1:228
	v_lshl_or_b32 v10, s33, 5, v192
	v_lshl_add_u32 v2, v1, 4, 0
	v_mad_u64_u32 v[6:7], s[6:7], v10, s57, v[2:3]
	v_add_u32_e32 v7, s31, v10
	s_waitcnt lgkmcnt(0)
	s_barrier
	v_mad_u64_u32 v[10:11], s[2:3], v7, s58, v[8:9]
	ds_read_b128 v[2:5], v6
	s_waitcnt lgkmcnt(0)
	global_store_dwordx4 v[10:11], v[2:5], off sc1
.Lst_m1_53:
	s_cbranch_execz .Lst_m1_60
	s_nop 1
	v_add_u32_e32 v10, 4, v7
	v_mad_u64_u32 v[10:11], s[2:3], v10, s58, v[8:9]
	ds_read_b128 v[2:5], v6 offset:1088
	s_waitcnt lgkmcnt(0)
	global_store_dwordx4 v[10:11], v[2:5], off sc1
	s_nop 1
	v_add_u32_e32 v10, 8, v7
	v_mad_u64_u32 v[10:11], s[2:3], v10, s58, v[8:9]
	ds_read_b128 v[2:5], v6 offset:2176
	s_waitcnt lgkmcnt(0)
	global_store_dwordx4 v[10:11], v[2:5], off sc1
	s_nop 1
	v_add_u32_e32 v10, 12, v7
	v_mad_u64_u32 v[10:11], s[2:3], v10, s58, v[8:9]
	ds_read_b128 v[2:5], v6 offset:3264
	s_waitcnt lgkmcnt(0)
	global_store_dwordx4 v[10:11], v[2:5], off sc1
	s_nop 1
	v_add_u32_e32 v10, 16, v7
	v_mad_u64_u32 v[10:11], s[2:3], v10, s58, v[8:9]
	ds_read_b128 v[2:5], v6 offset:4352
.Lst_m1_54:
	s_cbranch_execz .Lst_m1_61
	s_waitcnt lgkmcnt(0)
	global_store_dwordx4 v[10:11], v[2:5], off sc1
	s_nop 1
	v_add_u32_e32 v10, 20, v7
	v_mad_u64_u32 v[10:11], s[2:3], v10, s58, v[8:9]
	ds_read_b128 v[2:5], v6 offset:5440
	s_waitcnt lgkmcnt(0)
	global_store_dwordx4 v[10:11], v[2:5], off sc1
	s_nop 1
	v_add_u32_e32 v10, 24, v7
	ds_read_b128 v[2:5], v6 offset:6528
	v_mad_u64_u32 v[10:11], s[2:3], v10, s58, v[8:9]
	s_waitcnt lgkmcnt(0)
	global_store_dwordx4 v[10:11], v[2:5], off sc1
	s_nop 1
	ds_read_b128 v[2:5], v6 offset:7616
	v_add_u32_e32 v6, 28, v7
	v_mad_u64_u32 v[6:7], s[2:3], v6, s58, v[8:9]
	s_waitcnt lgkmcnt(0)
	global_store_dwordx4 v[6:7], v[2:5], off sc1
	s_nop 1
	s_waitcnt lgkmcnt(0)
.Lst_m1_55:
	s_cbranch_execz .Lst_m1_62
	s_barrier
	s_mov_b64 s[2:3], 0
	s_waitcnt vmcnt(0)

.Lst_m1_56:
	s_cbranch_execz .Lst_m1_63
	global_load_dword v3, v[4:5], off
	s_waitcnt vmcnt(0)
	v_lshl_add_u32 v34, v3, 12, v2

.LBB0_1444:
.Lst_m1_57:
	s_cbranch_execz .Lst_m1_64
	v_add_u32_e32 v2, 0xc0, v3
	v_lshrrev_b32_e32 v4, 8, v2
	v_lshl_add_u32 v3, v4, 12, s2
	v_and_or_b32 v2, v2, s51, v3
	v_ashrrev_i32_e32 v3, 31, v2
	v_lshl_add_u64 v[2:3], v[2:3], 2, s[16:17]
	global_load_dword v2, v[2:3], off
	v_lshl_or_b32 v3, v4, 23, v190
	s_waitcnt vmcnt(0)
	v_lshl_add_u32 v37, v2, 12, v3

.Lst_m1_58:
	s_cbranch_execz .Lst_m1_65
	s_or_b32 s36, s3, 0x100
	v_bitop3_b32 v185, s3, v203, v198 bitop3:0xde
	v_bitop3_b32 v181, s36, v203, v198 bitop3:0xde
	s_or_b32 s3, s3, 0x120
	s_lshl_b32 s36, s2, 10
	v_bitop3_b32 v172, s3, v203, v198 bitop3:0xde
	s_add_i32 s36, s36, 0
	s_mov_b32 s3, m0
	s_mov_b32 m0, s36
	s_nop 0
	global_load_lds_dwordx4 v34, s[18:19]
	s_mov_b32 m0, s3
	s_add_i32 s3, s36, 0x2000
	s_mov_b32 s37, m0
	s_mov_b32 m0, s3
	s_nop 0
	global_load_lds_dwordx4 v35, s[18:19]
	s_mov_b32 m0, s37
	s_add_i32 s3, s36, 0x4000
	s_mov_b32 s37, m0
	s_mov_b32 m0, s3
	s_nop 0
	global_load_lds_dwordx4 v36, s[18:19]
.Lst_m1_59:
	s_cbranch_execz .Lst_m1_66
	s_mov_b32 m0, s37
	s_add_i32 s3, s36, 0x6000
	v_lshlrev_b32_e32 v2, 9, v2
	v_lshlrev_b32_e32 v3, 5, v3
	s_mov_b32 s37, m0
	s_mov_b32 m0, s3
	s_nop 0
	global_load_lds_dwordx4 v37, s[18:19]
	s_mov_b32 m0, s37
	s_mul_i32 s3, s2, 0x5800
	v_bitop3_b32 v188, v3, v2, v194 bitop3:0xde
	v_or_b32_e32 v2, s83, v1
	s_mul_hi_u32 s37, s40, 0x2c00
	s_add_u32 s38, s59, s3
	s_waitcnt vmcnt(1)
	v_lshlrev_b32_e32 v38, 7, v2
	s_addc_u32 s39, s73, s37
	global_load_dwordx4 v[2:5], v199, s[38:39]
	s_add_i32 s38, s40, 16
	s_add_i32 s41, s3, 0x2c000
	s_mul_hi_u32 s84, s38, 0x2c00
	s_add_u32 s38, s59, s41
	s_addc_u32 s39, s73, s84
	global_load_dwordx4 v[6:9], v199, s[38:39]
.Lst_m1_60:
	s_cbranch_execz .Lst_m1_67
	s_add_i32 s38, s40, 32
	s_add_i32 s85, s3, 0x58000
	s_mul_hi_u32 s86, s38, 0x2c00
	s_add_u32 s38, s59, s85
	s_addc_u32 s39, s73, s86
	global_load_dwordx4 v[10:13], v199, s[38:39]
	s_add_i32 s38, s40, 48
	s_add_i32 s87, s3, 0x84000
	s_mul_hi_u32 s88, s38, 0x2c00
	s_add_u32 s38, s59, s87
	s_addc_u32 s39, s73, s88
	global_load_dwordx4 v[14:17], v199, s[38:39]
	s_add_u32 s38, s74, s3
	s_addc_u32 s39, s75, s37
	global_load_dwordx4 v[18:21], v199, s[38:39]
	s_add_u32 s38, s74, s41
	s_addc_u32 s39, s75, s84
	global_load_dwordx4 v[22:25], v199, s[38:39]
	s_add_u32 s38, s74, s85
	s_addc_u32 s39, s75, s86
	global_load_dwordx4 v[26:29], v199, s[38:39]
	s_add_u32 s38, s74, s87
	s_addc_u32 s39, s75, s88
.Lst_m1_61:
	s_cbranch_execz .Lst_m1_68
	global_load_dwordx4 v[30:33], v199, s[38:39]
	s_add_i32 s38, s36, 0x8000
	v_add_u32_e32 v39, 0x80, v34
	s_mov_b32 s39, m0
	s_mov_b32 m0, s38
	s_nop 0
	global_load_lds_dwordx4 v39, s[18:19]
	s_mov_b32 m0, s39
	v_add_u32_e32 v39, 0x80, v35
	s_add_i32 s38, s36, 0xa000
	s_mov_b32 s39, m0
	s_mov_b32 m0, s38
	s_nop 0
	global_load_lds_dwordx4 v39, s[18:19]
	s_mov_b32 m0, s39
	v_add_u32_e32 v39, 0x80, v36
	s_add_i32 s38, s36, 0xc000
	s_mov_b32 s39, m0
	s_mov_b32 m0, s38
	s_nop 0
	global_load_lds_dwordx4 v39, s[18:19]
	s_mov_b32 m0, s39
.Lst_m1_62:
	s_cbranch_execz .Lst_m1_69
	v_add_u32_e32 v39, 0x80, v37
	s_add_i32 s38, s36, 0xe000
	s_mov_b32 s39, m0
	s_mov_b32 m0, s38
	s_nop 0
	global_load_lds_dwordx4 v39, s[18:19]
	s_mov_b32 m0, s39
	s_waitcnt vmcnt(4)
	v_add_u32_e32 v189, s52, v188
	v_cvt_pk_bf16_f32 v2, v2, v3
	v_cvt_pk_bf16_f32 v3, v4, v5
	v_cvt_pk_bf16_f32 v4, v6, v7
	v_cvt_pk_bf16_f32 v5, v8, v9
	v_or_b32_e32 v186, 0x100, v188
	ds_write2st64_b64 v189, v[2:3], v[4:5] offset1:16
	v_cvt_pk_bf16_f32 v2, v10, v11
	v_cvt_pk_bf16_f32 v3, v12, v13
	v_cvt_pk_bf16_f32 v4, v14, v15
	v_cvt_pk_bf16_f32 v5, v16, v17
.Lst_m1_63:
	s_cbranch_execz .Lst_m1_70
	ds_write2st64_b64 v189, v[2:3], v[4:5] offset0:32 offset1:48
	v_cvt_pk_bf16_f32 v2, v18, v19
	v_cvt_pk_bf16_f32 v3, v20, v21
	v_add_u32_e32 v6, s52, v186
	v_cvt_pk_bf16_f32 v4, v22, v23
	v_cvt_pk_bf16_f32 v5, v24, v25
	s_add_i32 s38, s40, 64
	s_add_i32 s41, s3, 0xb0000
	ds_write2st64_b64 v6, v[2:3], v[4:5] offset1:16
	v_cvt_pk_bf16_f32 v2, v26, v27
	v_cvt_pk_bf16_f32 v3, v28, v29
	v_cvt_pk_bf16_f32 v4, v30, v31
	v_cvt_pk_bf16_f32 v5, v32, v33
	s_mul_hi_u32 s84, s38, 0x2c00
	s_add_u32 s38, s59, s41
	ds_write2st64_b64 v6, v[2:3], v[4:5] offset0:32 offset1:48
	s_addc_u32 s39, s73, s84
	global_load_dwordx4 v[30:33], v199, s[38:39]
.Lst_m1_64:
	s_cbranch_execz .Lsc_join_m1
	s_add_i32 s38, s40, 0x50
	s_add_i32 s85, s3, 0xdc000
	s_mul_hi_u32 s86, s38, 0x2c00
	s_add_u32 s38, s59, s85
	s_addc_u32 s39, s73, s86
	global_load_dwordx4 v[26:29], v199, s[38:39]
	s_add_i32 s38, s40, 0x60
	s_add_i32 s87, s3, 0x108000
	s_mul_hi_u32 s88, s38, 0x2c00
	s_add_u32 s38, s59, s87
	s_addc_u32 s39, s73, s88
	s_addk_i32 s40, 0x70
	s_add_i32 s89, s3, 0x134000
	global_load_dwordx4 v[22:25], v199, s[38:39]
	s_mul_hi_u32 s40, s40, 0x2c00
	s_add_u32 s38, s59, s89
	s_addc_u32 s39, s73, s40
	global_load_dwordx4 v[18:21], v199, s[38:39]
	s_add_u32 s38, s74, s41
	s_addc_u32 s39, s75, s84
	global_load_dwordx4 v[14:17], v199, s[38:39]
.Lst_m1_65:
	s_cbranch_execz .Lsc_join_m1
	s_add_u32 s38, s74, s85
	s_addc_u32 s39, s75, s86
	global_load_dwordx4 v[10:13], v199, s[38:39]
	s_add_u32 s38, s74, s87
	s_addc_u32 s39, s75, s88
	global_load_dwordx4 v[6:9], v199, s[38:39]
	s_add_u32 s38, s74, s89
	s_addc_u32 s39, s75, s40
	global_load_dwordx4 v[2:5], v199, s[38:39]
	s_mul_hi_u32 s2, s2, 0x5800
	s_add_u32 s38, s74, s3
	s_waitcnt lgkmcnt(0)
	s_barrier
	s_addc_u32 s39, s75, s2
	s_add_u32 s40, s59, s3
	v_add_u32_e32 v215, 0x100, v34
	v_mov_b32_e32 v34, 0
	v_or_b32_e32 v183, v38, v196
	s_mov_b32 s37, 0x8000
	v_or_b32_e32 v187, v38, v197
	s_addc_u32 s41, s73, s2
	v_add_u32_e32 v212, 0x100, v37
	v_add_u32_e32 v213, 0x100, v36
	v_add_u32_e32 v214, 0x100, v35
.Lst_m1_66:
	s_cbranch_execz .Lsc_join_m1
	s_mov_b32 s84, 0x10000
	s_mov_b32 s85, 0
	s_mov_b64 s[2:3], 0
	v_mov_b32_e32 v35, v34
	v_mov_b32_e32 v36, v34
	v_mov_b32_e32 v37, v34
	v_mov_b32_e32 v38, v34
	v_mov_b32_e32 v39, v34
	v_mov_b32_e32 v40, v34
	v_mov_b32_e32 v41, v34
	v_mov_b32_e32 v46, v34
	v_mov_b32_e32 v47, v34
	v_mov_b32_e32 v48, v34
	v_mov_b32_e32 v49, v34
	v_mov_b32_e32 v50, v34
	v_mov_b32_e32 v51, v34
	v_mov_b32_e32 v52, v34
	v_mov_b32_e32 v53, v34
	s_waitcnt vmcnt(0)
	v_mov_b32_e32 v42, v34
	v_mov_b32_e32 v43, v34
	v_mov_b32_e32 v44, v34
	v_mov_b32_e32 v45, v34
	v_mov_b32_e32 v54, v34
	v_mov_b32_e32 v55, v34
	v_mov_b32_e32 v56, v34
	v_mov_b32_e32 v57, v34
	v_mov_b32_e32 v58, v34
	v_mov_b32_e32 v59, v34
	v_mov_b32_e32 v60, v34
	v_mov_b32_e32 v61, v34
.Lst_m1_67:
	s_cbranch_execz .Lsc_join_m1
	v_mov_b32_e32 v62, v34
	v_mov_b32_e32 v63, v34
	v_mov_b32_e32 v64, v34
	v_mov_b32_e32 v65, v34
	v_mov_b32_e32 v66, v34
	v_mov_b32_e32 v67, v34
	v_mov_b32_e32 v68, v34
	v_mov_b32_e32 v69, v34
	v_mov_b32_e32 v70, v34
	v_mov_b32_e32 v71, v34
	v_mov_b32_e32 v72, v34
	v_mov_b32_e32 v73, v34
	v_mov_b32_e32 v74, v34
	v_mov_b32_e32 v75, v34
	v_mov_b32_e32 v76, v34
	v_mov_b32_e32 v77, v34
	v_mov_b32_e32 v78, v34
	v_mov_b32_e32 v79, v34
	v_mov_b32_e32 v80, v34
	v_mov_b32_e32 v81, v34
	v_mov_b32_e32 v82, v34
	v_mov_b32_e32 v83, v34
	v_mov_b32_e32 v84, v34
	v_mov_b32_e32 v85, v34
	v_mov_b32_e32 v86, v34
	v_mov_b32_e32 v87, v34
	v_mov_b32_e32 v88, v34
	v_mov_b32_e32 v89, v34
	v_mov_b32_e32 v90, v34
	v_mov_b32_e32 v91, v34
	v_mov_b32_e32 v92, v34
	v_mov_b32_e32 v93, v34
.Lst_m1_68:
	s_cbranch_execz .Lsc_join_m1
	v_mov_b32_e32 v94, v34
	v_mov_b32_e32 v95, v34
	v_mov_b32_e32 v96, v34
	v_mov_b32_e32 v97, v34
	v_mov_b32_e32 v98, v34
	v_mov_b32_e32 v99, v34
	v_mov_b32_e32 v100, v34
	v_mov_b32_e32 v101, v34
	v_mov_b32_e32 v102, v34
	v_mov_b32_e32 v103, v34
	v_mov_b32_e32 v104, v34
	v_mov_b32_e32 v105, v34
	v_mov_b32_e32 v106, v34
	v_mov_b32_e32 v107, v34
	v_mov_b32_e32 v108, v34
	v_mov_b32_e32 v109, v34
	v_mov_b32_e32 v110, v34
	v_mov_b32_e32 v111, v34
	v_mov_b32_e32 v112, v34
	v_mov_b32_e32 v113, v34
	v_mov_b32_e32 v114, v34
	v_mov_b32_e32 v115, v34
	v_mov_b32_e32 v116, v34
	v_mov_b32_e32 v117, v34
	v_mov_b32_e32 v118, v34
	v_mov_b32_e32 v119, v34
	v_mov_b32_e32 v120, v34
	v_mov_b32_e32 v121, v34
	v_mov_b32_e32 v122, v34
	v_mov_b32_e32 v123, v34
	v_mov_b32_e32 v124, v34
	v_mov_b32_e32 v125, v34
.Lst_m1_69:
	s_cbranch_execz .Lsc_join_m1
	v_mov_b32_e32 v126, v34
	v_mov_b32_e32 v127, v34
	v_mov_b32_e32 v128, v34
	v_mov_b32_e32 v129, v34
	v_mov_b32_e32 v130, v34
	v_mov_b32_e32 v131, v34
	v_mov_b32_e32 v132, v34
	v_mov_b32_e32 v133, v34
	v_mov_b32_e32 v134, v34
	v_mov_b32_e32 v135, v34
	v_mov_b32_e32 v136, v34
	v_mov_b32_e32 v137, v34
	v_mov_b32_e32 v138, v34
	v_mov_b32_e32 v139, v34
	v_mov_b32_e32 v140, v34
	v_mov_b32_e32 v141, v34
	v_mov_b32_e32 v142, v34
	v_mov_b32_e32 v143, v34
	v_mov_b32_e32 v144, v34
	v_mov_b32_e32 v145, v34
	v_mov_b32_e32 v146, v34
	v_mov_b32_e32 v147, v34
	v_mov_b32_e32 v148, v34
	v_mov_b32_e32 v149, v34
	v_mov_b32_e32 v150, v34
	v_mov_b32_e32 v151, v34
	v_mov_b32_e32 v152, v34
	v_mov_b32_e32 v153, v34
	v_mov_b32_e32 v154, v34
	v_mov_b32_e32 v155, v34
	v_mov_b32_e32 v156, v34
	v_mov_b32_e32 v157, v34
.Lst_m1_70:
	s_cbranch_execz .Lsc_join_m1
	v_mov_b32_e32 v158, v34
	v_mov_b32_e32 v159, v34
	v_mov_b32_e32 v160, v34
	v_mov_b32_e32 v161, v34

.LBB0_1533:
.Lst_m2_0:
	s_cbranch_execz .Lst_m2_7
	s_waitcnt vmcnt(0)
	s_cmp_lt_i32 s92, 13
	s_cselect_b64 s[0:1], -1, 0
	s_and_b64 s[2:3], s[0:1], s[2:3]
	s_andn2_b64 vcc, exec, s[2:3]
	s_cbranch_vccnz .LBB0_1544
	s_and_b32 s3, s96, 7
	s_ashr_i32 s4, s72, 3
	s_mul_i32 s3, s3, s4
	s_ashr_i32 s4, s96, 3
	s_and_b32 s2, s72, 7
	s_add_i32 s4, s4, s3
	s_cmp_eq_u32 s2, 0
	s_cselect_b32 s18, s4, s96
	s_cmpk_gt_i32 s18, 0x1ff
	s_mov_b32 s3, 0
	s_cbranch_scc1 .LBB0_1543
	s_waitcnt vmcnt(23)
	v_lshrrev_b32_e32 v3, 4, v0
	v_xor_b32_e32 v2, v3, v0
	v_lshlrev_b32_e32 v2, 3, v2
	v_and_b32_e32 v177, 56, v2
	v_lshrrev_b32_e32 v193, 4, v170
	v_lshrrev_b32_e32 v195, 1, v0
	v_bfe_u32 v2, v0, 1, 3
	v_bitop3_b32 v4, v193, v195, 7 bitop3:0x78
	v_bitop3_b32 v2, v193, v2, 4 bitop3:0x36
	s_add_u32 s19, s70, 0x14158000
	v_lshlrev_b32_e32 v196, 4, v4
.Lst_m2_1:
	s_cbranch_execz .Lst_m2_8
	v_lshlrev_b32_e32 v197, 4, v2
	v_bfe_u32 v2, v0, 2, 2
	v_lshrrev_b32_e32 v4, 2, v170
	s_addc_u32 s20, s71, 0
	v_and_or_b32 v4, v4, 4, v2
	s_waitcnt vmcnt(7)
	v_lshlrev_b32_e32 v7, 9, v2
	v_lshlrev_b32_e32 v2, 3, v0
	s_add_u32 s21, s70, 0x19958000
	v_lshlrev_b32_e32 v5, 12, v193
	v_and_b32_e32 v8, 24, v2
	v_and_b32_e32 v9, 31, v0
	s_addc_u32 s22, s71, 0
	v_lshlrev_b32_e32 v6, 6, v0
	s_waitcnt vmcnt(6)
	v_lshlrev_b32_e32 v10, 11, v0
	v_lshlrev_b32_e32 v198, 5, v4
	v_lshlrev_b32_e32 v2, 3, v9
	v_mov_b32_e32 v173, 0
	s_add_u32 s4, s70, 0x140c8000
	v_and_b32_e32 v4, 64, v6
	v_and_b32_e32 v172, 0xfe000, v10
	v_and_b32_e32 v6, 0xc0, v6
	v_or3_b32 v201, v5, v7, v8
	v_bitop3_b32 v3, v3, 7, v0 bitop3:0x48
.Lst_m2_2:
	s_cbranch_execz .Lst_m2_9
	v_mov_b32_e32 v5, 0x108100
	v_and_b32_e32 v1, 15, v0
	v_lshrrev_b32_e32 v171, 3, v0
	v_or_b32_e32 v190, 0x2c000, v177
	v_or_b32_e32 v191, 0x58000, v177
	v_or_b32_e32 v192, 0x84000, v177
	v_lshlrev_b32_e32 v194, 3, v170
	v_lshlrev_b32_e32 v199, 4, v170
	v_lshrrev_b32_e32 v200, 5, v170
	s_addc_u32 s5, s71, 0
	v_lshl_add_u64 v[174:175], s[64:65], 0, v[172:173]
	v_lshl_add_u32 v176, v9, 4, 0
	v_lshl_or_b32 v202, v3, 4, v5
	v_lshlrev_b32_e32 v178, 1, v4
	v_lshlrev_b32_e32 v180, 2, v6
	s_mov_b64 s[6:7], 0x80
	v_mov_b32_e32 v203, 0x60
	s_movk_i32 s23, 0x80
	s_add_i32 s24, 0, 0x18000
	s_add_i32 s25, 0, 0x20000
	s_mov_b32 s26, 0x6050400
.Lst_m2_3:
	s_cbranch_execz .Lst_m2_10
	s_movk_i32 s27, 0x210
	v_lshlrev_b32_e32 v182, 1, v2
	v_mov_b32_e32 v204, 0x1600000
	s_mov_b32 s16, s18
	s_mov_b32 s28, 0
	s_branch .LBB0_1537

.Lst_m2_4:
	s_cbranch_execz .Lst_m2_11
	v_ashrrev_i32_e32 v139, 31, v138
	v_lshl_add_u64 v[138:139], v[138:139], 2, s[4:5]
	v_add_u32_e32 v137, 32, v135
	global_load_dword v138, v[138:139], off
	v_lshrrev_b32_e32 v139, 4, v137
	v_and_b32_e32 v139, 0xfffff0, v139
	v_add_u32_e32 v132, s35, v132
	v_add_u32_e32 v139, s10, v139
	v_lshlrev_b32_e32 v130, 3, v130
	v_perm_b32 v140, v139, v137, s26
	v_mul_lo_u32 v132, v132, s27
	v_add_u32_e32 v137, 48, v135
	v_add3_u32 v152, s34, v130, v132
	v_lshrrev_b32_e32 v130, 4, v137
	v_and_b32_e32 v130, 0xfffff0, v130
	v_add_u32_e32 v130, s10, v130
	v_perm_b32 v142, v130, v137, s26
	v_ashrrev_i32_e32 v141, 31, v140
	v_ashrrev_i32_e32 v143, 31, v142
	v_lshl_add_u64 v[140:141], v[140:141], 2, s[4:5]
	v_lshl_add_u64 v[142:143], v[142:143], 2, s[4:5]
	global_load_dword v140, v[140:141], off
.Lst_m2_5:
	s_cbranch_execz .Lst_m2_12
	v_add_u32_e32 v139, 64, v135
	global_load_dword v142, v[142:143], off
	v_add_u32_e32 v141, 0x50, v135
	v_add_u32_e32 v145, 0x60, v135
	v_add_u32_e32 v135, 0x70, v135
	v_lshrrev_b32_e32 v132, 4, v139
	v_lshrrev_b32_e32 v144, 4, v141
	v_lshrrev_b32_e32 v146, 4, v145
	v_lshrrev_b32_e32 v147, 4, v135
	v_and_b32_e32 v132, 0xfffff0, v132
	v_and_b32_e32 v130, 0xfffff0, v144
	v_and_b32_e32 v137, 0xfffff0, v146
	v_and_b32_e32 v143, 0xfffff0, v147
	v_add_u32_e32 v132, s10, v132
	v_add_u32_e32 v130, s10, v130
	v_add_u32_e32 v137, s10, v137
	v_add_u32_e32 v143, s10, v143
	v_perm_b32 v144, v132, v139, s26
	v_perm_b32 v146, v130, v141, s26
	v_perm_b32 v148, v137, v145, s26
	v_perm_b32 v150, v143, v135, s26
.Lst_m2_6:
	s_cbranch_execz .Lst_m2_13
	v_ashrrev_i32_e32 v145, 31, v144
	v_ashrrev_i32_e32 v147, 31, v146
	v_ashrrev_i32_e32 v149, 31, v148
	v_ashrrev_i32_e32 v151, 31, v150
	v_lshl_add_u64 v[144:145], v[144:145], 2, s[4:5]
	v_lshl_add_u64 v[146:147], v[146:147], 2, s[4:5]
	v_lshl_add_u64 v[148:149], v[148:149], 2, s[4:5]
	global_load_dword v144, v[144:145], off
	v_lshl_add_u64 v[150:151], v[150:151], 2, s[4:5]
	global_load_dword v146, v[146:147], off
	s_nop 0
	global_load_dword v132, v[148:149], off
	global_load_dword v130, v[150:151], off
	s_lshl_b32 s2, s30, 1
	v_mov_b32_e32 v183, v173
	s_andn2_b64 vcc, exec, s[8:9]
	s_mov_b32 s16, s29
	s_waitcnt vmcnt(7)
	v_pk_mul_f32 v[126:127], v[126:127], v[136:137] op_sel_hi:[1,0]
	v_pk_mul_f32 v[128:129], v[128:129], v[136:137] op_sel_hi:[1,0]
	v_pk_mul_f32 v[122:123], v[122:123], v[136:137] op_sel_hi:[1,0]
.Lst_m2_7:
	s_cbranch_execz .Lst_m2_14
	v_pk_mul_f32 v[124:125], v[124:125], v[136:137] op_sel_hi:[1,0]
	v_pk_mul_f32 v[118:119], v[118:119], v[136:137] op_sel_hi:[1,0]
	v_pk_mul_f32 v[120:121], v[120:121], v[136:137] op_sel_hi:[1,0]
	v_pk_mul_f32 v[114:115], v[114:115], v[136:137] op_sel_hi:[1,0]
	v_pk_mul_f32 v[116:117], v[116:117], v[136:137] op_sel_hi:[1,0]
	v_cvt_pk_bf16_f32 v126, v126, v127
	v_cvt_pk_bf16_f32 v127, v128, v129
	v_cvt_pk_bf16_f32 v122, v122, v123
	v_cvt_pk_bf16_f32 v123, v124, v125
	v_cvt_pk_bf16_f32 v118, v118, v119
	v_cvt_pk_bf16_f32 v119, v120, v121
	v_cvt_pk_bf16_f32 v114, v114, v115
	v_cvt_pk_bf16_f32 v115, v116, v117
	ds_write2_b64 v152, v[126:127], v[122:123] offset1:4
	ds_write2_b64 v152, v[118:119], v[114:115] offset0:8 offset1:12
	s_waitcnt vmcnt(6)
	v_pk_mul_f32 v[110:111], v[110:111], v[138:139] op_sel_hi:[1,0]
.Lst_m2_8:
	s_cbranch_execz .Lst_m2_15
	v_pk_mul_f32 v[112:113], v[112:113], v[138:139] op_sel_hi:[1,0]
	v_pk_mul_f32 v[106:107], v[106:107], v[138:139] op_sel_hi:[1,0]
	v_pk_mul_f32 v[108:109], v[108:109], v[138:139] op_sel_hi:[1,0]
	v_pk_mul_f32 v[102:103], v[102:103], v[138:139] op_sel_hi:[1,0]
	v_pk_mul_f32 v[104:105], v[104:105], v[138:139] op_sel_hi:[1,0]
	v_pk_mul_f32 v[98:99], v[98:99], v[138:139] op_sel_hi:[1,0]
	v_pk_mul_f32 v[100:101], v[100:101], v[138:139] op_sel_hi:[1,0]
	v_cvt_pk_bf16_f32 v110, v110, v111
	v_cvt_pk_bf16_f32 v111, v112, v113
	s_waitcnt vmcnt(5)
	v_pk_mul_f32 v[94:95], v[94:95], v[140:141] op_sel_hi:[1,0]
	v_pk_mul_f32 v[96:97], v[96:97], v[140:141] op_sel_hi:[1,0]
	v_pk_mul_f32 v[90:91], v[90:91], v[140:141] op_sel_hi:[1,0]
	v_pk_mul_f32 v[92:93], v[92:93], v[140:141] op_sel_hi:[1,0]
	v_pk_mul_f32 v[86:87], v[86:87], v[140:141] op_sel_hi:[1,0]
	v_pk_mul_f32 v[88:89], v[88:89], v[140:141] op_sel_hi:[1,0]
	v_pk_mul_f32 v[82:83], v[82:83], v[140:141] op_sel_hi:[1,0]
.Lst_m2_9:
	s_cbranch_execz .Lst_m2_16
	v_pk_mul_f32 v[84:85], v[84:85], v[140:141] op_sel_hi:[1,0]
	s_waitcnt vmcnt(4)
	v_pk_mul_f32 v[78:79], v[78:79], v[142:143] op_sel_hi:[1,0]
	v_pk_mul_f32 v[80:81], v[80:81], v[142:143] op_sel_hi:[1,0]
	v_pk_mul_f32 v[74:75], v[74:75], v[142:143] op_sel_hi:[1,0]
	v_pk_mul_f32 v[76:77], v[76:77], v[142:143] op_sel_hi:[1,0]
	v_pk_mul_f32 v[70:71], v[70:71], v[142:143] op_sel_hi:[1,0]
	v_pk_mul_f32 v[72:73], v[72:73], v[142:143] op_sel_hi:[1,0]
	v_pk_mul_f32 v[66:67], v[66:67], v[142:143] op_sel_hi:[1,0]
	v_pk_mul_f32 v[68:69], v[68:69], v[142:143] op_sel_hi:[1,0]
	v_cvt_pk_bf16_f32 v106, v106, v107
	v_cvt_pk_bf16_f32 v107, v108, v109
	v_add_u32_e32 v108, 0x2000, v152
	v_cvt_pk_bf16_f32 v102, v102, v103
	v_cvt_pk_bf16_f32 v103, v104, v105
	v_cvt_pk_bf16_f32 v98, v98, v99
	v_cvt_pk_bf16_f32 v99, v100, v101
.Lst_m2_10:
	s_cbranch_execz .Lst_m2_17
	v_cvt_pk_bf16_f32 v94, v94, v95
	v_cvt_pk_bf16_f32 v95, v96, v97
	v_cvt_pk_bf16_f32 v90, v90, v91
	v_cvt_pk_bf16_f32 v91, v92, v93
	v_add_u32_e32 v92, 0x4000, v152
	v_cvt_pk_bf16_f32 v86, v86, v87
	s_waitcnt vmcnt(3)
	v_pk_mul_f32 v[62:63], v[62:63], v[144:145] op_sel_hi:[1,0]
	v_pk_mul_f32 v[64:65], v[64:65], v[144:145] op_sel_hi:[1,0]
	s_waitcnt vmcnt(0)
	v_pk_mul_f32 v[6:7], v[6:7], v[130:131] op_sel_hi:[1,0]
	v_pk_mul_f32 v[8:9], v[8:9], v[130:131] op_sel_hi:[1,0]
	v_pk_mul_f32 v[10:11], v[10:11], v[130:131] op_sel_hi:[1,0]
	v_pk_mul_f32 v[12:13], v[12:13], v[130:131] op_sel_hi:[1,0]
	v_cvt_pk_bf16_f32 v6, v6, v7
	v_cvt_pk_bf16_f32 v7, v8, v9
	v_pk_mul_f32 v[2:3], v[2:3], v[130:131] op_sel_hi:[1,0]
.Lst_m2_11:
	s_cbranch_execz .Lst_m2_18
	v_pk_mul_f32 v[4:5], v[4:5], v[130:131] op_sel_hi:[1,0]
	v_or_b32_e32 v8, s33, v200
	v_cvt_pk_bf16_f32 v10, v10, v11
	v_cvt_pk_bf16_f32 v11, v12, v13
	v_add_u32_e32 v12, 0xe000, v152
	v_cvt_pk_bf16_f32 v2, v2, v3
	v_cvt_pk_bf16_f32 v3, v4, v5
	v_add_u32_e32 v172, s31, v8
	v_pk_mul_f32 v[58:59], v[58:59], v[144:145] op_sel_hi:[1,0]
	v_pk_mul_f32 v[60:61], v[60:61], v[144:145] op_sel_hi:[1,0]
	v_pk_mul_f32 v[54:55], v[54:55], v[144:145] op_sel_hi:[1,0]
	v_pk_mul_f32 v[56:57], v[56:57], v[144:145] op_sel_hi:[1,0]
	v_pk_mul_f32 v[50:51], v[50:51], v[144:145] op_sel_hi:[1,0]
	v_pk_mul_f32 v[52:53], v[52:53], v[144:145] op_sel_hi:[1,0]
	v_pk_mul_f32 v[46:47], v[46:47], v[146:147] op_sel_hi:[1,0]
	v_pk_mul_f32 v[48:49], v[48:49], v[146:147] op_sel_hi:[1,0]
	v_pk_mul_f32 v[42:43], v[42:43], v[146:147] op_sel_hi:[1,0]
.Lst_m2_12:
	s_cbranch_execz .Lst_m2_19
	v_pk_mul_f32 v[44:45], v[44:45], v[146:147] op_sel_hi:[1,0]
	v_pk_mul_f32 v[38:39], v[38:39], v[146:147] op_sel_hi:[1,0]
	v_pk_mul_f32 v[40:41], v[40:41], v[146:147] op_sel_hi:[1,0]
	v_pk_mul_f32 v[34:35], v[34:35], v[146:147] op_sel_hi:[1,0]
	v_pk_mul_f32 v[36:37], v[36:37], v[146:147] op_sel_hi:[1,0]
	v_pk_mul_f32 v[30:31], v[30:31], v[132:133] op_sel_hi:[1,0]
	v_pk_mul_f32 v[32:33], v[32:33], v[132:133] op_sel_hi:[1,0]
	v_pk_mul_f32 v[26:27], v[26:27], v[132:133] op_sel_hi:[1,0]
	v_pk_mul_f32 v[28:29], v[28:29], v[132:133] op_sel_hi:[1,0]
	v_pk_mul_f32 v[22:23], v[22:23], v[132:133] op_sel_hi:[1,0]
	v_pk_mul_f32 v[24:25], v[24:25], v[132:133] op_sel_hi:[1,0]
	v_pk_mul_f32 v[18:19], v[18:19], v[132:133] op_sel_hi:[1,0]
	v_pk_mul_f32 v[20:21], v[20:21], v[132:133] op_sel_hi:[1,0]
	v_pk_mul_f32 v[14:15], v[14:15], v[130:131] op_sel_hi:[1,0]
	v_pk_mul_f32 v[16:17], v[16:17], v[130:131] op_sel_hi:[1,0]
	ds_write2_b64 v12, v[6:7], v[2:3] offset0:232 offset1:236
.Lst_m2_13:
	s_cbranch_execz .Lst_m2_20
	v_mad_u64_u32 v[6:7], s[10:11], v8, s27, v[176:177]
	v_lshlrev_b64 v[8:9], 12, v[172:173]
	v_cvt_pk_bf16_f32 v87, v88, v89
	v_cvt_pk_bf16_f32 v82, v82, v83
	v_cvt_pk_bf16_f32 v83, v84, v85
	v_cvt_pk_bf16_f32 v78, v78, v79
	v_cvt_pk_bf16_f32 v79, v80, v81
	v_cvt_pk_bf16_f32 v74, v74, v75
	v_cvt_pk_bf16_f32 v75, v76, v77
	v_add_u32_e32 v76, 0x6000, v152
	v_cvt_pk_bf16_f32 v70, v70, v71
	v_cvt_pk_bf16_f32 v71, v72, v73
	v_cvt_pk_bf16_f32 v66, v66, v67
	v_cvt_pk_bf16_f32 v67, v68, v69
	v_cvt_pk_bf16_f32 v62, v62, v63
	v_cvt_pk_bf16_f32 v63, v64, v65
.Lst_m2_14:
	s_cbranch_execz .Lst_m2_21
	v_cvt_pk_bf16_f32 v58, v58, v59
	v_cvt_pk_bf16_f32 v59, v60, v61
	v_add_u32_e32 v60, 0x8000, v152
	v_cvt_pk_bf16_f32 v54, v54, v55
	v_cvt_pk_bf16_f32 v55, v56, v57
	v_cvt_pk_bf16_f32 v50, v50, v51
	v_cvt_pk_bf16_f32 v51, v52, v53
	v_cvt_pk_bf16_f32 v46, v46, v47
	v_cvt_pk_bf16_f32 v47, v48, v49
	v_cvt_pk_bf16_f32 v42, v42, v43
	v_cvt_pk_bf16_f32 v43, v44, v45
	v_add_u32_e32 v44, 0xa000, v152
	v_cvt_pk_bf16_f32 v38, v38, v39
	v_cvt_pk_bf16_f32 v39, v40, v41
	v_cvt_pk_bf16_f32 v34, v34, v35
	v_cvt_pk_bf16_f32 v35, v36, v37
.Lst_m2_15:
	s_cbranch_execz .Lst_m2_22
	v_cvt_pk_bf16_f32 v30, v30, v31
	v_cvt_pk_bf16_f32 v31, v32, v33
	v_cvt_pk_bf16_f32 v26, v26, v27
	v_cvt_pk_bf16_f32 v27, v28, v29
	v_add_u32_e32 v28, 0xc000, v152
	v_cvt_pk_bf16_f32 v22, v22, v23
	v_cvt_pk_bf16_f32 v23, v24, v25
	v_cvt_pk_bf16_f32 v18, v18, v19
	v_cvt_pk_bf16_f32 v19, v20, v21
	v_cvt_pk_bf16_f32 v14, v14, v15
	v_cvt_pk_bf16_f32 v15, v16, v17
	v_lshl_add_u64 v[8:9], s[12:13], 0, v[8:9]
	ds_write2_b64 v108, v[110:111], v[106:107] offset0:32 offset1:36
	ds_write2_b64 v108, v[102:103], v[98:99] offset0:40 offset1:44
	ds_write2_b64 v92, v[94:95], v[90:91] offset0:64 offset1:68
	ds_write2_b64 v92, v[86:87], v[82:83] offset0:72 offset1:76
.Lst_m2_16:
	s_cbranch_execz .Lst_m2_23
	ds_write2_b64 v76, v[78:79], v[74:75] offset0:96 offset1:100
	ds_write2_b64 v76, v[70:71], v[66:67] offset0:104 offset1:108
	ds_write2_b64 v60, v[62:63], v[58:59] offset0:128 offset1:132
	ds_write2_b64 v60, v[54:55], v[50:51] offset0:136 offset1:140
	ds_write2_b64 v44, v[46:47], v[42:43] offset0:160 offset1:164
	ds_write2_b64 v44, v[38:39], v[34:35] offset0:168 offset1:172
	ds_write2_b64 v28, v[30:31], v[26:27] offset0:192 offset1:196
	ds_write2_b64 v28, v[22:23], v[18:19] offset0:200 offset1:204
	ds_write2_b64 v12, v[14:15], v[10:11] offset0:224 offset1:228
	v_lshl_add_u64 v[8:9], v[8:9], 0, s[2:3]
	s_waitcnt lgkmcnt(0)
	s_barrier
	v_lshl_add_u64 v[8:9], v[8:9], 0, v[182:183]
	ds_read_b128 v[2:5], v6
	s_waitcnt lgkmcnt(0)
	global_store_dwordx4 v[8:9], v[2:5], off sc1
	s_nop 1
	v_add_u32_e32 v8, 2, v172
	v_mov_b32_e32 v9, v173
.Lst_m2_17:
	s_cbranch_execz .Lst_m2_24
	v_lshlrev_b64 v[8:9], 12, v[8:9]
	v_lshl_add_u64 v[8:9], s[12:13], 0, v[8:9]
	v_lshl_add_u64 v[8:9], v[8:9], 0, s[2:3]
	v_lshl_add_u64 v[8:9], v[8:9], 0, v[182:183]
	ds_read_b128 v[2:5], v6 offset:1056
	s_waitcnt lgkmcnt(0)
	global_store_dwordx4 v[8:9], v[2:5], off sc1
	s_nop 1
	v_add_u32_e32 v8, 4, v172
	v_mov_b32_e32 v9, v173
	v_lshlrev_b64 v[8:9], 12, v[8:9]
	v_lshl_add_u64 v[8:9], s[12:13], 0, v[8:9]
	v_lshl_add_u64 v[8:9], v[8:9], 0, s[2:3]
	v_lshl_add_u64 v[8:9], v[8:9], 0, v[182:183]
	ds_read_b128 v[2:5], v6 offset:2112
	s_waitcnt lgkmcnt(0)
	global_store_dwordx4 v[8:9], v[2:5], off sc1
	s_nop 1
	v_add_u32_e32 v8, 6, v172
	v_mov_b32_e32 v9, v173
.Lst_m2_18:
	s_cbranch_execz .Lst_m2_25
	v_lshlrev_b64 v[8:9], 12, v[8:9]
	v_lshl_add_u64 v[8:9], s[12:13], 0, v[8:9]
	v_lshl_add_u64 v[8:9], v[8:9], 0, s[2:3]
	v_lshl_add_u64 v[8:9], v[8:9], 0, v[182:183]
	ds_read_b128 v[2:5], v6 offset:3168
	s_waitcnt lgkmcnt(0)
	global_store_dwordx4 v[8:9], v[2:5], off sc1
	s_nop 1
	v_add_u32_e32 v8, 8, v172
	v_mov_b32_e32 v9, v173
	v_lshlrev_b64 v[8:9], 12, v[8:9]
	v_lshl_add_u64 v[8:9], s[12:13], 0, v[8:9]
	v_lshl_add_u64 v[8:9], v[8:9], 0, s[2:3]
	v_lshl_add_u64 v[8:9], v[8:9], 0, v[182:183]
	ds_read_b128 v[2:5], v6 offset:4224
	s_waitcnt lgkmcnt(0)
	global_store_dwordx4 v[8:9], v[2:5], off sc1
	s_nop 1
	v_add_u32_e32 v8, 10, v172
	v_mov_b32_e32 v9, v173
.Lst_m2_19:
	s_cbranch_execz .Lst_m2_26
	v_lshlrev_b64 v[8:9], 12, v[8:9]
	v_lshl_add_u64 v[8:9], s[12:13], 0, v[8:9]
	v_lshl_add_u64 v[8:9], v[8:9], 0, s[2:3]
	v_lshl_add_u64 v[8:9], v[8:9], 0, v[182:183]
	ds_read_b128 v[2:5], v6 offset:5280
	s_waitcnt lgkmcnt(0)
	global_store_dwordx4 v[8:9], v[2:5], off sc1
	s_nop 1
	v_add_u32_e32 v8, 12, v172
	v_mov_b32_e32 v9, v173
	v_lshlrev_b64 v[8:9], 12, v[8:9]
	v_lshl_add_u64 v[8:9], s[12:13], 0, v[8:9]
	v_lshl_add_u64 v[8:9], v[8:9], 0, s[2:3]
	v_lshl_add_u64 v[8:9], v[8:9], 0, v[182:183]
	ds_read_b128 v[2:5], v6 offset:6336
	s_waitcnt lgkmcnt(0)
	global_store_dwordx4 v[8:9], v[2:5], off sc1
	s_nop 1
	v_add_u32_e32 v8, 14, v172
	v_mov_b32_e32 v9, v173
.Lst_m2_20:
	s_cbranch_execz .Lst_m2_27
	v_lshlrev_b64 v[8:9], 12, v[8:9]
	v_lshl_add_u64 v[8:9], s[12:13], 0, v[8:9]
	v_lshl_add_u64 v[8:9], v[8:9], 0, s[2:3]
	v_lshl_add_u64 v[8:9], v[8:9], 0, v[182:183]
	ds_read_b128 v[2:5], v6 offset:7392
	s_waitcnt lgkmcnt(0)
	global_store_dwordx4 v[8:9], v[2:5], off sc1
	s_nop 1
	v_add_u32_e32 v8, 16, v172
	v_mov_b32_e32 v9, v173
	v_lshlrev_b64 v[8:9], 12, v[8:9]
	v_lshl_add_u64 v[8:9], s[12:13], 0, v[8:9]
	v_lshl_add_u64 v[8:9], v[8:9], 0, s[2:3]
	v_lshl_add_u64 v[8:9], v[8:9], 0, v[182:183]
	ds_read_b128 v[2:5], v6 offset:8448
	s_waitcnt lgkmcnt(0)
	global_store_dwordx4 v[8:9], v[2:5], off sc1
	s_nop 1
	v_add_u32_e32 v8, 18, v172
	v_mov_b32_e32 v9, v173
.Lst_m2_21:
	s_cbranch_execz .Lst_m2_28
	v_lshlrev_b64 v[8:9], 12, v[8:9]
	v_lshl_add_u64 v[8:9], s[12:13], 0, v[8:9]
	v_lshl_add_u64 v[8:9], v[8:9], 0, s[2:3]
	v_lshl_add_u64 v[8:9], v[8:9], 0, v[182:183]
	ds_read_b128 v[2:5], v6 offset:9504
	s_waitcnt lgkmcnt(0)
	global_store_dwordx4 v[8:9], v[2:5], off sc1
	s_nop 1
	v_add_u32_e32 v8, 20, v172
	v_mov_b32_e32 v9, v173
	v_lshlrev_b64 v[8:9], 12, v[8:9]
	v_lshl_add_u64 v[8:9], s[12:13], 0, v[8:9]
	v_lshl_add_u64 v[8:9], v[8:9], 0, s[2:3]
	v_lshl_add_u64 v[8:9], v[8:9], 0, v[182:183]
	ds_read_b128 v[2:5], v6 offset:10560
	s_waitcnt lgkmcnt(0)
	global_store_dwordx4 v[8:9], v[2:5], off sc1
	s_nop 1
	v_add_u32_e32 v8, 22, v172
	v_mov_b32_e32 v9, v173
.Lst_m2_22:
	s_cbranch_execz .Lst_m2_29
	v_lshlrev_b64 v[8:9], 12, v[8:9]
	v_lshl_add_u64 v[8:9], s[12:13], 0, v[8:9]
	v_lshl_add_u64 v[8:9], v[8:9], 0, s[2:3]
	v_lshl_add_u64 v[8:9], v[8:9], 0, v[182:183]
	ds_read_b128 v[2:5], v6 offset:11616
	s_waitcnt lgkmcnt(0)
	global_store_dwordx4 v[8:9], v[2:5], off sc1
	s_nop 1
	v_add_u32_e32 v8, 24, v172
	v_mov_b32_e32 v9, v173
	v_lshlrev_b64 v[8:9], 12, v[8:9]
	v_lshl_add_u64 v[8:9], s[12:13], 0, v[8:9]
	v_lshl_add_u64 v[8:9], v[8:9], 0, s[2:3]
	v_lshl_add_u64 v[8:9], v[8:9], 0, v[182:183]
	ds_read_b128 v[2:5], v6 offset:12672
	s_waitcnt lgkmcnt(0)
	global_store_dwordx4 v[8:9], v[2:5], off sc1
	s_nop 1
	v_add_u32_e32 v8, 26, v172
	v_mov_b32_e32 v9, v173
.Lst_m2_23:
	s_cbranch_execz .Lst_m2_30
	v_lshlrev_b64 v[8:9], 12, v[8:9]
	v_lshl_add_u64 v[8:9], s[12:13], 0, v[8:9]
	v_lshl_add_u64 v[8:9], v[8:9], 0, s[2:3]
	v_lshl_add_u64 v[8:9], v[8:9], 0, v[182:183]
	ds_read_b128 v[2:5], v6 offset:13728
	s_waitcnt lgkmcnt(0)
	global_store_dwordx4 v[8:9], v[2:5], off sc1
	s_nop 1
	v_add_u32_e32 v8, 28, v172
	v_mov_b32_e32 v9, v173
	v_lshlrev_b64 v[8:9], 12, v[8:9]
	v_lshl_add_u64 v[8:9], s[12:13], 0, v[8:9]
	v_lshl_add_u64 v[8:9], v[8:9], 0, s[2:3]
	ds_read_b128 v[2:5], v6 offset:14784
	v_lshl_add_u64 v[8:9], v[8:9], 0, v[182:183]
	s_waitcnt lgkmcnt(0)
	global_store_dwordx4 v[8:9], v[2:5], off sc1
	s_nop 1
	v_add_u32_e32 v172, 30, v172
	ds_read_b128 v[2:5], v6 offset:15840
.Lst_m2_24:
	s_cbranch_execz .Lst_m2_31
	v_lshlrev_b64 v[6:7], 12, v[172:173]
	v_lshl_add_u64 v[6:7], s[12:13], 0, v[6:7]
	v_lshl_add_u64 v[6:7], v[6:7], 0, s[2:3]
	v_lshl_add_u64 v[6:7], v[6:7], 0, v[182:183]
	s_waitcnt lgkmcnt(0)
	global_store_dwordx4 v[6:7], v[2:5], off sc1
	s_nop 1
	s_waitcnt lgkmcnt(0)
	s_barrier
	s_cbranch_vccz .LBB0_1543

.Lst_m2_25:
	s_cbranch_execz .Lst_m2_32
	s_add_u32 s10, s19, s10
	s_addc_u32 s11, s20, s11
	s_lshl_b32 s14, s29, 8
	s_and_b32 s15, s14, 0x300
	v_or_b32_e32 v2, s15, v195
	v_mul_u32_u24_e32 v172, 0x1600, v2
	v_lshl_add_u64 v[2:3], s[10:11], 0, v[172:173]
	v_mov_b32_e32 v179, v173
	v_lshl_add_u64 v[184:185], v[2:3], 0, v[178:179]
	v_mad_i64_i32 v[2:3], s[10:11], s2, v204, v[174:175]
	s_and_b32 s2, s14, 0x1c00
	v_lshl_add_u64 v[2:3], v[2:3], 0, s[2:3]
	v_mov_b32_e32 v181, v173
	v_lshl_add_u64 v[186:187], v[2:3], 0, v[180:181]
	v_lshl_add_u64 v[188:189], v[186:187], 0, s[6:7]

.Lst_m2_26:
	s_cbranch_execz .Lst_m2_33
	s_mul_i32 s17, s10, 0x1600000
	s_mul_hi_i32 s2, s10, 0x1600000
	s_add_u32 s17, s64, s17
	s_addc_u32 s2, s65, s2
	s_lshl_b32 s30, s16, 6
	s_and_b32 s30, s30, 0x700
	s_lshl_b32 s31, s30, 2
	s_add_u32 s17, s17, s31
	s_addc_u32 s38, s2, 0
	s_lshl_b32 s2, s16, 8
	v_readfirstlane_b32 s16, v0
	s_and_b32 s31, s2, 0x300
	s_lshr_b32 s2, s16, 6
	s_lshl_b32 s34, s2, 9
	s_lshl_b32 s33, s2, 5
	s_and_b32 s35, s33, 0x60
	v_mov_b32_e32 v3, s34
	s_lshr_b32 s34, s16, 1
	v_bitop3_b32 v206, s35, v3, v194 bitop3:0xde
	s_and_b32 s35, s34, 0x7fffff80
	s_lshl_b32 s34, s16, 1
	s_and_b32 s34, s34, 0x180
	s_or_b32 s36, s34, 32
	v_or_b32_e32 v2, s31, v171
.Lst_m2_27:
	s_cbranch_execz .Lst_m2_34
	v_bitop3_b32 v181, s36, v201, v198 bitop3:0xde
	s_or_b32 s36, s34, 64
	v_mul_u32_u24_e32 v34, 0xb00, v2
	v_bitop3_b32 v179, s36, v201, v198 bitop3:0xde
	s_or_b32 s36, s34, 0x60
	v_or_b32_e32 v2, v34, v177
	v_bitop3_b32 v172, s36, v201, v198 bitop3:0xde
	s_lshl_b32 s36, s2, 10
	v_lshlrev_b32_e32 v35, 1, v2
	s_add_i32 s36, s36, 0
	s_mov_b32 s37, m0
	s_mov_b32 m0, s36
	s_nop 0
	global_load_lds_dwordx4 v35, s[14:15]
	s_mov_b32 m0, s37
	s_add_i32 s37, s36, 0x2000
	v_add_lshl_u32 v36, v190, v34, 1
	s_mov_b32 s39, m0
	s_mov_b32 m0, s37
	s_nop 0
	global_load_lds_dwordx4 v36, s[14:15]
	s_mov_b32 m0, s39
	s_add_i32 s37, s36, 0x4000
.Lst_m2_28:
	s_cbranch_execz .Lst_m2_35
	v_add_lshl_u32 v37, v191, v34, 1
	s_mov_b32 s39, m0
	s_mov_b32 m0, s37
	s_nop 0
	global_load_lds_dwordx4 v37, s[14:15]
	s_mov_b32 m0, s39
	s_add_i32 s37, s36, 0x6000
	s_lshl_b64 s[40:41], s[2:3], 13
	s_add_u32 s40, s17, s40
	v_bitop3_b32 v2, s33, v194, v203 bitop3:0x6c
	v_or_b32_e32 v4, s35, v1
	s_addc_u32 s41, s38, s41
	s_waitcnt vmcnt(1)
	v_add_lshl_u32 v38, v192, v34, 1
	v_lshlrev_b32_e32 v39, 7, v4
	v_bitop3_b32 v205, v2, s23, v3 bitop3:0x36
	s_mov_b32 s39, m0
	s_mov_b32 m0, s37
	s_nop 0
	global_load_lds_dwordx4 v38, s[14:15]
	s_mov_b32 m0, s39
	global_load_dwordx4 v[2:5], v199, s[40:41] nt
	s_add_i32 s40, s2, 8
	s_mov_b32 s41, s3
.Lst_m2_29:
	s_cbranch_execz .Lst_m2_36
	s_lshl_b64 s[40:41], s[40:41], 13
	s_add_u32 s40, s17, s40
	s_addc_u32 s41, s38, s41
	global_load_dwordx4 v[6:9], v199, s[40:41] nt
	s_add_i32 s40, s2, 16
	s_mov_b32 s41, s3
	s_lshl_b64 s[40:41], s[40:41], 13
	s_add_u32 s40, s17, s40
	s_addc_u32 s41, s38, s41
	global_load_dwordx4 v[10:13], v199, s[40:41] nt
	s_add_i32 s40, s2, 24
	s_mov_b32 s41, s3
	s_lshl_b64 s[40:41], s[40:41], 13
	s_add_u32 s40, s17, s40
	s_addc_u32 s41, s38, s41
	global_load_dwordx4 v[14:17], v199, s[40:41] nt
	s_add_i32 s40, s2, 32
	s_mov_b32 s41, s3
	s_lshl_b64 s[40:41], s[40:41], 13
	s_add_u32 s40, s17, s40
	s_addc_u32 s41, s38, s41
	global_load_dwordx4 v[18:21], v199, s[40:41] nt
	s_add_i32 s40, s2, 40
	s_mov_b32 s41, s3
	s_lshl_b64 s[40:41], s[40:41], 13
	s_add_u32 s40, s17, s40
	s_addc_u32 s41, s38, s41
	global_load_dwordx4 v[22:25], v199, s[40:41] nt
.Lst_m2_30:
	s_cbranch_execz .Lst_m2_37
	s_add_i32 s40, s2, 48
	s_mov_b32 s41, s3
	s_lshl_b64 s[40:41], s[40:41], 13
	s_add_u32 s40, s17, s40
	s_addc_u32 s41, s38, s41
	global_load_dwordx4 v[26:29], v199, s[40:41] nt
	s_add_i32 s40, s2, 56
	s_mov_b32 s41, s3
	s_lshl_b64 s[40:41], s[40:41], 13
	s_add_u32 s40, s17, s40
	s_addc_u32 s41, s38, s41
	s_add_i32 s39, s36, 0x8000
	v_or_b32_e32 v35, 0x80, v35
	global_load_dwordx4 v[30:33], v199, s[40:41] nt
	s_mov_b32 s40, m0
	s_mov_b32 m0, s39
	s_nop 0
	global_load_lds_dwordx4 v35, s[14:15]
	s_mov_b32 m0, s40
	v_or_b32_e32 v35, 0x80, v36
	s_add_i32 s39, s36, 0xa000
	s_mov_b32 s40, m0
	s_mov_b32 m0, s39
	s_nop 0
	global_load_lds_dwordx4 v35, s[14:15]
.Lst_m2_31:
	s_cbranch_execz .Lst_m2_38
	s_mov_b32 m0, s40
	v_or_b32_e32 v35, 0x80, v37
	s_add_i32 s39, s36, 0xc000
	s_mov_b32 s40, m0
	s_mov_b32 m0, s39
	s_nop 0
	global_load_lds_dwordx4 v35, s[14:15]
	s_mov_b32 m0, s40
	v_or_b32_e32 v35, 0x80, v38
	s_add_i32 s39, s36, 0xe000
	s_mov_b32 s40, m0
	s_mov_b32 m0, s39
	s_nop 0
	global_load_lds_dwordx4 v35, s[14:15]
	s_mov_b32 m0, s40
	s_waitcnt vmcnt(4)
	s_add_i32 s40, s2, 64
	v_cvt_pk_bf16_f32 v2, v2, v3
	v_cvt_pk_bf16_f32 v3, v4, v5
	v_add_u32_e32 v4, s24, v206
	ds_write_b64 v4, v[2:3]
	v_cvt_pk_bf16_f32 v2, v6, v7
.Lst_m2_32:
	s_cbranch_execz .Lst_m2_39
	v_cvt_pk_bf16_f32 v3, v8, v9
	v_add_u32_e32 v5, s24, v205
	ds_write_b64 v5, v[2:3] offset:4096
	v_cvt_pk_bf16_f32 v2, v10, v11
	v_cvt_pk_bf16_f32 v3, v12, v13
	ds_write_b64 v4, v[2:3] offset:8192
	v_cvt_pk_bf16_f32 v2, v14, v15
	v_cvt_pk_bf16_f32 v3, v16, v17
	ds_write_b64 v5, v[2:3] offset:12288
	v_cvt_pk_bf16_f32 v2, v18, v19
	v_cvt_pk_bf16_f32 v3, v20, v21
	s_mov_b32 s41, s3
	ds_write_b64 v4, v[2:3] offset:16384
	v_cvt_pk_bf16_f32 v2, v22, v23
	v_cvt_pk_bf16_f32 v3, v24, v25
	s_lshl_b64 s[40:41], s[40:41], 13
	ds_write_b64 v5, v[2:3] offset:20480
	v_cvt_pk_bf16_f32 v2, v26, v27
.Lst_m2_33:
	s_cbranch_execz .Lst_m2_40
	v_cvt_pk_bf16_f32 v3, v28, v29
	s_add_u32 s40, s17, s40
	ds_write_b64 v4, v[2:3] offset:24576
	v_cvt_pk_bf16_f32 v2, v30, v31
	v_cvt_pk_bf16_f32 v3, v32, v33
	s_addc_u32 s41, s38, s41
	ds_write_b64 v5, v[2:3] offset:28672
	global_load_dwordx4 v[30:33], v199, s[40:41] nt
	s_add_i32 s40, s2, 0x48
	s_mov_b32 s41, s3
	s_lshl_b64 s[40:41], s[40:41], 13
	s_add_u32 s40, s17, s40
	s_addc_u32 s41, s38, s41
	global_load_dwordx4 v[26:29], v199, s[40:41] nt
	s_add_i32 s40, s2, 0x50
	s_mov_b32 s41, s3
	s_lshl_b64 s[40:41], s[40:41], 13
	s_add_u32 s40, s17, s40
	s_addc_u32 s41, s38, s41
	global_load_dwordx4 v[22:25], v199, s[40:41] nt
	s_add_i32 s40, s2, 0x58
.Lst_m2_34:
	s_cbranch_execz .Lst_m2_41
	s_mov_b32 s41, s3
	s_lshl_b64 s[40:41], s[40:41], 13
	s_add_u32 s40, s17, s40
	s_addc_u32 s41, s38, s41
	global_load_dwordx4 v[18:21], v199, s[40:41] nt
	s_add_i32 s40, s2, 0x60
	s_mov_b32 s41, s3
	s_lshl_b64 s[40:41], s[40:41], 13
	s_add_u32 s40, s17, s40
	s_addc_u32 s41, s38, s41
	global_load_dwordx4 v[14:17], v199, s[40:41] nt
	s_add_i32 s40, s2, 0x68
	s_mov_b32 s41, s3
	s_lshl_b64 s[40:41], s[40:41], 13
	s_add_u32 s40, s17, s40
	s_addc_u32 s41, s38, s41
	global_load_dwordx4 v[10:13], v199, s[40:41] nt
	s_add_i32 s40, s2, 0x70
	s_mov_b32 s41, s3
	s_lshl_b64 s[40:41], s[40:41], 13
	s_add_u32 s40, s17, s40
	s_addc_u32 s41, s38, s41
	s_addk_i32 s2, 0x78
	global_load_dwordx4 v[6:9], v199, s[40:41] nt
	s_lshl_b64 s[40:41], s[2:3], 13
.Lst_m2_35:
	s_cbranch_execz .Lst_m2_42
	s_add_u32 s40, s17, s40
	s_addc_u32 s41, s38, s41
	global_load_dwordx4 v[2:5], v199, s[40:41] nt
	s_lshl_b64 s[40:41], s[16:17], 7
	s_waitcnt lgkmcnt(0)
	s_barrier
	s_and_b32 s16, s41, 0x7f
	s_and_b32 s2, s40, 0xffffe000
	s_add_u32 s2, s17, s2
	v_lshl_add_u32 v209, v34, 1, v202
	v_mov_b32_e32 v34, 0
	v_bitop3_b32 v183, s34, v201, v198 bitop3:0xde
	v_or_b32_e32 v207, v39, v196
	s_mov_b32 s37, 0x8000
	v_or_b32_e32 v208, v39, v197
	s_addc_u32 s38, s38, s16
	s_mov_b32 s39, 0x10000
	s_mov_b32 s40, 0
	s_mov_b64 s[16:17], 0
	v_mov_b32_e32 v35, v34
	v_mov_b32_e32 v36, v34
	v_mov_b32_e32 v37, v34
	v_mov_b32_e32 v38, v34
	v_mov_b32_e32 v39, v34
	v_mov_b32_e32 v40, v34
.Lst_m2_36:
	s_cbranch_execz .Lst_m2_43
	v_mov_b32_e32 v41, v34
	s_waitcnt vmcnt(0)
	v_mov_b32_e32 v42, v34
	v_mov_b32_e32 v43, v34
	v_mov_b32_e32 v44, v34
	v_mov_b32_e32 v45, v34
	v_mov_b32_e32 v46, v34
	v_mov_b32_e32 v47, v34
	v_mov_b32_e32 v48, v34
	v_mov_b32_e32 v49, v34
	v_mov_b32_e32 v50, v34
	v_mov_b32_e32 v51, v34
	v_mov_b32_e32 v52, v34
	v_mov_b32_e32 v53, v34
	v_mov_b32_e32 v54, v34
	v_mov_b32_e32 v55, v34
	v_mov_b32_e32 v56, v34
	v_mov_b32_e32 v57, v34
	v_mov_b32_e32 v58, v34
	v_mov_b32_e32 v59, v34
	v_mov_b32_e32 v60, v34
	v_mov_b32_e32 v61, v34
	v_mov_b32_e32 v62, v34
	v_mov_b32_e32 v63, v34
	v_mov_b32_e32 v64, v34
	v_mov_b32_e32 v65, v34
	v_mov_b32_e32 v66, v34
	v_mov_b32_e32 v67, v34
	v_mov_b32_e32 v68, v34
	v_mov_b32_e32 v69, v34
	v_mov_b32_e32 v70, v34
	v_mov_b32_e32 v71, v34
.Lst_m2_37:
	s_cbranch_execz .Lst_m2_44
	v_mov_b32_e32 v72, v34
	v_mov_b32_e32 v73, v34
	v_mov_b32_e32 v74, v34
	v_mov_b32_e32 v75, v34
	v_mov_b32_e32 v76, v34
	v_mov_b32_e32 v77, v34
	v_mov_b32_e32 v78, v34
	v_mov_b32_e32 v79, v34
	v_mov_b32_e32 v80, v34
	v_mov_b32_e32 v81, v34
	v_mov_b32_e32 v82, v34
	v_mov_b32_e32 v83, v34
	v_mov_b32_e32 v84, v34
	v_mov_b32_e32 v85, v34
	v_mov_b32_e32 v86, v34
	v_mov_b32_e32 v87, v34
	v_mov_b32_e32 v88, v34
	v_mov_b32_e32 v89, v34
	v_mov_b32_e32 v90, v34
	v_mov_b32_e32 v91, v34
	v_mov_b32_e32 v92, v34
	v_mov_b32_e32 v93, v34
	v_mov_b32_e32 v94, v34
	v_mov_b32_e32 v95, v34
	v_mov_b32_e32 v96, v34
	v_mov_b32_e32 v97, v34
	v_mov_b32_e32 v98, v34
	v_mov_b32_e32 v99, v34
	v_mov_b32_e32 v100, v34
	v_mov_b32_e32 v101, v34
	v_mov_b32_e32 v102, v34
	v_mov_b32_e32 v103, v34
.Lst_m2_38:
	s_cbranch_execz .Lst_m2_45
	v_mov_b32_e32 v104, v34
	v_mov_b32_e32 v105, v34
	v_mov_b32_e32 v106, v34
	v_mov_b32_e32 v107, v34
	v_mov_b32_e32 v108, v34
	v_mov_b32_e32 v109, v34
	v_mov_b32_e32 v110, v34
	v_mov_b32_e32 v111, v34
	v_mov_b32_e32 v112, v34
	v_mov_b32_e32 v113, v34
	v_mov_b32_e32 v114, v34
	v_mov_b32_e32 v115, v34
	v_mov_b32_e32 v116, v34
	v_mov_b32_e32 v117, v34
	v_mov_b32_e32 v118, v34
	v_mov_b32_e32 v119, v34
	v_mov_b32_e32 v120, v34
	v_mov_b32_e32 v121, v34
	v_mov_b32_e32 v122, v34
	v_mov_b32_e32 v123, v34
	v_mov_b32_e32 v124, v34
	v_mov_b32_e32 v125, v34
	v_mov_b32_e32 v126, v34
	v_mov_b32_e32 v127, v34
	v_mov_b32_e32 v128, v34
	v_mov_b32_e32 v129, v34
	v_mov_b32_e32 v130, v34
	v_mov_b32_e32 v131, v34
	v_mov_b32_e32 v132, v34
	v_mov_b32_e32 v133, v34
	v_mov_b32_e32 v134, v34
	v_mov_b32_e32 v135, v34
.Lst_m2_39:
	s_cbranch_execz .Lst_m2_46
	v_mov_b32_e32 v136, v34
	v_mov_b32_e32 v137, v34
	v_mov_b32_e32 v138, v34
	v_mov_b32_e32 v139, v34
	v_mov_b32_e32 v140, v34
	v_mov_b32_e32 v141, v34
	v_mov_b32_e32 v142, v34
	v_mov_b32_e32 v143, v34
	v_mov_b32_e32 v144, v34
	v_mov_b32_e32 v145, v34
	v_mov_b32_e32 v146, v34
	v_mov_b32_e32 v147, v34
	v_mov_b32_e32 v148, v34
	v_mov_b32_e32 v149, v34
	v_mov_b32_e32 v150, v34
	v_mov_b32_e32 v151, v34
	v_mov_b32_e32 v152, v34
	v_mov_b32_e32 v153, v34
	v_mov_b32_e32 v158, v34
	v_mov_b32_e32 v159, v34
	v_mov_b32_e32 v160, v34
	v_mov_b32_e32 v161, v34
	v_mov_b32_e32 v154, v34
	v_mov_b32_e32 v155, v34
	v_mov_b32_e32 v156, v34
	v_mov_b32_e32 v157, v34

.Lst_m2_40:
	s_cbranch_execz .Lst_m2_47
	v_add_u32_e32 v209, s24, v183
	v_add_u32_e32 v242, 0, v207
	v_add_u32_e32 v207, s24, v179
	v_add_u32_e32 v243, s24, v172
	v_add_u32_e32 v236, s24, v181
	ds_read_b64_tr_b16 v[162:163], v209
	ds_read_b64_tr_b16 v[164:165], v209 offset:2048
	ds_read_b64_tr_b16 v[166:167], v236
	ds_read_b64_tr_b16 v[168:169], v236 offset:2048
	ds_read_b128 v[210:213], v242
	ds_read_b128 v[214:217], v242 offset:2048
	ds_read_b64_tr_b16 v[218:219], v207
	ds_read_b64_tr_b16 v[220:221], v207 offset:2048
	ds_read_b64_tr_b16 v[222:223], v243
	ds_read_b64_tr_b16 v[224:225], v243 offset:2048
	s_waitcnt lgkmcnt(5)
	v_mfma_f32_16x16x32_bf16 v[34:37], v[162:165], v[210:213], v[34:37]
	ds_read_b128 v[226:229], v242 offset:4096
	v_mfma_f32_16x16x32_bf16 v[38:41], v[166:169], v[210:213], v[38:41]
.Lst_m2_41:
	s_cbranch_execz .Lst_m2_48
	s_waitcnt lgkmcnt(3)
	v_mfma_f32_16x16x32_bf16 v[42:45], v[218:221], v[210:213], v[42:45]
	s_waitcnt lgkmcnt(1)
	v_mfma_f32_16x16x32_bf16 v[46:49], v[222:225], v[210:213], v[46:49]
	v_mfma_f32_16x16x32_bf16 v[50:53], v[162:165], v[214:217], v[50:53]
	ds_read_b128 v[210:213], v242 offset:6144
	v_mfma_f32_16x16x32_bf16 v[54:57], v[166:169], v[214:217], v[54:57]
	v_mfma_f32_16x16x32_bf16 v[58:61], v[218:221], v[214:217], v[58:61]
	v_mfma_f32_16x16x32_bf16 v[62:65], v[222:225], v[214:217], v[62:65]
	s_waitcnt lgkmcnt(1)
	v_mfma_f32_16x16x32_bf16 v[66:69], v[162:165], v[226:229], v[66:69]
	ds_read_b128 v[214:217], v242 offset:8192
	v_mfma_f32_16x16x32_bf16 v[70:73], v[166:169], v[226:229], v[70:73]
	v_mfma_f32_16x16x32_bf16 v[74:77], v[218:221], v[226:229], v[74:77]
	v_mfma_f32_16x16x32_bf16 v[78:81], v[222:225], v[226:229], v[78:81]
	s_waitcnt lgkmcnt(1)
	v_mfma_f32_16x16x32_bf16 v[82:85], v[162:165], v[210:213], v[82:85]
	ds_read_b128 v[226:229], v242 offset:10240
.Lst_m2_42:
	s_cbranch_execz .Lst_m2_49
	v_mfma_f32_16x16x32_bf16 v[86:89], v[166:169], v[210:213], v[86:89]
	v_mfma_f32_16x16x32_bf16 v[90:93], v[218:221], v[210:213], v[90:93]
	v_mfma_f32_16x16x32_bf16 v[94:97], v[222:225], v[210:213], v[94:97]
	ds_read_b128 v[210:213], v242 offset:12288
	ds_read_b64_tr_b16 v[230:231], v209 offset:16384
	ds_read_b64_tr_b16 v[232:233], v209 offset:18432
	s_waitcnt lgkmcnt(4)
	v_mfma_f32_16x16x32_bf16 v[98:101], v[162:165], v[214:217], v[98:101]
	v_mfma_f32_16x16x32_bf16 v[102:105], v[166:169], v[214:217], v[102:105]
	v_mfma_f32_16x16x32_bf16 v[106:109], v[218:221], v[214:217], v[106:109]
	v_mfma_f32_16x16x32_bf16 v[110:113], v[222:225], v[214:217], v[110:113]
	ds_read_b128 v[214:217], v242 offset:14336
	ds_read_b64_tr_b16 v[234:235], v236 offset:16384
	ds_read_b64_tr_b16 v[236:237], v236 offset:18432
	s_waitcnt lgkmcnt(6)
	v_mfma_f32_16x16x32_bf16 v[114:117], v[162:165], v[226:229], v[114:117]
	v_mfma_f32_16x16x32_bf16 v[118:121], v[166:169], v[226:229], v[118:121]
.Lst_m2_43:
	s_cbranch_execz .Lst_m2_50
	v_mfma_f32_16x16x32_bf16 v[122:125], v[218:221], v[226:229], v[122:125]
	v_mfma_f32_16x16x32_bf16 v[126:129], v[222:225], v[226:229], v[126:129]
	v_add_u32_e32 v244, 0, v208
	ds_read_b128 v[226:229], v244
	ds_read_b64_tr_b16 v[238:239], v207 offset:16384
	ds_read_b64_tr_b16 v[240:241], v207 offset:18432
	s_waitcnt lgkmcnt(8)
	v_mfma_f32_16x16x32_bf16 v[130:133], v[162:165], v[210:213], v[130:133]
	v_mfma_f32_16x16x32_bf16 v[134:137], v[166:169], v[210:213], v[134:137]
	v_mfma_f32_16x16x32_bf16 v[138:141], v[218:221], v[210:213], v[138:141]
	v_mfma_f32_16x16x32_bf16 v[142:145], v[222:225], v[210:213], v[142:145]
	s_waitcnt lgkmcnt(5)
	v_mfma_f32_16x16x32_bf16 v[146:149], v[162:165], v[214:217], v[146:149]
	v_mfma_f32_16x16x32_bf16 v[150:153], v[166:169], v[214:217], v[150:153]
	ds_read_b128 v[162:165], v244 offset:2048
	ds_read_b64_tr_b16 v[166:167], v243 offset:16384
	ds_read_b64_tr_b16 v[168:169], v243 offset:18432
	v_mfma_f32_16x16x32_bf16 v[158:161], v[218:221], v[214:217], v[158:161]
.Lst_m2_44:
	s_cbranch_execz .Lst_m2_51
	v_mfma_f32_16x16x32_bf16 v[154:157], v[222:225], v[214:217], v[154:157]
	ds_read_b128 v[208:211], v244 offset:4096
	s_waitcnt vmcnt(7)
	v_add_u32_e32 v206, s25, v206
	v_cvt_pk_bf16_f32 v30, v30, v31
	v_cvt_pk_bf16_f32 v31, v32, v33
	s_waitcnt lgkmcnt(6)
	v_mfma_f32_16x16x32_bf16 v[34:37], v[230:233], v[226:229], v[34:37]
	ds_write_b64 v206, v[30:31]
	v_mfma_f32_16x16x32_bf16 v[38:41], v[234:237], v[226:229], v[38:41]
	s_waitcnt lgkmcnt(5)
	v_mfma_f32_16x16x32_bf16 v[42:45], v[238:241], v[226:229], v[42:45]
	s_waitcnt lgkmcnt(2)
	v_mfma_f32_16x16x32_bf16 v[30:33], v[166:169], v[226:229], v[46:49]
	v_mfma_f32_16x16x32_bf16 v[46:49], v[230:233], v[162:165], v[50:53]
	v_add_u32_e32 v205, s25, v205
	v_mfma_f32_16x16x32_bf16 v[50:53], v[234:237], v[162:165], v[54:57]
	s_nop 2
	ds_read_b128 v[54:57], v244 offset:6144
	s_waitcnt vmcnt(6)
.Lst_m2_45:
	s_cbranch_execz .Lst_m2_52
	v_mfma_f32_16x16x32_bf16 v[58:61], v[238:241], v[162:165], v[58:61]
	v_cvt_pk_bf16_f32 v26, v26, v27
	v_cvt_pk_bf16_f32 v27, v28, v29
	ds_write_b64 v205, v[26:27] offset:4096
	v_mfma_f32_16x16x32_bf16 v[26:29], v[166:169], v[162:165], v[62:65]
	s_waitcnt lgkmcnt(3)
	v_mfma_f32_16x16x32_bf16 v[62:65], v[230:233], v[208:211], v[66:69]
	v_mfma_f32_16x16x32_bf16 v[66:69], v[234:237], v[208:211], v[70:73]
	s_nop 2
	ds_read_b128 v[70:73], v244 offset:8192
	s_waitcnt vmcnt(5)
	v_mfma_f32_16x16x32_bf16 v[74:77], v[238:241], v[208:211], v[74:77]
	v_cvt_pk_bf16_f32 v22, v22, v23
	v_cvt_pk_bf16_f32 v23, v24, v25
	ds_write_b64 v206, v[22:23] offset:8192
	v_mfma_f32_16x16x32_bf16 v[22:25], v[166:169], v[208:211], v[78:81]
	s_waitcnt lgkmcnt(3)
	v_mfma_f32_16x16x32_bf16 v[78:81], v[230:233], v[54:57], v[82:85]
.Lst_m2_46:
	s_cbranch_execz .Lst_m2_53
	v_mfma_f32_16x16x32_bf16 v[82:85], v[234:237], v[54:57], v[86:89]
	s_nop 2
	ds_read_b128 v[86:89], v244 offset:10240
	s_waitcnt vmcnt(4)
	v_mfma_f32_16x16x32_bf16 v[90:93], v[238:241], v[54:57], v[90:93]
	v_cvt_pk_bf16_f32 v18, v18, v19
	v_cvt_pk_bf16_f32 v19, v20, v21
	ds_write_b64 v205, v[18:19] offset:12288
	v_mfma_f32_16x16x32_bf16 v[18:21], v[166:169], v[54:57], v[94:97]
	s_waitcnt lgkmcnt(3)
	v_mfma_f32_16x16x32_bf16 v[54:57], v[230:233], v[70:73], v[98:101]
	s_nop 2
	ds_read_b128 v[98:101], v244 offset:12288
	s_waitcnt vmcnt(3)
	v_mfma_f32_16x16x32_bf16 v[94:97], v[234:237], v[70:73], v[102:105]
	v_cvt_pk_bf16_f32 v14, v14, v15
	v_cvt_pk_bf16_f32 v15, v16, v17
	ds_write_b64 v206, v[14:15] offset:16384
	v_mfma_f32_16x16x32_bf16 v[102:105], v[238:241], v[70:73], v[106:109]
.Lst_m2_47:
	s_cbranch_execz .Lst_m2_54
	v_mfma_f32_16x16x32_bf16 v[14:17], v[166:169], v[70:73], v[110:113]
	s_nop 2
	ds_read_b128 v[110:113], v244 offset:14336
	s_waitcnt vmcnt(2)
	s_waitcnt lgkmcnt(4)
	v_mfma_f32_16x16x32_bf16 v[70:73], v[230:233], v[86:89], v[114:117]
	v_cvt_pk_bf16_f32 v10, v10, v11
	v_cvt_pk_bf16_f32 v11, v12, v13
	ds_write_b64 v205, v[10:11] offset:20480
	v_mfma_f32_16x16x32_bf16 v[106:109], v[234:237], v[86:89], v[118:121]
	v_mfma_f32_16x16x32_bf16 v[114:117], v[238:241], v[86:89], v[122:125]
	v_mfma_f32_16x16x32_bf16 v[10:13], v[166:169], v[86:89], v[126:129]
	s_waitcnt vmcnt(1)
	s_waitcnt lgkmcnt(3)
	v_mfma_f32_16x16x32_bf16 v[86:89], v[230:233], v[98:101], v[130:133]
	v_cvt_pk_bf16_f32 v6, v6, v7
	v_cvt_pk_bf16_f32 v7, v8, v9
	ds_write_b64 v206, v[6:7] offset:24576
	v_mfma_f32_16x16x32_bf16 v[118:121], v[234:237], v[98:101], v[134:137]
.Lst_m2_48:
	s_cbranch_execz .Lst_m2_55
	v_mfma_f32_16x16x32_bf16 v[122:125], v[238:241], v[98:101], v[138:141]
	v_mfma_f32_16x16x32_bf16 v[6:9], v[166:169], v[98:101], v[142:145]
	s_waitcnt vmcnt(0)
	s_waitcnt lgkmcnt(2)
	v_mfma_f32_16x16x32_bf16 v[98:101], v[230:233], v[110:113], v[146:149]
	v_cvt_pk_bf16_f32 v2, v2, v3
	v_cvt_pk_bf16_f32 v3, v4, v5
	ds_write_b64 v205, v[2:3] offset:28672
	v_mfma_f32_16x16x32_bf16 v[126:129], v[234:237], v[110:113], v[150:153]
	v_mfma_f32_16x16x32_bf16 v[130:133], v[238:241], v[110:113], v[158:161]
	v_mfma_f32_16x16x32_bf16 v[2:5], v[166:169], v[110:113], v[154:157]
	s_waitcnt lgkmcnt(0)
	s_barrier
	v_add_u32_e32 v168, s25, v183
	v_add_u32_e32 v181, s25, v181
	v_add_u32_e32 v179, s25, v179
	ds_read_b64_tr_b16 v[110:111], v168
	ds_read_b64_tr_b16 v[112:113], v168 offset:2048
	ds_read_b64_tr_b16 v[134:135], v181
	ds_read_b64_tr_b16 v[136:137], v181 offset:2048
.Lst_m2_49:
	s_cbranch_execz .Lst_m2_56
	ds_read_b128 v[138:141], v242 offset:32768
	ds_read_b64_tr_b16 v[142:143], v179
	ds_read_b128 v[146:149], v242 offset:34816
	ds_read_b128 v[150:153], v242 offset:36864
	ds_read_b64_tr_b16 v[144:145], v179 offset:2048
	v_add_u32_e32 v172, s25, v172
	ds_read_b64_tr_b16 v[154:155], v172
	ds_read_b64_tr_b16 v[156:157], v172 offset:2048
	s_waitcnt lgkmcnt(6)
	v_mfma_f32_16x16x32_bf16 v[34:37], v[110:113], v[138:141], v[34:37]
	v_mfma_f32_16x16x32_bf16 v[38:41], v[134:137], v[138:141], v[38:41]
	s_waitcnt lgkmcnt(2)
	v_mfma_f32_16x16x32_bf16 v[42:45], v[142:145], v[138:141], v[42:45]
	s_waitcnt lgkmcnt(0)
	v_mfma_f32_16x16x32_bf16 v[30:33], v[154:157], v[138:141], v[30:33]
	v_mfma_f32_16x16x32_bf16 v[46:49], v[110:113], v[146:149], v[46:49]
	ds_read_b128 v[138:141], v242 offset:38912
	v_mfma_f32_16x16x32_bf16 v[50:53], v[134:137], v[146:149], v[50:53]
.Lst_m2_50:
	s_cbranch_execz .Lst_m2_57
	v_mfma_f32_16x16x32_bf16 v[58:61], v[142:145], v[146:149], v[58:61]
	v_mfma_f32_16x16x32_bf16 v[26:29], v[154:157], v[146:149], v[26:29]
	v_mfma_f32_16x16x32_bf16 v[62:65], v[110:113], v[150:153], v[62:65]
	ds_read_b128 v[146:149], v242 offset:40960
	v_mfma_f32_16x16x32_bf16 v[66:69], v[134:137], v[150:153], v[66:69]
	v_mfma_f32_16x16x32_bf16 v[74:77], v[142:145], v[150:153], v[74:77]
	v_mfma_f32_16x16x32_bf16 v[22:25], v[154:157], v[150:153], v[22:25]
	s_waitcnt lgkmcnt(1)
	v_mfma_f32_16x16x32_bf16 v[150:153], v[134:137], v[138:141], v[82:85]
	s_nop 2
	ds_read_b128 v[82:85], v242 offset:43008
	v_mfma_f32_16x16x32_bf16 v[78:81], v[110:113], v[138:141], v[78:81]
	v_mfma_f32_16x16x32_bf16 v[18:21], v[154:157], v[138:141], v[18:21]
	v_mfma_f32_16x16x32_bf16 v[158:161], v[142:145], v[138:141], v[90:93]
	s_nop 2
	ds_read_b128 v[90:93], v242 offset:45056
	ds_read_b64_tr_b16 v[166:167], v168 offset:16384
	ds_read_b64_tr_b16 v[168:169], v168 offset:18432
.Lst_m2_51:
	s_cbranch_execz .Lst_m2_58
	s_waitcnt lgkmcnt(4)
	v_mfma_f32_16x16x32_bf16 v[54:57], v[110:113], v[146:149], v[54:57]
	v_mfma_f32_16x16x32_bf16 v[14:17], v[154:157], v[146:149], v[14:17]
	v_mfma_f32_16x16x32_bf16 v[138:141], v[134:137], v[146:149], v[94:97]
	v_mfma_f32_16x16x32_bf16 v[162:165], v[142:145], v[146:149], v[102:105]
	s_waitcnt lgkmcnt(3)
	v_mfma_f32_16x16x32_bf16 v[146:149], v[110:113], v[82:85], v[70:73]
	s_nop 2
	ds_read_b128 v[70:73], v242 offset:47104
	ds_read_b64_tr_b16 v[214:215], v181 offset:16384
	ds_read_b64_tr_b16 v[216:217], v181 offset:18432
	v_mfma_f32_16x16x32_bf16 v[10:13], v[154:157], v[82:85], v[10:13]
	v_mfma_f32_16x16x32_bf16 v[206:209], v[134:137], v[82:85], v[106:109]
	v_mfma_f32_16x16x32_bf16 v[210:213], v[142:145], v[82:85], v[114:117]
	ds_read_b128 v[82:85], v244 offset:32768
	ds_read_b64_tr_b16 v[230:231], v179 offset:16384
	ds_read_b64_tr_b16 v[232:233], v179 offset:18432
	s_waitcnt lgkmcnt(8)
.Lst_m2_52:
	s_cbranch_execz .Lst_m2_59
	v_mfma_f32_16x16x32_bf16 v[6:9], v[154:157], v[90:93], v[6:9]
	v_mfma_f32_16x16x32_bf16 v[218:221], v[110:113], v[90:93], v[86:89]
	v_mfma_f32_16x16x32_bf16 v[222:225], v[134:137], v[90:93], v[118:121]
	v_mfma_f32_16x16x32_bf16 v[226:229], v[142:145], v[90:93], v[122:125]
	s_waitcnt lgkmcnt(5)
	v_mfma_f32_16x16x32_bf16 v[130:133], v[142:145], v[70:73], v[130:133]
	ds_read_b128 v[86:89], v244 offset:34816
	ds_read_b64_tr_b16 v[142:143], v172 offset:16384
	ds_read_b64_tr_b16 v[144:145], v172 offset:18432
	v_mfma_f32_16x16x32_bf16 v[134:137], v[134:137], v[70:73], v[126:129]
	v_mfma_f32_16x16x32_bf16 v[2:5], v[154:157], v[70:73], v[2:5]
	v_mfma_f32_16x16x32_bf16 v[234:237], v[110:113], v[70:73], v[98:101]
	s_waitcnt lgkmcnt(5)
	v_mfma_f32_16x16x32_bf16 v[126:129], v[166:169], v[82:85], v[34:37]
	s_nop 2
	ds_read_b128 v[34:37], v244 offset:36864
	v_mfma_f32_16x16x32_bf16 v[122:125], v[214:217], v[82:85], v[38:41]
	s_waitcnt lgkmcnt(4)
.Lst_m2_53:
	s_cbranch_execz .Lst_m2_60
	v_mfma_f32_16x16x32_bf16 v[118:121], v[230:233], v[82:85], v[42:45]
	s_waitcnt lgkmcnt(1)
	v_mfma_f32_16x16x32_bf16 v[114:117], v[142:145], v[82:85], v[30:33]
	s_nop 2
	ds_read_b128 v[30:33], v244 offset:38912
	v_mfma_f32_16x16x32_bf16 v[110:113], v[166:169], v[86:89], v[46:49]
	v_mfma_f32_16x16x32_bf16 v[106:109], v[214:217], v[86:89], v[50:53]
	v_mfma_f32_16x16x32_bf16 v[102:105], v[230:233], v[86:89], v[58:61]
	v_mfma_f32_16x16x32_bf16 v[98:101], v[142:145], v[86:89], v[26:29]
	s_nop 2
	ds_read_b128 v[26:29], v244 offset:40960
	s_waitcnt lgkmcnt(2)
	v_mfma_f32_16x16x32_bf16 v[94:97], v[166:169], v[34:37], v[62:65]
	v_mfma_f32_16x16x32_bf16 v[90:93], v[214:217], v[34:37], v[66:69]
	v_mfma_f32_16x16x32_bf16 v[86:89], v[230:233], v[34:37], v[74:77]
	v_mfma_f32_16x16x32_bf16 v[82:85], v[142:145], v[34:37], v[22:25]
	s_nop 2
	ds_read_b128 v[22:25], v244 offset:43008
	s_waitcnt lgkmcnt(2)
.Lst_m2_54:
	s_cbranch_execz .Lsc_join_m2
	v_mfma_f32_16x16x32_bf16 v[78:81], v[166:169], v[30:33], v[78:81]
	v_mfma_f32_16x16x32_bf16 v[74:77], v[214:217], v[30:33], v[150:153]
	v_mfma_f32_16x16x32_bf16 v[70:73], v[230:233], v[30:33], v[158:161]
	v_mfma_f32_16x16x32_bf16 v[66:69], v[142:145], v[30:33], v[18:21]
	s_nop 2
	ds_read_b128 v[18:21], v244 offset:45056
	s_waitcnt lgkmcnt(2)
	v_mfma_f32_16x16x32_bf16 v[62:65], v[166:169], v[26:29], v[54:57]
	v_mfma_f32_16x16x32_bf16 v[58:61], v[214:217], v[26:29], v[138:141]
	v_mfma_f32_16x16x32_bf16 v[54:57], v[230:233], v[26:29], v[162:165]
	v_mfma_f32_16x16x32_bf16 v[50:53], v[142:145], v[26:29], v[14:17]
	s_waitcnt lgkmcnt(1)
	v_mfma_f32_16x16x32_bf16 v[46:49], v[166:169], v[22:25], v[146:149]
	ds_read_b128 v[138:141], v244 offset:47104
	v_mfma_f32_16x16x32_bf16 v[42:45], v[214:217], v[22:25], v[206:209]
	v_mfma_f32_16x16x32_bf16 v[38:41], v[230:233], v[22:25], v[210:213]
	v_mfma_f32_16x16x32_bf16 v[34:37], v[142:145], v[22:25], v[10:13]
	s_waitcnt lgkmcnt(1)
.Lst_m2_55:
	s_cbranch_execz .Lsc_join_m2
	v_mfma_f32_16x16x32_bf16 v[30:33], v[166:169], v[18:21], v[218:221]
	v_mfma_f32_16x16x32_bf16 v[26:29], v[214:217], v[18:21], v[222:225]
	v_mfma_f32_16x16x32_bf16 v[22:25], v[230:233], v[18:21], v[226:229]
	v_mfma_f32_16x16x32_bf16 v[18:21], v[142:145], v[18:21], v[6:9]
	s_waitcnt lgkmcnt(0)
	v_mfma_f32_16x16x32_bf16 v[14:17], v[166:169], v[138:141], v[234:237]
	v_mfma_f32_16x16x32_bf16 v[10:13], v[214:217], v[138:141], v[134:137]
	v_mfma_f32_16x16x32_bf16 v[6:9], v[230:233], v[138:141], v[130:133]
	v_mfma_f32_16x16x32_bf16 v[2:5], v[142:145], v[138:141], v[2:5]
	s_waitcnt lgkmcnt(0)
	s_barrier
	s_nop 0
	v_mov_b32_e32 v131, 0
	s_andn2_b64 vcc, exec, s[12:13]
	v_mov_b32_e32 v133, 0
	v_mov_b32_e32 v134, 0
	s_cbranch_vccnz .LBB0_1536
	global_load_dword v131, v[184:185], off
	global_load_dword v133, v[186:187], off
	global_load_dword v134, v[188:189], off
	s_branch .LBB0_1536
.LBB0_1543:
.Lst_m2_56:
	s_cbranch_execz .Lsc_join_m2
	s_barrier

.Lst_m2_57:
	s_cbranch_execz .Lsc_join_m2
	s_addc_u32 s9, s71, 0
	s_mov_b32 s17, 1
	s_waitcnt vmcnt(5)
	v_mov_b32_e32 v17, 0
	s_branch .LBB0_1549

.Lst_m2_58:
	s_cbranch_execz .Lsc_join_m2
	global_load_dword v13, v17, s[4:5] sc1
	global_load_dword v14, v17, s[6:7] sc1
	global_load_dword v15, v17, s[8:9] sc1
	s_mov_b64 s[10:11], -1
	s_mov_b64 s[12:13], -1
	s_waitcnt vmcnt(14)
	v_add_u32_e32 v18, v1, v16
	s_waitcnt vmcnt(13)
	v_add_u32_e32 v18, v18, v2
	s_waitcnt vmcnt(12)
	v_add_u32_e32 v18, v18, v3
	s_waitcnt vmcnt(11)
	v_add_u32_e32 v18, v18, v4
	s_waitcnt vmcnt(10)
	v_add_u32_e32 v18, v18, v5
	s_waitcnt vmcnt(9)
	v_add_u32_e32 v18, v18, v6
	s_waitcnt vmcnt(8)
	v_add_u32_e32 v18, v18, v7
	s_waitcnt vmcnt(7)
	v_add_u32_e32 v18, v18, v8
	s_waitcnt vmcnt(6)
	v_add_u32_e32 v18, v18, v9
	s_waitcnt vmcnt(5)
	v_add_u32_e32 v18, v18, v10
	s_waitcnt vmcnt(4)
	v_add_u32_e32 v18, v18, v11
	s_waitcnt vmcnt(3)
	v_add_u32_e32 v18, v18, v12
.Lst_m2_59:
	s_cbranch_execz .Lsc_join_m2
	s_waitcnt vmcnt(2)
	v_add_u32_e32 v18, v18, v13
	s_waitcnt vmcnt(1)
	v_add_u32_e32 v18, v18, v14
	s_waitcnt vmcnt(0)
	v_add_u32_e32 v18, v18, v15
	v_cmp_eq_u32_e32 vcc, s16, v18
	s_cbranch_vccnz .LBB0_1548
	s_and_b32 s10, s17, 0xff
	s_cmp_eq_u32 s10, 0
	s_mov_b64 s[10:11], -1
	s_mov_b64 s[14:15], -1
	s_sleep 1
	s_cbranch_scc1 .LBB0_1553
	s_and_b64 vcc, exec, s[14:15]
	s_cbranch_vccz .LBB0_1548

.Lst_m2_60:
	s_cbranch_execz .Lsc_join_m2
	s_branch .LBB0_1548

.LBB0_1595:
.Lst_fi_0:
	s_cbranch_execz .Lst_fi_7
	s_waitcnt vmcnt(0)
	s_cmp_gt_i32 s92, 13
	s_cselect_b64 s[0:1], -1, 0
	s_xor_b64 s[2:3], s[2:3], -1
	s_or_b64 s[0:1], s[0:1], s[2:3]
	s_and_b64 vcc, exec, s[0:1]
	s_cbranch_vccnz .LBB0_1700
	s_lshl_b32 s0, s96, 3
	s_add_i32 s2, s0, s80
	s_cmpk_gt_i32 s2, 0x1fff
	s_cbranch_scc1 .LBB0_1699
	s_waitcnt vmcnt(1)
	v_mov_b32_e32 v65, 0
	v_lshlrev_b32_e32 v64, 4, v170
	v_lshl_add_u64 v[16:17], s[66:67], 0, v[64:65]
	v_add_co_u32_e32 v32, vcc, 0x1000, v16
	global_load_dwordx4 v[0:3], v64, s[66:67]
	global_load_dwordx4 v[4:7], v64, s[66:67] offset:1024
	global_load_dwordx4 v[8:11], v64, s[66:67] offset:2048
	global_load_dwordx4 v[12:15], v64, s[66:67] offset:3072
	v_addc_co_u32_e32 v33, vcc, 0, v17, vcc
	global_load_dwordx4 v[16:19], v[32:33], off
	global_load_dwordx4 v[20:23], v[32:33], off offset:1024
	global_load_dwordx4 v[24:27], v[32:33], off offset:2048
	global_load_dwordx4 v[28:31], v[32:33], off offset:3072
	v_mbcnt_lo_u32_b32 v32, -1, 0
	v_mbcnt_hi_u32_b32 v32, -1, v32
	v_and_b32_e32 v33, 64, v32
	v_add_u32_e32 v33, 64, v33
	v_xor_b32_e32 v34, 32, v32
	v_cmp_lt_i32_e32 vcc, v34, v33
	s_add_u32 s4, s70, 0x19958000
	s_addc_u32 s5, s71, 0
	v_cndmask_b32_e32 v34, v32, v34, vcc
	v_lshlrev_b32_e32 v67, 2, v34
	v_xor_b32_e32 v34, 16, v32
.Lst_fi_1:
	s_cbranch_execz .Lst_fi_8
	v_cmp_lt_i32_e32 vcc, v34, v33
	v_lshlrev_b32_e32 v64, 3, v170
	v_lshlrev_b32_e32 v66, 2, v170
	v_cndmask_b32_e32 v34, v32, v34, vcc
	v_lshlrev_b32_e32 v171, 2, v34
	v_xor_b32_e32 v34, 8, v32
	v_cmp_lt_i32_e32 vcc, v34, v33
	s_add_u32 s8, s70, 0x140d8000
	s_mov_b64 s[10:11], 0xe038000
	v_cndmask_b32_e32 v34, v32, v34, vcc
	v_lshlrev_b32_e32 v186, 2, v34
	v_xor_b32_e32 v34, 4, v32
	v_cmp_lt_i32_e32 vcc, v34, v33
	s_movk_i32 s28, 0x1000
	s_mov_b32 s7, 0
	v_cndmask_b32_e32 v34, v32, v34, vcc
	v_lshlrev_b32_e32 v187, 2, v34
	v_xor_b32_e32 v34, 2, v32
	v_cmp_lt_i32_e32 vcc, v34, v33
	s_addc_u32 s9, s71, 0
	s_lshl_b32 s29, s72, 3
	v_cndmask_b32_e32 v34, v32, v34, vcc
	v_lshlrev_b32_e32 v188, 2, v34
	v_xor_b32_e32 v34, 1, v32
	v_cmp_lt_i32_e32 vcc, v34, v33
	s_lshl_b32 s30, s72, 5
	v_cmp_gt_u32_e64 s[0:1], 16, v170
	v_cndmask_b32_e32 v32, v32, v34, vcc
	v_lshlrev_b32_e32 v189, 2, v32
	v_cmp_lt_u32_e32 vcc, 15, v170
	v_lshl_add_u64 v[32:33], s[70:71], 0, v[64:65]
	v_lshl_add_u64 v[68:69], v[32:33], 0, s[10:11]
	v_lshl_add_u64 v[70:71], s[4:5], 0, v[64:65]
	s_xor_b64 s[10:11], vcc, -1
	v_lshlrev_b32_e32 v64, 2, v66
	s_mov_b64 s[12:13], 0x12000
	s_mov_b32 s31, 0x12000
	v_mov_b32_e32 v190, 0x358637bd
	s_mov_b32 s33, 0x800000

.Lst_fi_3:
	s_cbranch_execz .Lst_fi_10
	v_lshlrev_b32_e32 v144, 16, v145
	v_and_b32_e32 v145, 0xffff0000, v145
	v_pk_fma_f32 v[56:57], v[56:57], v[162:163], v[150:151]
	v_mul_f32_e32 v160, v61, v61
	v_pk_fma_f32 v[58:59], v[58:59], v[164:165], v[144:145]
	v_mul_f32_e32 v144, v57, v57
	v_fmac_f32_e32 v160, v60, v60
	v_fmac_f32_e32 v144, v56, v56
	v_fmac_f32_e32 v160, v62, v62
	v_fmac_f32_e32 v144, v58, v58
	v_fmac_f32_e32 v160, v63, v63
	v_fmac_f32_e32 v144, v59, v59
	v_add_f32_e32 v150, v160, v144
	v_lshlrev_b32_e32 v144, 16, v138
	v_and_b32_e32 v145, 0xffff0000, v138
	v_lshlrev_b32_e32 v138, 16, v139
	v_and_b32_e32 v139, 0xffff0000, v139
	v_pk_fma_f32 v[52:53], v[52:53], v[156:157], v[144:145]
	v_pk_fma_f32 v[54:55], v[54:55], v[158:159], v[138:139]
	v_mul_f32_e32 v138, v53, v53
	v_fmac_f32_e32 v138, v52, v52
	v_fmac_f32_e32 v138, v54, v54
	v_fmac_f32_e32 v138, v55, v55
	v_add_f32_e32 v144, v138, v150
	v_lshlrev_b32_e32 v138, 16, v132
	v_and_b32_e32 v139, 0xffff0000, v132
	v_lshlrev_b32_e32 v132, 16, v133
	v_and_b32_e32 v133, 0xffff0000, v133
	s_waitcnt vmcnt(8)
	v_pk_fma_f32 v[48:49], v[48:49], v[152:153], v[138:139]
	v_pk_fma_f32 v[50:51], v[50:51], v[154:155], v[132:133]
	v_mul_f32_e32 v132, v49, v49
	v_fmac_f32_e32 v132, v48, v48
	v_fmac_f32_e32 v132, v50, v50
	v_fmac_f32_e32 v132, v51, v51
	v_add_f32_e32 v138, v132, v144
	s_waitcnt vmcnt(5)
.Lst_fi_4:
	s_cbranch_execz .Lst_fi_11
	v_lshlrev_b32_e32 v132, 16, v128
	v_and_b32_e32 v133, 0xffff0000, v128
	v_lshlrev_b32_e32 v128, 16, v129
	v_and_b32_e32 v129, 0xffff0000, v129
	v_pk_fma_f32 v[46:47], v[46:47], v[148:149], v[128:129]
	s_waitcnt vmcnt(4)
	v_lshlrev_b32_e32 v128, 16, v124
	v_and_b32_e32 v129, 0xffff0000, v124
	v_pk_fma_f32 v[44:45], v[44:45], v[146:147], v[132:133]
	v_pk_fma_f32 v[40:41], v[40:41], v[140:141], v[128:129]
	v_lshlrev_b32_e32 v124, 16, v125
	v_and_b32_e32 v125, 0xffff0000, v125
	v_mov_b32_e32 v128, v41
	v_mov_b32_e32 v129, v45
	v_pk_fma_f32 v[42:43], v[42:43], v[142:143], v[124:125]
	v_mov_b32_e32 v124, v40
	v_mov_b32_e32 v125, v44
	v_pk_mul_f32 v[128:129], v[128:129], v[128:129]
	s_lshl_b64 s[14:15], s[14:15], 13
	v_pk_fma_f32 v[124:125], v[124:125], v[124:125], v[128:129]
	v_mov_b32_e32 v128, v42
	v_mov_b32_e32 v129, v46
	v_pk_fma_f32 v[124:125], v[128:129], v[128:129], v[124:125]
	v_mov_b32_e32 v128, v43
	v_mov_b32_e32 v129, v47
	v_pk_fma_f32 v[124:125], v[128:129], v[128:129], v[124:125]
	s_add_u32 s14, s68, s14
	v_add_f32_e32 v125, v125, v138
	v_add_f32_e32 v128, v124, v125
	s_waitcnt vmcnt(3)
	v_lshlrev_b32_e32 v124, 16, v122
	v_and_b32_e32 v125, 0xffff0000, v122
	v_lshlrev_b32_e32 v122, 16, v123
	v_and_b32_e32 v123, 0xffff0000, v123
.Lst_fi_5:
	s_cbranch_execz .Lst_fi_12
	s_waitcnt vmcnt(1)
	v_pk_fma_f32 v[38:39], v[38:39], v[136:137], v[122:123]
	v_lshlrev_b32_e32 v122, 16, v120
	v_and_b32_e32 v123, 0xffff0000, v120
	v_pk_fma_f32 v[36:37], v[36:37], v[134:135], v[124:125]
	v_lshlrev_b32_e32 v120, 16, v121
	v_and_b32_e32 v121, 0xffff0000, v121
	s_waitcnt vmcnt(0)
	v_pk_fma_f32 v[122:123], v[32:33], v[126:127], v[122:123]
	v_pk_fma_f32 v[120:121], v[34:35], v[130:131], v[120:121]
	v_mov_b32_e32 v34, v123
	v_mov_b32_e32 v35, v37
	v_mov_b32_e32 v32, v122
	v_mov_b32_e32 v33, v36
	v_pk_mul_f32 v[34:35], v[34:35], v[34:35]
	s_addc_u32 s15, s69, s15
	v_pk_fma_f32 v[32:33], v[32:33], v[32:33], v[34:35]
	v_mov_b32_e32 v34, v120
	v_mov_b32_e32 v35, v38
	v_pk_fma_f32 v[32:33], v[34:35], v[34:35], v[32:33]
	v_mov_b32_e32 v34, v121
	v_mov_b32_e32 v35, v39
	v_pk_fma_f32 v[32:33], v[34:35], v[34:35], v[32:33]
	s_nop 0
	v_add_f32_e32 v33, v33, v128
	v_add_f32_e32 v32, v32, v33
	ds_bpermute_b32 v33, v67, v32
	s_waitcnt lgkmcnt(0)
	v_add_f32_e32 v32, v32, v33
	ds_bpermute_b32 v33, v171, v32
	s_waitcnt lgkmcnt(0)
	v_add_f32_e32 v32, v32, v33
	ds_bpermute_b32 v33, v186, v32
	s_waitcnt lgkmcnt(0)
	v_add_f32_e32 v32, v32, v33
.Lst_fi_6:
	s_cbranch_execz .Lst_fi_13
	ds_bpermute_b32 v33, v187, v32
	s_waitcnt lgkmcnt(0)
	v_add_f32_e32 v32, v32, v33
	ds_bpermute_b32 v33, v188, v32
	s_waitcnt lgkmcnt(0)
	v_add_f32_e32 v32, v32, v33
	ds_bpermute_b32 v33, v189, v32
	s_waitcnt lgkmcnt(0)
	v_add_f32_e32 v32, v32, v33
	v_fmamk_f32 v32, v32, 0x3a000000, v190
	v_mul_f32_e32 v33, 0x4b800000, v32
	v_cmp_gt_f32_e32 vcc, s33, v32
	s_nop 1
	v_cndmask_b32_e32 v32, v32, v33, vcc
	v_rsq_f32_e32 v32, v32
	s_nop 0
	v_mul_f32_e32 v33, 0x45800000, v32
	v_cndmask_b32_e32 v124, v32, v33, vcc
	v_pk_mul_f32 v[32:33], v[60:61], v[124:125] op_sel_hi:[1,0]
	v_pk_mul_f32 v[34:35], v[62:63], v[124:125] op_sel_hi:[1,0]
	v_pk_mul_f32 v[32:33], v[0:1], v[32:33]
	v_pk_mul_f32 v[34:35], v[2:3], v[34:35]
	global_store_dwordx4 v64, v[32:35], s[14:15]
	v_lshl_add_u64 v[60:61], s[14:15], 0, v[64:65]
	s_nop 0
	v_pk_mul_f32 v[32:33], v[56:57], v[124:125] op_sel_hi:[1,0]
	v_pk_mul_f32 v[34:35], v[58:59], v[124:125] op_sel_hi:[1,0]
	v_pk_mul_f32 v[32:33], v[4:5], v[32:33]
	v_pk_mul_f32 v[34:35], v[6:7], v[34:35]
	global_store_dwordx4 v64, v[32:35], s[14:15] offset:1024
	s_nop 1
.Lst_fi_7:
	s_cbranch_execz .Lst_fi_14
	v_pk_mul_f32 v[32:33], v[52:53], v[124:125] op_sel_hi:[1,0]
	v_pk_mul_f32 v[34:35], v[54:55], v[124:125] op_sel_hi:[1,0]
	v_pk_mul_f32 v[32:33], v[8:9], v[32:33]
	v_pk_mul_f32 v[34:35], v[10:11], v[34:35]
	global_store_dwordx4 v64, v[32:35], s[14:15] offset:2048
	s_nop 1
	v_pk_mul_f32 v[32:33], v[48:49], v[124:125] op_sel_hi:[1,0]
	v_pk_mul_f32 v[34:35], v[50:51], v[124:125] op_sel_hi:[1,0]
	v_pk_mul_f32 v[32:33], v[12:13], v[32:33]
	v_pk_mul_f32 v[34:35], v[14:15], v[34:35]
	global_store_dwordx4 v64, v[32:35], s[14:15] offset:3072
	s_nop 1
	v_pk_mul_f32 v[32:33], v[44:45], v[124:125] op_sel_hi:[1,0]
	v_pk_mul_f32 v[34:35], v[46:47], v[124:125] op_sel_hi:[1,0]
	v_add_co_u32_e32 v44, vcc, s28, v60
	v_pk_mul_f32 v[34:35], v[18:19], v[34:35]
	v_pk_mul_f32 v[32:33], v[16:17], v[32:33]
	v_addc_co_u32_e32 v45, vcc, 0, v61, vcc
	global_store_dwordx4 v[44:45], v[32:35], off
	s_nop 1
	v_pk_mul_f32 v[32:33], v[40:41], v[124:125] op_sel_hi:[1,0]
	v_pk_mul_f32 v[34:35], v[42:43], v[124:125] op_sel_hi:[1,0]
	v_pk_mul_f32 v[32:33], v[20:21], v[32:33]
	v_pk_mul_f32 v[34:35], v[22:23], v[34:35]
	global_store_dwordx4 v[44:45], v[32:35], off offset:1024
	s_nop 1
	v_pk_mul_f32 v[32:33], v[36:37], v[124:125] op_sel_hi:[1,0]
.Lst_fi_8:
	s_cbranch_execz .Lst_fi_15
	v_pk_mul_f32 v[34:35], v[38:39], v[124:125] op_sel_hi:[1,0]
	v_pk_mul_f32 v[32:33], v[24:25], v[32:33]
	v_pk_mul_f32 v[34:35], v[26:27], v[34:35]
	global_store_dwordx4 v[44:45], v[32:35], off offset:2048
	s_nop 1
	v_pk_mul_f32 v[32:33], v[122:123], v[124:125] op_sel_hi:[1,0]
	v_pk_mul_f32 v[34:35], v[120:121], v[124:125] op_sel_hi:[1,0]
	v_pk_mul_f32 v[32:33], v[28:29], v[32:33]
	v_pk_mul_f32 v[34:35], v[30:31], v[34:35]
	global_store_dwordx4 v[44:45], v[32:35], off offset:3072

.Lst_fi_9:
	s_cbranch_execz .Lst_fi_16
	s_ashr_i32 s6, s2, 11
	s_lshl_b64 s[20:21], s[2:3], 12
	v_lshl_add_u64 v[32:33], v[68:69], 0, s[20:21]
	s_mul_i32 s20, s6, 0x3000
	s_ashr_i32 s21, s20, 31
	s_lshl_b64 s[20:21], s[20:21], 2
	s_add_u32 s20, s70, s20
	s_addc_u32 s21, s71, s21
	v_lshl_add_u64 v[34:35], s[20:21], 0, v[64:65]
	v_add_co_u32_e32 v38, vcc, s31, v34
	v_lshl_add_u64 v[36:37], v[34:35], 0, s[12:13]
	s_nop 0
	v_addc_co_u32_e32 v39, vcc, 0, v35, vcc
	v_add_co_u32_e32 v34, vcc, 0x13000, v34
	global_load_dwordx4 v[56:59], v[36:37], off offset:1024
	global_load_dwordx4 v[52:55], v[36:37], off offset:2048
	global_load_dwordx2 v[150:151], v[32:33], off nt
	global_load_dwordx2 v[144:145], v[32:33], off offset:512 nt
	global_load_dwordx2 v[138:139], v[32:33], off offset:1024 nt
	global_load_dwordx2 v[132:133], v[32:33], off offset:1536 nt
	global_load_dwordx4 v[60:63], v[38:39], off
	global_load_dwordx4 v[48:51], v[36:37], off offset:3072
	v_addc_co_u32_e32 v35, vcc, 0, v35, vcc
	global_load_dwordx4 v[44:47], v[34:35], off
	global_load_dwordx4 v[40:43], v[34:35], off offset:1024
	global_load_dwordx2 v[128:129], v[32:33], off offset:2048 nt
	global_load_dwordx2 v[124:125], v[32:33], off offset:2560 nt
	global_load_dwordx2 v[122:123], v[32:33], off offset:3072 nt
	global_load_dwordx2 v[120:121], v[32:33], off offset:3584 nt
.Lst_fi_10:
	s_cbranch_execz .Lst_fi_17
	global_load_dwordx4 v[36:39], v[34:35], off offset:2048
	s_nop 0
	global_load_dwordx4 v[32:35], v[34:35], off offset:3072
	s_waitcnt vmcnt(16)
	v_cmp_lt_i32_e32 vcc, -1, v194
	s_and_b32 s17, vcc_lo, 0xffff
	s_cmp_eq_u32 s17, 0
	s_cbranch_scc1 .LBB0_1630
	s_lshl_b32 s6, s6, 8
	v_mov_b32_e32 v160, 0
	s_ashr_i32 s15, s6, 31
	v_mov_b32_e32 v161, v160
	v_mov_b32_e32 v166, v160
	v_mov_b32_e32 v167, v160
	v_mov_b32_e32 v162, v160
	v_mov_b32_e32 v163, v160
	v_mov_b32_e32 v164, v160
	v_mov_b32_e32 v165, v160
	v_mov_b32_e32 v156, v160
	v_mov_b32_e32 v157, v160
	v_mov_b32_e32 v158, v160
	v_mov_b32_e32 v159, v160
	v_mov_b32_e32 v152, v160
	v_mov_b32_e32 v153, v160
	v_mov_b32_e32 v154, v160
	v_mov_b32_e32 v155, v160
	v_mov_b32_e32 v146, v160
	v_mov_b32_e32 v147, v160
	v_mov_b32_e32 v148, v160
	v_mov_b32_e32 v149, v160
	v_mov_b32_e32 v140, v160
	v_mov_b32_e32 v141, v160
	v_mov_b32_e32 v142, v160
	v_mov_b32_e32 v143, v160
	v_mov_b32_e32 v134, v160
	v_mov_b32_e32 v135, v160
	v_mov_b32_e32 v136, v160
	v_mov_b32_e32 v137, v160
	v_mov_b32_e32 v126, v160
	v_mov_b32_e32 v127, v160
	v_mov_b32_e32 v130, v160
	v_mov_b32_e32 v131, v160
	s_branch .LBB0_1612

.LBB0_1612:
.Lst_fi_11:
	s_cbranch_execz .Lst_fi_18
	s_add_i32 s19, s17, -1
	s_ff1_i32_b32 s25, s17
	s_and_b32 s17, s19, s17
	v_readlane_b32 s24, v194, s25
	s_cmp_eq_u32 s17, 0
	s_mov_b32 s34, 0
	s_cbranch_scc1 .LBB0_1629
	s_ff1_i32_b32 s19, s17
	s_add_i32 s20, s17, -1
	s_and_b32 s17, s20, s17
	v_readlane_b32 s20, v194, s19
	s_lshl_b32 s19, s19, 10
	s_add_u32 s19, s19, s6
	s_addc_u32 s21, 0, s15
	s_ashr_i32 s22, s20, 31
	s_add_u32 s20, s19, s20
	s_addc_u32 s21, s21, s22
	s_lshl_b64 s[20:21], s[20:21], 12
	s_add_u32 s22, s4, s20
	s_addc_u32 s23, s5, s21
	s_mov_b32 s19, 2
	s_cmp_eq_u32 s17, 0
	s_mov_b64 s[20:21], s[4:5]
	s_cbranch_scc1 .LBB0_1615

.Lst_fi_12:
	s_cbranch_execz .Lst_fi_19
	v_readlane_b32 s26, v194, s19
	s_lshl_b32 s19, s19, 10
	s_add_u32 s19, s19, s6
	s_addc_u32 s27, 0, s15
	s_ashr_i32 s34, s26, 31
	s_add_u32 s26, s19, s26
	s_addc_u32 s27, s27, s34
	s_lshl_b64 s[26:27], s[26:27], 12
	s_add_u32 s26, s4, s26
	s_addc_u32 s27, s5, s27
	s_mov_b32 s19, 4

.Lst_fi_13:
	s_cbranch_execz .Lst_fi_20
	global_load_dwordx2 v[106:107], v118, s[22:23] offset:1536 nt
	global_load_dwordx2 v[110:111], v118, s[22:23] offset:2048 nt
	global_load_dwordx2 v[114:115], v118, s[22:23] offset:2560 nt
	global_load_dwordx2 v[116:117], v118, s[22:23] offset:3072 nt
	s_nop 0
	global_load_dwordx2 v[118:119], v118, s[22:23] offset:3584 nt
	s_cmp_gt_u32 s19, 2
	s_cselect_b64 s[22:23], -1, 0
	s_cmp_lt_u32 s19, 3
	s_cbranch_scc0 .LBB0_1625

.Lst_fi_14:
	s_cbranch_execz .Lst_fi_21
	v_and_b32_e32 v185, 0xffff0000, v182
	v_lshlrev_b32_e32 v182, 16, v183
	v_and_b32_e32 v183, 0xffff0000, v183
	v_pk_add_f32 v[164:165], v[164:165], v[182:183]
	s_waitcnt vmcnt(5)
	v_lshlrev_b32_e32 v182, 16, v180
	v_and_b32_e32 v183, 0xffff0000, v180
	v_lshlrev_b32_e32 v180, 16, v181
	v_and_b32_e32 v181, 0xffff0000, v181
	v_pk_add_f32 v[158:159], v[158:159], v[180:181]
	s_waitcnt vmcnt(4)
	v_lshlrev_b32_e32 v180, 16, v178
	v_and_b32_e32 v181, 0xffff0000, v178
	v_lshlrev_b32_e32 v178, 16, v179
	v_and_b32_e32 v179, 0xffff0000, v179
	v_pk_add_f32 v[154:155], v[154:155], v[178:179]
	s_waitcnt vmcnt(3)
	v_lshlrev_b32_e32 v178, 16, v176
	v_and_b32_e32 v179, 0xffff0000, v176
	v_lshlrev_b32_e32 v176, 16, v177
	v_and_b32_e32 v177, 0xffff0000, v177
	v_pk_add_f32 v[148:149], v[148:149], v[176:177]
	s_waitcnt vmcnt(2)
	v_lshlrev_b32_e32 v176, 16, v174
	v_and_b32_e32 v177, 0xffff0000, v174
	v_lshlrev_b32_e32 v174, 16, v175
	v_and_b32_e32 v175, 0xffff0000, v175
	v_pk_add_f32 v[142:143], v[142:143], v[174:175]
	s_waitcnt vmcnt(1)
	v_lshlrev_b32_e32 v174, 16, v172
	v_and_b32_e32 v175, 0xffff0000, v172
	v_lshlrev_b32_e32 v172, 16, v173
.Lst_fi_15:
	s_cbranch_execz .Lst_fi_22
	v_and_b32_e32 v173, 0xffff0000, v173
	v_pk_add_f32 v[136:137], v[136:137], v[172:173]
	s_waitcnt vmcnt(0)
	v_lshlrev_b32_e32 v172, 16, v168
	v_and_b32_e32 v173, 0xffff0000, v168
	v_lshlrev_b32_e32 v168, 16, v169
	v_and_b32_e32 v169, 0xffff0000, v169
	v_pk_add_f32 v[160:161], v[160:161], v[196:197]
	v_pk_add_f32 v[162:163], v[162:163], v[184:185]
	v_pk_add_f32 v[156:157], v[156:157], v[182:183]
	v_pk_add_f32 v[152:153], v[152:153], v[180:181]
	v_pk_add_f32 v[146:147], v[146:147], v[178:179]
	v_pk_add_f32 v[140:141], v[140:141], v[176:177]
	v_pk_add_f32 v[134:135], v[134:135], v[174:175]
	v_pk_add_f32 v[126:127], v[126:127], v[172:173]
	s_andn2_b64 vcc, exec, s[24:25]
	v_pk_add_f32 v[130:131], v[130:131], v[168:169]
	s_cbranch_vccnz .LBB0_1626
	v_lshlrev_b32_e32 v168, 16, v90
	v_and_b32_e32 v169, 0xffff0000, v90
	v_pk_add_f32 v[160:161], v[160:161], v[168:169]
	v_lshlrev_b32_e32 v168, 16, v91
	v_and_b32_e32 v169, 0xffff0000, v91
	v_pk_add_f32 v[166:167], v[166:167], v[168:169]
	v_lshlrev_b32_e32 v168, 16, v96
	v_and_b32_e32 v169, 0xffff0000, v96
	v_pk_add_f32 v[162:163], v[162:163], v[168:169]
	v_lshlrev_b32_e32 v168, 16, v97
	v_and_b32_e32 v169, 0xffff0000, v97
.Lst_fi_16:
	s_cbranch_execz .Lst_fi_23
	v_pk_add_f32 v[164:165], v[164:165], v[168:169]
	v_lshlrev_b32_e32 v168, 16, v102
	v_and_b32_e32 v169, 0xffff0000, v102
	v_pk_add_f32 v[156:157], v[156:157], v[168:169]
	v_lshlrev_b32_e32 v168, 16, v103
	v_and_b32_e32 v169, 0xffff0000, v103
	v_pk_add_f32 v[158:159], v[158:159], v[168:169]
	v_lshlrev_b32_e32 v168, 16, v106
	v_and_b32_e32 v169, 0xffff0000, v106
	v_pk_add_f32 v[152:153], v[152:153], v[168:169]
	v_lshlrev_b32_e32 v168, 16, v107
	v_and_b32_e32 v169, 0xffff0000, v107
	v_pk_add_f32 v[154:155], v[154:155], v[168:169]
	v_lshlrev_b32_e32 v168, 16, v110
	v_and_b32_e32 v169, 0xffff0000, v110
	v_pk_add_f32 v[146:147], v[146:147], v[168:169]
	v_lshlrev_b32_e32 v168, 16, v111
	v_and_b32_e32 v169, 0xffff0000, v111
	v_pk_add_f32 v[148:149], v[148:149], v[168:169]
	v_lshlrev_b32_e32 v168, 16, v114
	v_and_b32_e32 v169, 0xffff0000, v114
	v_pk_add_f32 v[140:141], v[140:141], v[168:169]
	v_lshlrev_b32_e32 v168, 16, v115
	v_and_b32_e32 v169, 0xffff0000, v115
	v_pk_add_f32 v[142:143], v[142:143], v[168:169]
	v_lshlrev_b32_e32 v168, 16, v116
	v_and_b32_e32 v169, 0xffff0000, v116
	v_pk_add_f32 v[134:135], v[134:135], v[168:169]
	v_lshlrev_b32_e32 v168, 16, v117
.Lst_fi_17:
	s_cbranch_execz .Lst_fi_24
	v_and_b32_e32 v169, 0xffff0000, v117
	v_pk_add_f32 v[136:137], v[136:137], v[168:169]
	v_lshlrev_b32_e32 v168, 16, v118
	v_and_b32_e32 v169, 0xffff0000, v118
	v_pk_add_f32 v[126:127], v[126:127], v[168:169]
	v_lshlrev_b32_e32 v168, 16, v119
	v_and_b32_e32 v169, 0xffff0000, v119
	v_pk_add_f32 v[130:131], v[130:131], v[168:169]
	s_andn2_b64 vcc, exec, s[22:23]
	s_cbranch_vccz .LBB0_1627

.LBB0_1627:
.Lst_fi_18:
	s_cbranch_execz .Lst_fi_25
	v_lshlrev_b32_e32 v168, 16, v78
	v_and_b32_e32 v169, 0xffff0000, v78
	v_pk_add_f32 v[160:161], v[160:161], v[168:169]
	v_lshlrev_b32_e32 v168, 16, v79
	v_and_b32_e32 v169, 0xffff0000, v79
	v_pk_add_f32 v[166:167], v[166:167], v[168:169]
	v_lshlrev_b32_e32 v168, 16, v82
	v_and_b32_e32 v169, 0xffff0000, v82
	v_pk_add_f32 v[162:163], v[162:163], v[168:169]
	v_lshlrev_b32_e32 v168, 16, v83
	v_and_b32_e32 v169, 0xffff0000, v83
	v_pk_add_f32 v[164:165], v[164:165], v[168:169]
	v_lshlrev_b32_e32 v168, 16, v86
	v_and_b32_e32 v169, 0xffff0000, v86
	v_pk_add_f32 v[156:157], v[156:157], v[168:169]
	v_lshlrev_b32_e32 v168, 16, v87
	v_and_b32_e32 v169, 0xffff0000, v87
	v_pk_add_f32 v[158:159], v[158:159], v[168:169]
	v_lshlrev_b32_e32 v168, 16, v92
	v_and_b32_e32 v169, 0xffff0000, v92
	v_pk_add_f32 v[152:153], v[152:153], v[168:169]
	v_lshlrev_b32_e32 v168, 16, v93
	v_and_b32_e32 v169, 0xffff0000, v93
	v_pk_add_f32 v[154:155], v[154:155], v[168:169]
	v_lshlrev_b32_e32 v168, 16, v98
	v_and_b32_e32 v169, 0xffff0000, v98
	v_pk_add_f32 v[146:147], v[146:147], v[168:169]
	v_lshlrev_b32_e32 v168, 16, v99
	v_and_b32_e32 v169, 0xffff0000, v99
.Lst_fi_19:
	s_cbranch_execz .Lst_fi_26
	v_pk_add_f32 v[148:149], v[148:149], v[168:169]
	v_lshlrev_b32_e32 v168, 16, v104
	v_and_b32_e32 v169, 0xffff0000, v104
	v_pk_add_f32 v[140:141], v[140:141], v[168:169]
	v_lshlrev_b32_e32 v168, 16, v105
	v_and_b32_e32 v169, 0xffff0000, v105
	v_pk_add_f32 v[142:143], v[142:143], v[168:169]
	v_lshlrev_b32_e32 v168, 16, v108
	v_and_b32_e32 v169, 0xffff0000, v108
	v_pk_add_f32 v[134:135], v[134:135], v[168:169]
	v_lshlrev_b32_e32 v168, 16, v109
	v_and_b32_e32 v169, 0xffff0000, v109
	v_pk_add_f32 v[136:137], v[136:137], v[168:169]
	v_lshlrev_b32_e32 v168, 16, v112
	v_and_b32_e32 v169, 0xffff0000, v112
	v_pk_add_f32 v[126:127], v[126:127], v[168:169]
	v_lshlrev_b32_e32 v168, 16, v113
	v_and_b32_e32 v169, 0xffff0000, v113
	v_pk_add_f32 v[130:131], v[130:131], v[168:169]
	s_andn2_b64 vcc, exec, s[20:21]
	s_cbranch_vccnz .LBB0_1611

.Lst_fi_20:
	s_cbranch_execz .Lst_fi_27
	v_lshlrev_b32_e32 v168, 16, v75
	v_and_b32_e32 v169, 0xffff0000, v75
	v_pk_add_f32 v[164:165], v[164:165], v[168:169]
	v_lshlrev_b32_e32 v168, 16, v76
	v_and_b32_e32 v169, 0xffff0000, v76
	v_pk_add_f32 v[156:157], v[156:157], v[168:169]
	v_lshlrev_b32_e32 v168, 16, v77
	v_and_b32_e32 v169, 0xffff0000, v77
	v_pk_add_f32 v[158:159], v[158:159], v[168:169]
	v_lshlrev_b32_e32 v168, 16, v80
	v_and_b32_e32 v169, 0xffff0000, v80
	v_pk_add_f32 v[152:153], v[152:153], v[168:169]
	v_lshlrev_b32_e32 v168, 16, v81
	v_and_b32_e32 v169, 0xffff0000, v81
	v_pk_add_f32 v[154:155], v[154:155], v[168:169]
	v_lshlrev_b32_e32 v168, 16, v84
	v_and_b32_e32 v169, 0xffff0000, v84
	v_pk_add_f32 v[146:147], v[146:147], v[168:169]
	v_lshlrev_b32_e32 v168, 16, v85
	v_and_b32_e32 v169, 0xffff0000, v85
	v_pk_add_f32 v[148:149], v[148:149], v[168:169]
	v_lshlrev_b32_e32 v168, 16, v88
	v_and_b32_e32 v169, 0xffff0000, v88
	v_pk_add_f32 v[140:141], v[140:141], v[168:169]
	v_lshlrev_b32_e32 v168, 16, v89
	v_and_b32_e32 v169, 0xffff0000, v89
	v_pk_add_f32 v[142:143], v[142:143], v[168:169]
	v_lshlrev_b32_e32 v168, 16, v94
	v_and_b32_e32 v169, 0xffff0000, v94
.Lst_fi_21:
	s_cbranch_execz .Lst_fi_28
	v_pk_add_f32 v[134:135], v[134:135], v[168:169]
	v_lshlrev_b32_e32 v168, 16, v95
	v_and_b32_e32 v169, 0xffff0000, v95
	v_pk_add_f32 v[136:137], v[136:137], v[168:169]
	v_lshlrev_b32_e32 v168, 16, v100
	v_and_b32_e32 v169, 0xffff0000, v100
	v_pk_add_f32 v[126:127], v[126:127], v[168:169]
	v_lshlrev_b32_e32 v168, 16, v101
	v_and_b32_e32 v169, 0xffff0000, v101
	v_pk_add_f32 v[130:131], v[130:131], v[168:169]
	s_branch .LBB0_1611

.Lst_fi_22:
	s_cbranch_execz .Lst_fi_29
	v_mov_b32_e32 v156, v131
	v_mov_b32_e32 v165, v131
	v_mov_b32_e32 v164, v131
	v_mov_b32_e32 v163, v131
	v_mov_b32_e32 v162, v131
	v_mov_b32_e32 v167, v131
	v_mov_b32_e32 v166, v131
	v_mov_b32_e32 v161, v131
	v_mov_b32_e32 v160, v131

.Lst_fi_23:
	s_cbranch_execz .Lst_fi_30
	v_pk_fma_f32 v[54:55], v[54:55], v[158:159], v[138:139]
	v_mul_f32_e32 v138, v53, v53
	v_fmac_f32_e32 v138, v52, v52
	v_fmac_f32_e32 v138, v54, v54
	v_fmac_f32_e32 v138, v55, v55
	v_add_f32_e32 v144, v138, v150
	v_lshlrev_b32_e32 v138, 16, v132
	v_and_b32_e32 v139, 0xffff0000, v132
	v_lshlrev_b32_e32 v132, 16, v133
	v_and_b32_e32 v133, 0xffff0000, v133
	s_waitcnt vmcnt(8)
	v_pk_fma_f32 v[48:49], v[48:49], v[152:153], v[138:139]
	v_pk_fma_f32 v[50:51], v[50:51], v[154:155], v[132:133]
	v_mul_f32_e32 v132, v49, v49
	v_fmac_f32_e32 v132, v48, v48
	v_fmac_f32_e32 v132, v50, v50
	v_fmac_f32_e32 v132, v51, v51
	v_add_f32_e32 v138, v132, v144
	s_waitcnt vmcnt(5)
	v_lshlrev_b32_e32 v132, 16, v128
	v_and_b32_e32 v133, 0xffff0000, v128
	v_lshlrev_b32_e32 v128, 16, v129
	v_and_b32_e32 v129, 0xffff0000, v129
	v_pk_fma_f32 v[46:47], v[46:47], v[148:149], v[128:129]
	s_waitcnt vmcnt(4)
	v_lshlrev_b32_e32 v128, 16, v124
	v_and_b32_e32 v129, 0xffff0000, v124
	v_pk_fma_f32 v[44:45], v[44:45], v[146:147], v[132:133]
	v_pk_fma_f32 v[40:41], v[40:41], v[140:141], v[128:129]
	v_lshlrev_b32_e32 v124, 16, v125
	v_and_b32_e32 v125, 0xffff0000, v125
	v_mov_b32_e32 v128, v41
	v_mov_b32_e32 v129, v45
	v_pk_fma_f32 v[42:43], v[42:43], v[142:143], v[124:125]
	v_mov_b32_e32 v124, v40
.Lst_fi_24:
	s_cbranch_execz .Lst_fi_31
	v_mov_b32_e32 v125, v44
	v_pk_mul_f32 v[128:129], v[128:129], v[128:129]
	s_lshl_b64 s[20:21], s[2:3], 13
	v_pk_fma_f32 v[124:125], v[124:125], v[124:125], v[128:129]
	v_mov_b32_e32 v128, v42
	v_mov_b32_e32 v129, v46
	v_pk_fma_f32 v[124:125], v[128:129], v[128:129], v[124:125]
	v_mov_b32_e32 v128, v43
	v_mov_b32_e32 v129, v47
	v_pk_fma_f32 v[124:125], v[128:129], v[128:129], v[124:125]
	s_add_u32 s20, s68, s20
	v_add_f32_e32 v125, v125, v138
	v_add_f32_e32 v128, v124, v125
	s_waitcnt vmcnt(3)
	v_lshlrev_b32_e32 v124, 16, v122
	v_and_b32_e32 v125, 0xffff0000, v122
	v_lshlrev_b32_e32 v122, 16, v123
	v_and_b32_e32 v123, 0xffff0000, v123
	s_waitcnt vmcnt(1)
	v_pk_fma_f32 v[38:39], v[38:39], v[136:137], v[122:123]
	v_lshlrev_b32_e32 v122, 16, v120
	v_and_b32_e32 v123, 0xffff0000, v120
	v_pk_fma_f32 v[36:37], v[36:37], v[134:135], v[124:125]
	v_lshlrev_b32_e32 v120, 16, v121
	v_and_b32_e32 v121, 0xffff0000, v121
	s_waitcnt vmcnt(0)
	v_pk_fma_f32 v[122:123], v[32:33], v[126:127], v[122:123]
	v_pk_fma_f32 v[120:121], v[34:35], v[130:131], v[120:121]
	v_mov_b32_e32 v34, v123
	v_mov_b32_e32 v35, v37
	v_mov_b32_e32 v32, v122
	v_mov_b32_e32 v33, v36
	v_pk_mul_f32 v[34:35], v[34:35], v[34:35]
	s_addc_u32 s21, s69, s21
	v_pk_fma_f32 v[32:33], v[32:33], v[32:33], v[34:35]
.Lst_fi_25:
	s_cbranch_execz .Lst_fi_32
	v_mov_b32_e32 v34, v120
	v_mov_b32_e32 v35, v38
	v_pk_fma_f32 v[32:33], v[34:35], v[34:35], v[32:33]
	v_mov_b32_e32 v34, v121
	v_mov_b32_e32 v35, v39
	v_pk_fma_f32 v[32:33], v[34:35], v[34:35], v[32:33]
	s_cmpk_gt_i32 s18, 0x1fff
	v_add_f32_e32 v33, v33, v128
	v_add_f32_e32 v32, v32, v33
	ds_bpermute_b32 v33, v67, v32
	s_waitcnt lgkmcnt(0)
	v_add_f32_e32 v32, v32, v33
	ds_bpermute_b32 v33, v171, v32
	s_waitcnt lgkmcnt(0)
	v_add_f32_e32 v32, v32, v33
	ds_bpermute_b32 v33, v186, v32
	s_waitcnt lgkmcnt(0)
	v_add_f32_e32 v32, v32, v33
	ds_bpermute_b32 v33, v187, v32
	s_waitcnt lgkmcnt(0)
	v_add_f32_e32 v32, v32, v33
	ds_bpermute_b32 v33, v188, v32
	s_waitcnt lgkmcnt(0)
	v_add_f32_e32 v32, v32, v33
	ds_bpermute_b32 v33, v189, v32
	s_waitcnt lgkmcnt(0)
	v_add_f32_e32 v32, v32, v33
	v_fmamk_f32 v32, v32, 0x3a000000, v190
	v_mul_f32_e32 v33, 0x4b800000, v32
	v_cmp_gt_f32_e32 vcc, s33, v32
	s_nop 1
	v_cndmask_b32_e32 v32, v32, v33, vcc
	v_rsq_f32_e32 v32, v32
	s_nop 0
	v_mul_f32_e32 v33, 0x45800000, v32
	v_cndmask_b32_e32 v124, v32, v33, vcc
	v_pk_mul_f32 v[32:33], v[60:61], v[124:125] op_sel_hi:[1,0]
.Lst_fi_26:
	s_cbranch_execz .Lst_fi_33
	v_pk_mul_f32 v[34:35], v[62:63], v[124:125] op_sel_hi:[1,0]
	v_pk_mul_f32 v[32:33], v[0:1], v[32:33]
	v_pk_mul_f32 v[34:35], v[2:3], v[34:35]
	global_store_dwordx4 v64, v[32:35], s[20:21]
	v_lshl_add_u64 v[60:61], s[20:21], 0, v[64:65]
	s_nop 0
	v_pk_mul_f32 v[32:33], v[56:57], v[124:125] op_sel_hi:[1,0]
	v_pk_mul_f32 v[34:35], v[58:59], v[124:125] op_sel_hi:[1,0]
	v_pk_mul_f32 v[32:33], v[4:5], v[32:33]
	v_pk_mul_f32 v[34:35], v[6:7], v[34:35]
	global_store_dwordx4 v64, v[32:35], s[20:21] offset:1024
	s_nop 1
	v_pk_mul_f32 v[32:33], v[52:53], v[124:125] op_sel_hi:[1,0]
	v_pk_mul_f32 v[34:35], v[54:55], v[124:125] op_sel_hi:[1,0]
	v_pk_mul_f32 v[32:33], v[8:9], v[32:33]
	v_pk_mul_f32 v[34:35], v[10:11], v[34:35]
	global_store_dwordx4 v64, v[32:35], s[20:21] offset:2048
	s_nop 1
	v_pk_mul_f32 v[32:33], v[48:49], v[124:125] op_sel_hi:[1,0]
	v_pk_mul_f32 v[34:35], v[50:51], v[124:125] op_sel_hi:[1,0]
	v_pk_mul_f32 v[32:33], v[12:13], v[32:33]
	v_pk_mul_f32 v[34:35], v[14:15], v[34:35]
	global_store_dwordx4 v64, v[32:35], s[20:21] offset:3072
	s_nop 1
	v_pk_mul_f32 v[32:33], v[44:45], v[124:125] op_sel_hi:[1,0]
	v_pk_mul_f32 v[34:35], v[46:47], v[124:125] op_sel_hi:[1,0]
.Lst_fi_27:
	s_cbranch_execz .Lst_fi_34
	v_add_co_u32_e32 v44, vcc, s28, v60
	v_pk_mul_f32 v[34:35], v[18:19], v[34:35]
	v_pk_mul_f32 v[32:33], v[16:17], v[32:33]
	v_addc_co_u32_e32 v45, vcc, 0, v61, vcc
	global_store_dwordx4 v[44:45], v[32:35], off
	s_nop 1
	v_pk_mul_f32 v[32:33], v[40:41], v[124:125] op_sel_hi:[1,0]
	v_pk_mul_f32 v[34:35], v[42:43], v[124:125] op_sel_hi:[1,0]
	v_pk_mul_f32 v[32:33], v[20:21], v[32:33]
	v_pk_mul_f32 v[34:35], v[22:23], v[34:35]
	global_store_dwordx4 v[44:45], v[32:35], off offset:1024
	s_nop 1
	v_pk_mul_f32 v[32:33], v[36:37], v[124:125] op_sel_hi:[1,0]
	v_pk_mul_f32 v[34:35], v[38:39], v[124:125] op_sel_hi:[1,0]
	v_pk_mul_f32 v[32:33], v[24:25], v[32:33]
	v_pk_mul_f32 v[34:35], v[26:27], v[34:35]
	global_store_dwordx4 v[44:45], v[32:35], off offset:2048
	s_nop 1
	v_pk_mul_f32 v[32:33], v[122:123], v[124:125] op_sel_hi:[1,0]
	v_pk_mul_f32 v[34:35], v[120:121], v[124:125] op_sel_hi:[1,0]
	v_pk_mul_f32 v[32:33], v[28:29], v[32:33]
	v_pk_mul_f32 v[34:35], v[30:31], v[34:35]
	global_store_dwordx4 v[44:45], v[32:35], off offset:3072
	s_cbranch_scc1 .LBB0_1600
	s_ashr_i32 s19, s18, 31
	s_ashr_i32 s3, s18, 11
	s_lshl_b64 s[20:21], s[18:19], 12
	v_lshl_add_u64 v[32:33], v[68:69], 0, s[20:21]
	s_mul_i32 s20, s3, 0x3000
.Lst_fi_28:
	s_cbranch_execz .Lst_fi_35
	s_ashr_i32 s21, s20, 31
	s_lshl_b64 s[20:21], s[20:21], 2
	s_add_u32 s20, s70, s20
	s_addc_u32 s21, s71, s21
	v_lshl_add_u64 v[34:35], s[20:21], 0, v[64:65]
	v_add_co_u32_e32 v38, vcc, s31, v34
	v_lshl_add_u64 v[36:37], v[34:35], 0, s[12:13]
	s_nop 0
	v_addc_co_u32_e32 v39, vcc, 0, v35, vcc
	v_add_co_u32_e32 v34, vcc, 0x13000, v34
	global_load_dwordx4 v[56:59], v[36:37], off offset:1024
	global_load_dwordx4 v[52:55], v[36:37], off offset:2048
	global_load_dwordx2 v[150:151], v[32:33], off nt
	global_load_dwordx2 v[144:145], v[32:33], off offset:512 nt
	global_load_dwordx2 v[138:139], v[32:33], off offset:1024 nt
	global_load_dwordx2 v[132:133], v[32:33], off offset:1536 nt
	global_load_dwordx4 v[60:63], v[38:39], off
	global_load_dwordx4 v[48:51], v[36:37], off offset:3072
	v_addc_co_u32_e32 v35, vcc, 0, v35, vcc
	global_load_dwordx4 v[44:47], v[34:35], off
	global_load_dwordx4 v[40:43], v[34:35], off offset:1024
	global_load_dwordx2 v[128:129], v[32:33], off offset:2048 nt
	global_load_dwordx2 v[124:125], v[32:33], off offset:2560 nt
	global_load_dwordx2 v[122:123], v[32:33], off offset:3072 nt
	global_load_dwordx2 v[120:121], v[32:33], off offset:3584 nt
	global_load_dwordx4 v[36:39], v[34:35], off offset:2048
	s_nop 0
	global_load_dwordx4 v[32:35], v[34:35], off offset:3072
	v_cmp_lt_i32_e32 vcc, -1, v193
.Lst_fi_29:
	s_cbranch_execz .Lst_fi_36
	s_and_b32 s15, vcc_lo, 0xffff
	s_cmp_eq_u32 s15, 0
	s_cbranch_scc1 .LBB0_1653
	s_lshl_b32 s3, s3, 8
	v_mov_b32_e32 v160, 0
	s_ashr_i32 s6, s3, 31
	v_mov_b32_e32 v161, v160
	v_mov_b32_e32 v166, v160
	v_mov_b32_e32 v167, v160
	v_mov_b32_e32 v162, v160
	v_mov_b32_e32 v163, v160
	v_mov_b32_e32 v164, v160
	v_mov_b32_e32 v165, v160
	v_mov_b32_e32 v156, v160
	v_mov_b32_e32 v157, v160
	v_mov_b32_e32 v158, v160
	v_mov_b32_e32 v159, v160
	v_mov_b32_e32 v152, v160
	v_mov_b32_e32 v153, v160
	v_mov_b32_e32 v154, v160
	v_mov_b32_e32 v155, v160
	v_mov_b32_e32 v146, v160
	v_mov_b32_e32 v147, v160
	v_mov_b32_e32 v148, v160
	v_mov_b32_e32 v149, v160
	v_mov_b32_e32 v140, v160
	v_mov_b32_e32 v141, v160
	v_mov_b32_e32 v142, v160
	v_mov_b32_e32 v143, v160
	v_mov_b32_e32 v134, v160
	v_mov_b32_e32 v135, v160
	v_mov_b32_e32 v136, v160
	v_mov_b32_e32 v137, v160
	v_mov_b32_e32 v126, v160
	v_mov_b32_e32 v127, v160
	v_mov_b32_e32 v130, v160
	v_mov_b32_e32 v131, v160
	s_branch .LBB0_1635

.Lst_fi_30:
	s_cbranch_execz .Lst_fi_37
	s_cbranch_scc1 .LBB0_1652
	s_ff1_i32_b32 s17, s15
	s_add_i32 s20, s15, -1
	s_and_b32 s15, s20, s15
	v_readlane_b32 s20, v193, s17
	s_lshl_b32 s17, s17, 10
	s_add_u32 s17, s17, s3
	s_addc_u32 s21, 0, s6
	s_ashr_i32 s22, s20, 31
	s_add_u32 s20, s17, s20
	s_addc_u32 s21, s21, s22
	s_lshl_b64 s[20:21], s[20:21], 12
	s_add_u32 s22, s4, s20
	s_addc_u32 s23, s5, s21
	s_mov_b32 s17, 2
	s_cmp_eq_u32 s15, 0
	s_mov_b64 s[20:21], s[4:5]
	s_cbranch_scc1 .LBB0_1638

.Lst_fi_31:
	s_cbranch_execz .Lst_fi_38
	s_addc_u32 s27, s27, s34
	s_lshl_b64 s[26:27], s[26:27], 12
	s_add_u32 s26, s4, s26
	s_addc_u32 s27, s5, s27
	s_mov_b32 s17, 4

.Lst_fi_32:
	s_cbranch_execz .Lst_fi_39
	global_load_dwordx2 v[116:117], v118, s[22:23] offset:3072 nt
	s_nop 0
	global_load_dwordx2 v[118:119], v118, s[22:23] offset:3584 nt
	s_cmp_gt_u32 s17, 2
	s_cselect_b64 s[22:23], -1, 0
	s_cmp_lt_u32 s17, 3
	s_cbranch_scc0 .LBB0_1648

.Lst_fi_33:
	s_cbranch_execz .Lst_fi_40
	s_waitcnt vmcnt(5)
	v_lshlrev_b32_e32 v182, 16, v180
	v_and_b32_e32 v183, 0xffff0000, v180
	v_lshlrev_b32_e32 v180, 16, v181
	v_and_b32_e32 v181, 0xffff0000, v181
	v_pk_add_f32 v[158:159], v[158:159], v[180:181]
	s_waitcnt vmcnt(4)
	v_lshlrev_b32_e32 v180, 16, v178
	v_and_b32_e32 v181, 0xffff0000, v178
	v_lshlrev_b32_e32 v178, 16, v179
	v_and_b32_e32 v179, 0xffff0000, v179
	v_pk_add_f32 v[154:155], v[154:155], v[178:179]
	s_waitcnt vmcnt(3)
	v_lshlrev_b32_e32 v178, 16, v176
	v_and_b32_e32 v179, 0xffff0000, v176
	v_lshlrev_b32_e32 v176, 16, v177
	v_and_b32_e32 v177, 0xffff0000, v177
	v_pk_add_f32 v[148:149], v[148:149], v[176:177]
	s_waitcnt vmcnt(2)
	v_lshlrev_b32_e32 v176, 16, v174
	v_and_b32_e32 v177, 0xffff0000, v174
	v_lshlrev_b32_e32 v174, 16, v175
	v_and_b32_e32 v175, 0xffff0000, v175
	v_pk_add_f32 v[142:143], v[142:143], v[174:175]
	s_waitcnt vmcnt(1)
	v_lshlrev_b32_e32 v174, 16, v172
	v_and_b32_e32 v175, 0xffff0000, v172
	v_lshlrev_b32_e32 v172, 16, v173
	v_and_b32_e32 v173, 0xffff0000, v173
	v_pk_add_f32 v[136:137], v[136:137], v[172:173]
	s_waitcnt vmcnt(0)
	v_lshlrev_b32_e32 v172, 16, v168
	v_and_b32_e32 v173, 0xffff0000, v168
.Lst_fi_34:
	s_cbranch_execz .Lst_fi_41
	v_lshlrev_b32_e32 v168, 16, v169
	v_and_b32_e32 v169, 0xffff0000, v169
	v_pk_add_f32 v[160:161], v[160:161], v[194:195]
	v_pk_add_f32 v[162:163], v[162:163], v[184:185]
	v_pk_add_f32 v[156:157], v[156:157], v[182:183]
	v_pk_add_f32 v[152:153], v[152:153], v[180:181]
	v_pk_add_f32 v[146:147], v[146:147], v[178:179]
	v_pk_add_f32 v[140:141], v[140:141], v[176:177]
	v_pk_add_f32 v[134:135], v[134:135], v[174:175]
	v_pk_add_f32 v[126:127], v[126:127], v[172:173]
	s_andn2_b64 vcc, exec, s[24:25]
	v_pk_add_f32 v[130:131], v[130:131], v[168:169]
	s_cbranch_vccnz .LBB0_1649
	v_lshlrev_b32_e32 v168, 16, v90
	v_and_b32_e32 v169, 0xffff0000, v90
	v_pk_add_f32 v[160:161], v[160:161], v[168:169]
	v_lshlrev_b32_e32 v168, 16, v91
	v_and_b32_e32 v169, 0xffff0000, v91
	v_pk_add_f32 v[166:167], v[166:167], v[168:169]
	v_lshlrev_b32_e32 v168, 16, v96
	v_and_b32_e32 v169, 0xffff0000, v96
	v_pk_add_f32 v[162:163], v[162:163], v[168:169]
	v_lshlrev_b32_e32 v168, 16, v97
	v_and_b32_e32 v169, 0xffff0000, v97
	v_pk_add_f32 v[164:165], v[164:165], v[168:169]
	v_lshlrev_b32_e32 v168, 16, v102
	v_and_b32_e32 v169, 0xffff0000, v102
	v_pk_add_f32 v[156:157], v[156:157], v[168:169]
.Lst_fi_35:
	s_cbranch_execz .Lst_fi_42
	v_lshlrev_b32_e32 v168, 16, v103
	v_and_b32_e32 v169, 0xffff0000, v103
	v_pk_add_f32 v[158:159], v[158:159], v[168:169]
	v_lshlrev_b32_e32 v168, 16, v106
	v_and_b32_e32 v169, 0xffff0000, v106
	v_pk_add_f32 v[152:153], v[152:153], v[168:169]
	v_lshlrev_b32_e32 v168, 16, v107
	v_and_b32_e32 v169, 0xffff0000, v107
	v_pk_add_f32 v[154:155], v[154:155], v[168:169]
	v_lshlrev_b32_e32 v168, 16, v110
	v_and_b32_e32 v169, 0xffff0000, v110
	v_pk_add_f32 v[146:147], v[146:147], v[168:169]
	v_lshlrev_b32_e32 v168, 16, v111
	v_and_b32_e32 v169, 0xffff0000, v111
	v_pk_add_f32 v[148:149], v[148:149], v[168:169]
	v_lshlrev_b32_e32 v168, 16, v114
	v_and_b32_e32 v169, 0xffff0000, v114
	v_pk_add_f32 v[140:141], v[140:141], v[168:169]
	v_lshlrev_b32_e32 v168, 16, v115
	v_and_b32_e32 v169, 0xffff0000, v115
	v_pk_add_f32 v[142:143], v[142:143], v[168:169]
	v_lshlrev_b32_e32 v168, 16, v116
	v_and_b32_e32 v169, 0xffff0000, v116
	v_pk_add_f32 v[134:135], v[134:135], v[168:169]
	v_lshlrev_b32_e32 v168, 16, v117
	v_and_b32_e32 v169, 0xffff0000, v117
	v_pk_add_f32 v[136:137], v[136:137], v[168:169]
	v_lshlrev_b32_e32 v168, 16, v118
	v_and_b32_e32 v169, 0xffff0000, v118
.Lst_fi_36:
	s_cbranch_execz .Lst_fi_43
	v_pk_add_f32 v[126:127], v[126:127], v[168:169]
	v_lshlrev_b32_e32 v168, 16, v119
	v_and_b32_e32 v169, 0xffff0000, v119
	v_pk_add_f32 v[130:131], v[130:131], v[168:169]
	s_andn2_b64 vcc, exec, s[22:23]
	s_cbranch_vccz .LBB0_1650

.Lst_fi_37:
	s_cbranch_execz .Lst_fi_44
	v_pk_add_f32 v[166:167], v[166:167], v[168:169]
	v_lshlrev_b32_e32 v168, 16, v82
	v_and_b32_e32 v169, 0xffff0000, v82
	v_pk_add_f32 v[162:163], v[162:163], v[168:169]
	v_lshlrev_b32_e32 v168, 16, v83
	v_and_b32_e32 v169, 0xffff0000, v83
	v_pk_add_f32 v[164:165], v[164:165], v[168:169]
	v_lshlrev_b32_e32 v168, 16, v86
	v_and_b32_e32 v169, 0xffff0000, v86
	v_pk_add_f32 v[156:157], v[156:157], v[168:169]
	v_lshlrev_b32_e32 v168, 16, v87
	v_and_b32_e32 v169, 0xffff0000, v87
	v_pk_add_f32 v[158:159], v[158:159], v[168:169]
	v_lshlrev_b32_e32 v168, 16, v92
	v_and_b32_e32 v169, 0xffff0000, v92
	v_pk_add_f32 v[152:153], v[152:153], v[168:169]
	v_lshlrev_b32_e32 v168, 16, v93
	v_and_b32_e32 v169, 0xffff0000, v93
	v_pk_add_f32 v[154:155], v[154:155], v[168:169]
	v_lshlrev_b32_e32 v168, 16, v98
	v_and_b32_e32 v169, 0xffff0000, v98
	v_pk_add_f32 v[146:147], v[146:147], v[168:169]
	v_lshlrev_b32_e32 v168, 16, v99
	v_and_b32_e32 v169, 0xffff0000, v99
	v_pk_add_f32 v[148:149], v[148:149], v[168:169]
	v_lshlrev_b32_e32 v168, 16, v104
	v_and_b32_e32 v169, 0xffff0000, v104
	v_pk_add_f32 v[140:141], v[140:141], v[168:169]
	v_lshlrev_b32_e32 v168, 16, v105
.Lst_fi_38:
	s_cbranch_execz .Lst_fi_45
	v_and_b32_e32 v169, 0xffff0000, v105
	v_pk_add_f32 v[142:143], v[142:143], v[168:169]
	v_lshlrev_b32_e32 v168, 16, v108
	v_and_b32_e32 v169, 0xffff0000, v108
	v_pk_add_f32 v[134:135], v[134:135], v[168:169]
	v_lshlrev_b32_e32 v168, 16, v109
	v_and_b32_e32 v169, 0xffff0000, v109
	v_pk_add_f32 v[136:137], v[136:137], v[168:169]
	v_lshlrev_b32_e32 v168, 16, v112
	v_and_b32_e32 v169, 0xffff0000, v112
	v_pk_add_f32 v[126:127], v[126:127], v[168:169]
	v_lshlrev_b32_e32 v168, 16, v113
	v_and_b32_e32 v169, 0xffff0000, v113
	v_pk_add_f32 v[130:131], v[130:131], v[168:169]
	s_andn2_b64 vcc, exec, s[20:21]
	s_cbranch_vccnz .LBB0_1634

.Lst_fi_39:
	s_cbranch_execz .Lst_fi_46
	v_pk_add_f32 v[156:157], v[156:157], v[168:169]
	v_lshlrev_b32_e32 v168, 16, v77
	v_and_b32_e32 v169, 0xffff0000, v77
	v_pk_add_f32 v[158:159], v[158:159], v[168:169]
	v_lshlrev_b32_e32 v168, 16, v80
	v_and_b32_e32 v169, 0xffff0000, v80
	v_pk_add_f32 v[152:153], v[152:153], v[168:169]
	v_lshlrev_b32_e32 v168, 16, v81
	v_and_b32_e32 v169, 0xffff0000, v81
	v_pk_add_f32 v[154:155], v[154:155], v[168:169]
	v_lshlrev_b32_e32 v168, 16, v84
	v_and_b32_e32 v169, 0xffff0000, v84
	v_pk_add_f32 v[146:147], v[146:147], v[168:169]
	v_lshlrev_b32_e32 v168, 16, v85
	v_and_b32_e32 v169, 0xffff0000, v85
	v_pk_add_f32 v[148:149], v[148:149], v[168:169]
	v_lshlrev_b32_e32 v168, 16, v88
	v_and_b32_e32 v169, 0xffff0000, v88
	v_pk_add_f32 v[140:141], v[140:141], v[168:169]
	v_lshlrev_b32_e32 v168, 16, v89
	v_and_b32_e32 v169, 0xffff0000, v89
	v_pk_add_f32 v[142:143], v[142:143], v[168:169]
	v_lshlrev_b32_e32 v168, 16, v94
	v_and_b32_e32 v169, 0xffff0000, v94
	v_pk_add_f32 v[134:135], v[134:135], v[168:169]
	v_lshlrev_b32_e32 v168, 16, v95
	v_and_b32_e32 v169, 0xffff0000, v95
	v_pk_add_f32 v[136:137], v[136:137], v[168:169]
	v_lshlrev_b32_e32 v168, 16, v100
.Lst_fi_40:
	s_cbranch_execz .Lst_fi_47
	v_and_b32_e32 v169, 0xffff0000, v100
	v_pk_add_f32 v[126:127], v[126:127], v[168:169]
	v_lshlrev_b32_e32 v168, 16, v101
	v_and_b32_e32 v169, 0xffff0000, v101
	v_pk_add_f32 v[130:131], v[130:131], v[168:169]
	s_branch .LBB0_1634

.Lst_fi_41:
	s_cbranch_execz .Lst_fi_48
	v_mov_b32_e32 v160, v131

.Lst_fi_42:
	s_cbranch_execz .Lst_fi_49
	v_and_b32_e32 v139, 0xffff0000, v132
	v_lshlrev_b32_e32 v132, 16, v133
	v_and_b32_e32 v133, 0xffff0000, v133
	s_waitcnt vmcnt(8)
	v_pk_fma_f32 v[48:49], v[48:49], v[152:153], v[138:139]
	v_pk_fma_f32 v[50:51], v[50:51], v[154:155], v[132:133]
	v_mul_f32_e32 v132, v49, v49
	v_fmac_f32_e32 v132, v48, v48
	v_fmac_f32_e32 v132, v50, v50
	v_fmac_f32_e32 v132, v51, v51
	v_add_f32_e32 v138, v132, v144
	s_waitcnt vmcnt(5)
	v_lshlrev_b32_e32 v132, 16, v128
	v_and_b32_e32 v133, 0xffff0000, v128
	v_lshlrev_b32_e32 v128, 16, v129
	v_and_b32_e32 v129, 0xffff0000, v129
	v_pk_fma_f32 v[46:47], v[46:47], v[148:149], v[128:129]
	s_waitcnt vmcnt(4)
	v_lshlrev_b32_e32 v128, 16, v124
	v_and_b32_e32 v129, 0xffff0000, v124
	v_pk_fma_f32 v[44:45], v[44:45], v[146:147], v[132:133]
	v_pk_fma_f32 v[40:41], v[40:41], v[140:141], v[128:129]
	v_lshlrev_b32_e32 v124, 16, v125
	v_and_b32_e32 v125, 0xffff0000, v125
	v_mov_b32_e32 v128, v41
	v_mov_b32_e32 v129, v45
	v_pk_fma_f32 v[42:43], v[42:43], v[142:143], v[124:125]
	v_mov_b32_e32 v124, v40
	v_mov_b32_e32 v125, v44
	v_pk_mul_f32 v[128:129], v[128:129], v[128:129]
	s_lshl_b64 s[18:19], s[18:19], 13
	v_pk_fma_f32 v[124:125], v[124:125], v[124:125], v[128:129]
	v_mov_b32_e32 v128, v42
	v_mov_b32_e32 v129, v46
.Lst_fi_43:
	s_cbranch_execz .Lst_fi_50
	v_pk_fma_f32 v[124:125], v[128:129], v[128:129], v[124:125]
	v_mov_b32_e32 v128, v43
	v_mov_b32_e32 v129, v47
	v_pk_fma_f32 v[124:125], v[128:129], v[128:129], v[124:125]
	s_add_u32 s18, s68, s18
	v_add_f32_e32 v125, v125, v138
	v_add_f32_e32 v128, v124, v125
	s_waitcnt vmcnt(3)
	v_lshlrev_b32_e32 v124, 16, v122
	v_and_b32_e32 v125, 0xffff0000, v122
	v_lshlrev_b32_e32 v122, 16, v123
	v_and_b32_e32 v123, 0xffff0000, v123
	s_waitcnt vmcnt(1)
	v_pk_fma_f32 v[38:39], v[38:39], v[136:137], v[122:123]
	v_lshlrev_b32_e32 v122, 16, v120
	v_and_b32_e32 v123, 0xffff0000, v120
	v_pk_fma_f32 v[36:37], v[36:37], v[134:135], v[124:125]
	v_lshlrev_b32_e32 v120, 16, v121
	v_and_b32_e32 v121, 0xffff0000, v121
	s_waitcnt vmcnt(0)
	v_pk_fma_f32 v[122:123], v[32:33], v[126:127], v[122:123]
	v_pk_fma_f32 v[120:121], v[34:35], v[130:131], v[120:121]
	v_mov_b32_e32 v34, v123
	v_mov_b32_e32 v35, v37
	v_mov_b32_e32 v32, v122
	v_mov_b32_e32 v33, v36
	v_pk_mul_f32 v[34:35], v[34:35], v[34:35]
	s_addc_u32 s19, s69, s19
	v_pk_fma_f32 v[32:33], v[32:33], v[32:33], v[34:35]
	v_mov_b32_e32 v34, v120
	v_mov_b32_e32 v35, v38
	v_pk_fma_f32 v[32:33], v[34:35], v[34:35], v[32:33]
	v_mov_b32_e32 v34, v121
	v_mov_b32_e32 v35, v39
	v_pk_fma_f32 v[32:33], v[34:35], v[34:35], v[32:33]
.Lst_fi_44:
	s_cbranch_execz .Lst_fi_51
	s_cmpk_gt_i32 s16, 0x1fff
	v_add_f32_e32 v33, v33, v128
	v_add_f32_e32 v32, v32, v33
	ds_bpermute_b32 v33, v67, v32
	s_waitcnt lgkmcnt(0)
	v_add_f32_e32 v32, v32, v33
	ds_bpermute_b32 v33, v171, v32
	s_waitcnt lgkmcnt(0)
	v_add_f32_e32 v32, v32, v33
	ds_bpermute_b32 v33, v186, v32
	s_waitcnt lgkmcnt(0)
	v_add_f32_e32 v32, v32, v33
	ds_bpermute_b32 v33, v187, v32
	s_waitcnt lgkmcnt(0)
	v_add_f32_e32 v32, v32, v33
	ds_bpermute_b32 v33, v188, v32
	s_waitcnt lgkmcnt(0)
	v_add_f32_e32 v32, v32, v33
	ds_bpermute_b32 v33, v189, v32
	s_waitcnt lgkmcnt(0)
	v_add_f32_e32 v32, v32, v33
	v_fmamk_f32 v32, v32, 0x3a000000, v190
	v_mul_f32_e32 v33, 0x4b800000, v32
	v_cmp_gt_f32_e32 vcc, s33, v32
	s_nop 1
	v_cndmask_b32_e32 v32, v32, v33, vcc
	v_rsq_f32_e32 v32, v32
	s_nop 0
	v_mul_f32_e32 v33, 0x45800000, v32
	v_cndmask_b32_e32 v124, v32, v33, vcc
	v_pk_mul_f32 v[32:33], v[60:61], v[124:125] op_sel_hi:[1,0]
	v_pk_mul_f32 v[34:35], v[62:63], v[124:125] op_sel_hi:[1,0]
	v_pk_mul_f32 v[32:33], v[0:1], v[32:33]
	v_pk_mul_f32 v[34:35], v[2:3], v[34:35]
	global_store_dwordx4 v64, v[32:35], s[18:19]
.Lst_fi_45:
	s_cbranch_execz .Lst_fi_52
	v_lshl_add_u64 v[60:61], s[18:19], 0, v[64:65]
	s_nop 0
	v_pk_mul_f32 v[32:33], v[56:57], v[124:125] op_sel_hi:[1,0]
	v_pk_mul_f32 v[34:35], v[58:59], v[124:125] op_sel_hi:[1,0]
	v_pk_mul_f32 v[32:33], v[4:5], v[32:33]
	v_pk_mul_f32 v[34:35], v[6:7], v[34:35]
	global_store_dwordx4 v64, v[32:35], s[18:19] offset:1024
	s_nop 1
	v_pk_mul_f32 v[32:33], v[52:53], v[124:125] op_sel_hi:[1,0]
	v_pk_mul_f32 v[34:35], v[54:55], v[124:125] op_sel_hi:[1,0]
	v_pk_mul_f32 v[32:33], v[8:9], v[32:33]
	v_pk_mul_f32 v[34:35], v[10:11], v[34:35]
	global_store_dwordx4 v64, v[32:35], s[18:19] offset:2048
	s_nop 1
	v_pk_mul_f32 v[32:33], v[48:49], v[124:125] op_sel_hi:[1,0]
	v_pk_mul_f32 v[34:35], v[50:51], v[124:125] op_sel_hi:[1,0]
	v_pk_mul_f32 v[32:33], v[12:13], v[32:33]
	v_pk_mul_f32 v[34:35], v[14:15], v[34:35]
	global_store_dwordx4 v64, v[32:35], s[18:19] offset:3072
	s_nop 1
	v_pk_mul_f32 v[32:33], v[44:45], v[124:125] op_sel_hi:[1,0]
	v_pk_mul_f32 v[34:35], v[46:47], v[124:125] op_sel_hi:[1,0]
	v_add_co_u32_e32 v44, vcc, s28, v60
	v_pk_mul_f32 v[34:35], v[18:19], v[34:35]
	v_pk_mul_f32 v[32:33], v[16:17], v[32:33]
	v_addc_co_u32_e32 v45, vcc, 0, v61, vcc
	global_store_dwordx4 v[44:45], v[32:35], off
.Lst_fi_46:
	s_cbranch_execz .Lst_fi_53
	s_nop 1
	v_pk_mul_f32 v[32:33], v[40:41], v[124:125] op_sel_hi:[1,0]
	v_pk_mul_f32 v[34:35], v[42:43], v[124:125] op_sel_hi:[1,0]
	v_pk_mul_f32 v[32:33], v[20:21], v[32:33]
	v_pk_mul_f32 v[34:35], v[22:23], v[34:35]
	global_store_dwordx4 v[44:45], v[32:35], off offset:1024
	s_nop 1
	v_pk_mul_f32 v[32:33], v[36:37], v[124:125] op_sel_hi:[1,0]
	v_pk_mul_f32 v[34:35], v[38:39], v[124:125] op_sel_hi:[1,0]
	v_pk_mul_f32 v[32:33], v[24:25], v[32:33]
	v_pk_mul_f32 v[34:35], v[26:27], v[34:35]
	global_store_dwordx4 v[44:45], v[32:35], off offset:2048
	s_nop 1
	v_pk_mul_f32 v[32:33], v[122:123], v[124:125] op_sel_hi:[1,0]
	v_pk_mul_f32 v[34:35], v[120:121], v[124:125] op_sel_hi:[1,0]
	v_pk_mul_f32 v[32:33], v[28:29], v[32:33]
	v_pk_mul_f32 v[34:35], v[30:31], v[34:35]
	global_store_dwordx4 v[44:45], v[32:35], off offset:3072
	s_cbranch_scc1 .LBB0_1600
	s_ashr_i32 s17, s16, 31
	s_ashr_i32 s3, s16, 11
	s_lshl_b64 s[18:19], s[16:17], 12
	v_lshl_add_u64 v[32:33], v[68:69], 0, s[18:19]
	s_mul_i32 s18, s3, 0x3000
	s_ashr_i32 s19, s18, 31
	s_lshl_b64 s[18:19], s[18:19], 2
	s_add_u32 s18, s70, s18
	s_addc_u32 s19, s71, s19
	v_lshl_add_u64 v[34:35], s[18:19], 0, v[64:65]
	v_add_co_u32_e32 v38, vcc, s31, v34
.Lst_fi_47:
	s_cbranch_execz .Lst_fi_54
	v_lshl_add_u64 v[36:37], v[34:35], 0, s[12:13]
	s_nop 0
	v_addc_co_u32_e32 v39, vcc, 0, v35, vcc
	v_add_co_u32_e32 v34, vcc, 0x13000, v34
	global_load_dwordx4 v[56:59], v[36:37], off offset:1024
	global_load_dwordx4 v[52:55], v[36:37], off offset:2048
	global_load_dwordx2 v[150:151], v[32:33], off nt
	global_load_dwordx2 v[144:145], v[32:33], off offset:512 nt
	global_load_dwordx2 v[138:139], v[32:33], off offset:1024 nt
	global_load_dwordx2 v[132:133], v[32:33], off offset:1536 nt
	global_load_dwordx4 v[60:63], v[38:39], off
	global_load_dwordx4 v[48:51], v[36:37], off offset:3072
	v_addc_co_u32_e32 v35, vcc, 0, v35, vcc
	global_load_dwordx4 v[44:47], v[34:35], off
	global_load_dwordx4 v[40:43], v[34:35], off offset:1024
	global_load_dwordx2 v[128:129], v[32:33], off offset:2048 nt
	global_load_dwordx2 v[124:125], v[32:33], off offset:2560 nt
	global_load_dwordx2 v[122:123], v[32:33], off offset:3072 nt
	global_load_dwordx2 v[120:121], v[32:33], off offset:3584 nt
	global_load_dwordx4 v[36:39], v[34:35], off offset:2048
	s_nop 0
	global_load_dwordx4 v[32:35], v[34:35], off offset:3072
	v_cmp_lt_i32_e32 vcc, -1, v192
	s_and_b32 s15, vcc_lo, 0xffff
	s_cmp_eq_u32 s15, 0
	s_cbranch_scc1 .LBB0_1676
	s_lshl_b32 s3, s3, 8
	v_mov_b32_e32 v160, 0
	s_ashr_i32 s6, s3, 31
.Lst_fi_48:
	s_cbranch_execz .Lst_fi_55
	v_mov_b32_e32 v161, v160
	v_mov_b32_e32 v166, v160
	v_mov_b32_e32 v167, v160
	v_mov_b32_e32 v162, v160
	v_mov_b32_e32 v163, v160
	v_mov_b32_e32 v164, v160
	v_mov_b32_e32 v165, v160
	v_mov_b32_e32 v156, v160
	v_mov_b32_e32 v157, v160
	v_mov_b32_e32 v158, v160
	v_mov_b32_e32 v159, v160
	v_mov_b32_e32 v152, v160
	v_mov_b32_e32 v153, v160
	v_mov_b32_e32 v154, v160
	v_mov_b32_e32 v155, v160
	v_mov_b32_e32 v146, v160
	v_mov_b32_e32 v147, v160
	v_mov_b32_e32 v148, v160
	v_mov_b32_e32 v149, v160
	v_mov_b32_e32 v140, v160
	v_mov_b32_e32 v141, v160
	v_mov_b32_e32 v142, v160
	v_mov_b32_e32 v143, v160
	v_mov_b32_e32 v134, v160
	v_mov_b32_e32 v135, v160
	v_mov_b32_e32 v136, v160
	v_mov_b32_e32 v137, v160
	v_mov_b32_e32 v126, v160
	v_mov_b32_e32 v127, v160
	v_mov_b32_e32 v130, v160
	v_mov_b32_e32 v131, v160
	s_branch .LBB0_1658

.Lst_fi_49:
	s_cbranch_execz .Lst_fi_56
	s_add_u32 s18, s18, s3
	s_addc_u32 s20, 0, s6
	s_ashr_i32 s21, s19, 31
	s_add_u32 s18, s18, s19
	s_addc_u32 s19, s20, s21
	s_lshl_b64 s[18:19], s[18:19], 12
	s_add_u32 s20, s4, s18
	s_addc_u32 s21, s5, s19
	s_mov_b32 s26, 2
	s_cmp_eq_u32 s15, 0
	s_mov_b64 s[18:19], s[4:5]
	s_cbranch_scc1 .LBB0_1661

.Lst_fi_50:
	s_cbranch_execz .Lst_fi_57
	s_addc_u32 s27, 0, s6
	s_ashr_i32 s34, s22, 31
	s_add_u32 s22, s23, s22
	s_addc_u32 s23, s27, s34
	s_lshl_b64 s[22:23], s[22:23], 12
	v_lshl_add_u64 v[168:169], v[70:71], 0, s[22:23]
	global_load_dwordx2 v[184:185], v[168:169], off nt
	global_load_dwordx2 v[182:183], v[168:169], off offset:512 nt
	global_load_dwordx2 v[180:181], v[168:169], off offset:1024 nt
	global_load_dwordx2 v[178:179], v[168:169], off offset:1536 nt
	global_load_dwordx2 v[176:177], v[168:169], off offset:2048 nt
	global_load_dwordx2 v[174:175], v[168:169], off offset:2560 nt
	global_load_dwordx2 v[172:173], v[168:169], off offset:3072 nt
	s_nop 0
	global_load_dwordx2 v[168:169], v[168:169], off offset:3584 nt
	s_cmp_gt_u32 s26, 1
	s_cselect_b64 s[22:23], -1, 0
	s_cmp_lt_u32 s26, 2
	s_cbranch_scc1 .LBB0_1670
	v_lshlrev_b32_e32 v118, 1, v66
	global_load_dwordx2 v[90:91], v118, s[20:21] nt
	global_load_dwordx2 v[96:97], v118, s[20:21] offset:512 nt
	global_load_dwordx2 v[102:103], v118, s[20:21] offset:1024 nt
	global_load_dwordx2 v[106:107], v118, s[20:21] offset:1536 nt
	global_load_dwordx2 v[110:111], v118, s[20:21] offset:2048 nt
	global_load_dwordx2 v[114:115], v118, s[20:21] offset:2560 nt
	global_load_dwordx2 v[116:117], v118, s[20:21] offset:3072 nt
	s_nop 0
	global_load_dwordx2 v[118:119], v118, s[20:21] offset:3584 nt
	s_cmp_gt_u32 s26, 2
	s_cselect_b64 s[20:21], -1, 0
.Lst_fi_51:
	s_cbranch_execz .Lst_fi_58
	s_cmp_lt_u32 s26, 3
	s_cbranch_scc0 .LBB0_1671

.Lst_fi_52:
	s_cbranch_execz .Lst_fi_59
	v_pk_add_f32 v[158:159], v[158:159], v[180:181]
	s_waitcnt vmcnt(4)
	v_lshlrev_b32_e32 v180, 16, v178
	v_and_b32_e32 v181, 0xffff0000, v178
	v_lshlrev_b32_e32 v178, 16, v179
	v_and_b32_e32 v179, 0xffff0000, v179
	v_pk_add_f32 v[154:155], v[154:155], v[178:179]
	s_waitcnt vmcnt(3)
	v_lshlrev_b32_e32 v178, 16, v176
	v_and_b32_e32 v179, 0xffff0000, v176
	v_lshlrev_b32_e32 v176, 16, v177
	v_and_b32_e32 v177, 0xffff0000, v177
	v_pk_add_f32 v[148:149], v[148:149], v[176:177]
	s_waitcnt vmcnt(2)
	v_lshlrev_b32_e32 v176, 16, v174
	v_and_b32_e32 v177, 0xffff0000, v174
	v_lshlrev_b32_e32 v174, 16, v175
	v_and_b32_e32 v175, 0xffff0000, v175
	v_pk_add_f32 v[142:143], v[142:143], v[174:175]
	s_waitcnt vmcnt(1)
	v_lshlrev_b32_e32 v174, 16, v172
	v_and_b32_e32 v175, 0xffff0000, v172
	v_lshlrev_b32_e32 v172, 16, v173
	v_and_b32_e32 v173, 0xffff0000, v173
	v_pk_add_f32 v[136:137], v[136:137], v[172:173]
	s_waitcnt vmcnt(0)
	v_lshlrev_b32_e32 v172, 16, v168
	v_and_b32_e32 v173, 0xffff0000, v168
	v_lshlrev_b32_e32 v168, 16, v169
	v_and_b32_e32 v169, 0xffff0000, v169
	v_pk_add_f32 v[160:161], v[160:161], v[194:195]
	v_pk_add_f32 v[162:163], v[162:163], v[184:185]
.Lst_fi_53:
	s_cbranch_execz .Lst_fi_60
	v_pk_add_f32 v[156:157], v[156:157], v[182:183]
	v_pk_add_f32 v[152:153], v[152:153], v[180:181]
	v_pk_add_f32 v[146:147], v[146:147], v[178:179]
	v_pk_add_f32 v[140:141], v[140:141], v[176:177]
	v_pk_add_f32 v[134:135], v[134:135], v[174:175]
	v_pk_add_f32 v[126:127], v[126:127], v[172:173]
	s_andn2_b64 vcc, exec, s[22:23]
	v_pk_add_f32 v[130:131], v[130:131], v[168:169]
	s_cbranch_vccnz .LBB0_1672
	v_lshlrev_b32_e32 v168, 16, v90
	v_and_b32_e32 v169, 0xffff0000, v90
	v_pk_add_f32 v[160:161], v[160:161], v[168:169]
	v_lshlrev_b32_e32 v168, 16, v91
	v_and_b32_e32 v169, 0xffff0000, v91
	v_pk_add_f32 v[166:167], v[166:167], v[168:169]
	v_lshlrev_b32_e32 v168, 16, v96
	v_and_b32_e32 v169, 0xffff0000, v96
	v_pk_add_f32 v[162:163], v[162:163], v[168:169]
	v_lshlrev_b32_e32 v168, 16, v97
	v_and_b32_e32 v169, 0xffff0000, v97
	v_pk_add_f32 v[164:165], v[164:165], v[168:169]
	v_lshlrev_b32_e32 v168, 16, v102
	v_and_b32_e32 v169, 0xffff0000, v102
	v_pk_add_f32 v[156:157], v[156:157], v[168:169]
	v_lshlrev_b32_e32 v168, 16, v103
	v_and_b32_e32 v169, 0xffff0000, v103
	v_pk_add_f32 v[158:159], v[158:159], v[168:169]
	v_lshlrev_b32_e32 v168, 16, v106
	v_and_b32_e32 v169, 0xffff0000, v106
.Lst_fi_54:
	s_cbranch_execz .Lst_fi_61
	v_pk_add_f32 v[152:153], v[152:153], v[168:169]
	v_lshlrev_b32_e32 v168, 16, v107
	v_and_b32_e32 v169, 0xffff0000, v107
	v_pk_add_f32 v[154:155], v[154:155], v[168:169]
	v_lshlrev_b32_e32 v168, 16, v110
	v_and_b32_e32 v169, 0xffff0000, v110
	v_pk_add_f32 v[146:147], v[146:147], v[168:169]
	v_lshlrev_b32_e32 v168, 16, v111
	v_and_b32_e32 v169, 0xffff0000, v111
	v_pk_add_f32 v[148:149], v[148:149], v[168:169]
	v_lshlrev_b32_e32 v168, 16, v114
	v_and_b32_e32 v169, 0xffff0000, v114
	v_pk_add_f32 v[140:141], v[140:141], v[168:169]
	v_lshlrev_b32_e32 v168, 16, v115
	v_and_b32_e32 v169, 0xffff0000, v115
	v_pk_add_f32 v[142:143], v[142:143], v[168:169]
	v_lshlrev_b32_e32 v168, 16, v116
	v_and_b32_e32 v169, 0xffff0000, v116
	v_pk_add_f32 v[134:135], v[134:135], v[168:169]
	v_lshlrev_b32_e32 v168, 16, v117
	v_and_b32_e32 v169, 0xffff0000, v117
	v_pk_add_f32 v[136:137], v[136:137], v[168:169]
	v_lshlrev_b32_e32 v168, 16, v118
	v_and_b32_e32 v169, 0xffff0000, v118
	v_pk_add_f32 v[126:127], v[126:127], v[168:169]
	v_lshlrev_b32_e32 v168, 16, v119
	v_and_b32_e32 v169, 0xffff0000, v119
	v_pk_add_f32 v[130:131], v[130:131], v[168:169]
	s_andn2_b64 vcc, exec, s[20:21]
.Lst_fi_55:
	s_cbranch_execz .Lst_fi_62
	s_cbranch_vccz .LBB0_1673

.Lst_fi_56:
	s_cbranch_execz .Lst_fi_63
	v_lshlrev_b32_e32 v168, 16, v83
	v_and_b32_e32 v169, 0xffff0000, v83
	v_pk_add_f32 v[164:165], v[164:165], v[168:169]
	v_lshlrev_b32_e32 v168, 16, v86
	v_and_b32_e32 v169, 0xffff0000, v86
	v_pk_add_f32 v[156:157], v[156:157], v[168:169]
	v_lshlrev_b32_e32 v168, 16, v87
	v_and_b32_e32 v169, 0xffff0000, v87
	v_pk_add_f32 v[158:159], v[158:159], v[168:169]
	v_lshlrev_b32_e32 v168, 16, v92
	v_and_b32_e32 v169, 0xffff0000, v92
	v_pk_add_f32 v[152:153], v[152:153], v[168:169]
	v_lshlrev_b32_e32 v168, 16, v93
	v_and_b32_e32 v169, 0xffff0000, v93
	v_pk_add_f32 v[154:155], v[154:155], v[168:169]
	v_lshlrev_b32_e32 v168, 16, v98
	v_and_b32_e32 v169, 0xffff0000, v98
	v_pk_add_f32 v[146:147], v[146:147], v[168:169]
	v_lshlrev_b32_e32 v168, 16, v99
	v_and_b32_e32 v169, 0xffff0000, v99
	v_pk_add_f32 v[148:149], v[148:149], v[168:169]
	v_lshlrev_b32_e32 v168, 16, v104
	v_and_b32_e32 v169, 0xffff0000, v104
	v_pk_add_f32 v[140:141], v[140:141], v[168:169]
	v_lshlrev_b32_e32 v168, 16, v105
	v_and_b32_e32 v169, 0xffff0000, v105
	v_pk_add_f32 v[142:143], v[142:143], v[168:169]
	v_lshlrev_b32_e32 v168, 16, v108
	v_and_b32_e32 v169, 0xffff0000, v108
.Lst_fi_57:
	s_cbranch_execz .Lst_fi_64
	v_pk_add_f32 v[134:135], v[134:135], v[168:169]
	v_lshlrev_b32_e32 v168, 16, v109
	v_and_b32_e32 v169, 0xffff0000, v109
	v_pk_add_f32 v[136:137], v[136:137], v[168:169]
	v_lshlrev_b32_e32 v168, 16, v112
	v_and_b32_e32 v169, 0xffff0000, v112
	v_pk_add_f32 v[126:127], v[126:127], v[168:169]
	v_lshlrev_b32_e32 v168, 16, v113
	v_and_b32_e32 v169, 0xffff0000, v113
	v_pk_add_f32 v[130:131], v[130:131], v[168:169]
	s_andn2_b64 vcc, exec, s[18:19]
	s_cbranch_vccnz .LBB0_1657

.Lst_fi_58:
	s_cbranch_execz .Lst_fi_65
	v_lshlrev_b32_e32 v168, 16, v80
	v_and_b32_e32 v169, 0xffff0000, v80
	v_pk_add_f32 v[152:153], v[152:153], v[168:169]
	v_lshlrev_b32_e32 v168, 16, v81
	v_and_b32_e32 v169, 0xffff0000, v81
	v_pk_add_f32 v[154:155], v[154:155], v[168:169]
	v_lshlrev_b32_e32 v168, 16, v84
	v_and_b32_e32 v169, 0xffff0000, v84
	v_pk_add_f32 v[146:147], v[146:147], v[168:169]
	v_lshlrev_b32_e32 v168, 16, v85
	v_and_b32_e32 v169, 0xffff0000, v85
	v_pk_add_f32 v[148:149], v[148:149], v[168:169]
	v_lshlrev_b32_e32 v168, 16, v88
	v_and_b32_e32 v169, 0xffff0000, v88
	v_pk_add_f32 v[140:141], v[140:141], v[168:169]
	v_lshlrev_b32_e32 v168, 16, v89
	v_and_b32_e32 v169, 0xffff0000, v89
	v_pk_add_f32 v[142:143], v[142:143], v[168:169]
	v_lshlrev_b32_e32 v168, 16, v94
	v_and_b32_e32 v169, 0xffff0000, v94
	v_pk_add_f32 v[134:135], v[134:135], v[168:169]
	v_lshlrev_b32_e32 v168, 16, v95
	v_and_b32_e32 v169, 0xffff0000, v95
	v_pk_add_f32 v[136:137], v[136:137], v[168:169]
	v_lshlrev_b32_e32 v168, 16, v100
	v_and_b32_e32 v169, 0xffff0000, v100
	v_pk_add_f32 v[126:127], v[126:127], v[168:169]
	v_lshlrev_b32_e32 v168, 16, v101
	v_and_b32_e32 v169, 0xffff0000, v101
.Lst_fi_59:
	s_cbranch_execz .Lst_fi_66
	v_pk_add_f32 v[130:131], v[130:131], v[168:169]
	s_branch .LBB0_1657

.Lst_fi_60:
	s_cbranch_execz .Lst_fi_67
	s_waitcnt vmcnt(9)
	v_pk_fma_f32 v[62:63], v[62:63], v[166:167], v[150:151]
	v_lshlrev_b32_e32 v150, 16, v144
	v_and_b32_e32 v151, 0xffff0000, v144
	v_pk_fma_f32 v[60:61], v[60:61], v[160:161], v[168:169]
	v_lshlrev_b32_e32 v144, 16, v145
	v_and_b32_e32 v145, 0xffff0000, v145
	v_pk_fma_f32 v[56:57], v[56:57], v[162:163], v[150:151]
	v_mul_f32_e32 v160, v61, v61
	v_pk_fma_f32 v[58:59], v[58:59], v[164:165], v[144:145]
	v_mul_f32_e32 v144, v57, v57
	v_fmac_f32_e32 v160, v60, v60
	v_fmac_f32_e32 v144, v56, v56
	v_fmac_f32_e32 v160, v62, v62
	v_fmac_f32_e32 v144, v58, v58
	v_fmac_f32_e32 v160, v63, v63
	v_fmac_f32_e32 v144, v59, v59
	v_add_f32_e32 v150, v160, v144
	v_lshlrev_b32_e32 v144, 16, v138
	v_and_b32_e32 v145, 0xffff0000, v138
	v_lshlrev_b32_e32 v138, 16, v139
	v_and_b32_e32 v139, 0xffff0000, v139
	v_pk_fma_f32 v[52:53], v[52:53], v[156:157], v[144:145]
	v_pk_fma_f32 v[54:55], v[54:55], v[158:159], v[138:139]
	v_mul_f32_e32 v138, v53, v53
	v_fmac_f32_e32 v138, v52, v52
	v_fmac_f32_e32 v138, v54, v54
	v_fmac_f32_e32 v138, v55, v55
	v_add_f32_e32 v144, v138, v150
	v_lshlrev_b32_e32 v138, 16, v132
	v_and_b32_e32 v139, 0xffff0000, v132
	v_lshlrev_b32_e32 v132, 16, v133
	v_and_b32_e32 v133, 0xffff0000, v133
	s_waitcnt vmcnt(8)
	v_pk_fma_f32 v[48:49], v[48:49], v[152:153], v[138:139]
.Lst_fi_61:
	s_cbranch_execz .Lst_fi_68
	v_pk_fma_f32 v[50:51], v[50:51], v[154:155], v[132:133]
	v_mul_f32_e32 v132, v49, v49
	v_fmac_f32_e32 v132, v48, v48
	v_fmac_f32_e32 v132, v50, v50
	v_fmac_f32_e32 v132, v51, v51
	v_add_f32_e32 v138, v132, v144
	s_waitcnt vmcnt(5)
	v_lshlrev_b32_e32 v132, 16, v128
	v_and_b32_e32 v133, 0xffff0000, v128
	v_lshlrev_b32_e32 v128, 16, v129
	v_and_b32_e32 v129, 0xffff0000, v129
	v_pk_fma_f32 v[46:47], v[46:47], v[148:149], v[128:129]
	s_waitcnt vmcnt(4)
	v_lshlrev_b32_e32 v128, 16, v124
	v_and_b32_e32 v129, 0xffff0000, v124
	v_pk_fma_f32 v[44:45], v[44:45], v[146:147], v[132:133]
	v_pk_fma_f32 v[40:41], v[40:41], v[140:141], v[128:129]
	v_lshlrev_b32_e32 v124, 16, v125
	v_and_b32_e32 v125, 0xffff0000, v125
	v_mov_b32_e32 v128, v41
	v_mov_b32_e32 v129, v45
	v_pk_fma_f32 v[42:43], v[42:43], v[142:143], v[124:125]
	v_mov_b32_e32 v124, v40
	v_mov_b32_e32 v125, v44
	v_pk_mul_f32 v[128:129], v[128:129], v[128:129]
	s_lshl_b64 s[16:17], s[16:17], 13
	v_pk_fma_f32 v[124:125], v[124:125], v[124:125], v[128:129]
	v_mov_b32_e32 v128, v42
	v_mov_b32_e32 v129, v46
	v_pk_fma_f32 v[124:125], v[128:129], v[128:129], v[124:125]
	v_mov_b32_e32 v128, v43
	v_mov_b32_e32 v129, v47
	v_pk_fma_f32 v[124:125], v[128:129], v[128:129], v[124:125]
	s_add_u32 s16, s68, s16
	v_add_f32_e32 v125, v125, v138
.Lst_fi_62:
	s_cbranch_execz .Lst_fi_69
	v_add_f32_e32 v128, v124, v125
	s_waitcnt vmcnt(3)
	v_lshlrev_b32_e32 v124, 16, v122
	v_and_b32_e32 v125, 0xffff0000, v122
	v_lshlrev_b32_e32 v122, 16, v123
	v_and_b32_e32 v123, 0xffff0000, v123
	s_waitcnt vmcnt(1)
	v_pk_fma_f32 v[38:39], v[38:39], v[136:137], v[122:123]
	v_lshlrev_b32_e32 v122, 16, v120
	v_and_b32_e32 v123, 0xffff0000, v120
	v_pk_fma_f32 v[36:37], v[36:37], v[134:135], v[124:125]
	v_lshlrev_b32_e32 v120, 16, v121
	v_and_b32_e32 v121, 0xffff0000, v121
	s_waitcnt vmcnt(0)
	v_pk_fma_f32 v[122:123], v[32:33], v[126:127], v[122:123]
	v_pk_fma_f32 v[120:121], v[34:35], v[130:131], v[120:121]
	v_mov_b32_e32 v34, v123
	v_mov_b32_e32 v35, v37
	v_mov_b32_e32 v32, v122
	v_mov_b32_e32 v33, v36
	v_pk_mul_f32 v[34:35], v[34:35], v[34:35]
	s_addc_u32 s17, s69, s17
	v_pk_fma_f32 v[32:33], v[32:33], v[32:33], v[34:35]
	v_mov_b32_e32 v34, v120
	v_mov_b32_e32 v35, v38
	v_pk_fma_f32 v[32:33], v[34:35], v[34:35], v[32:33]
	v_mov_b32_e32 v34, v121
	v_mov_b32_e32 v35, v39
	v_pk_fma_f32 v[32:33], v[34:35], v[34:35], v[32:33]
	s_cmpk_gt_i32 s14, 0x1fff
	v_add_f32_e32 v33, v33, v128
	v_add_f32_e32 v32, v32, v33
	ds_bpermute_b32 v33, v67, v32
	s_waitcnt lgkmcnt(0)
	v_add_f32_e32 v32, v32, v33
.Lst_fi_63:
	s_cbranch_execz .Lst_fi_70
	ds_bpermute_b32 v33, v171, v32
	s_waitcnt lgkmcnt(0)
	v_add_f32_e32 v32, v32, v33
	ds_bpermute_b32 v33, v186, v32
	s_waitcnt lgkmcnt(0)
	v_add_f32_e32 v32, v32, v33
	ds_bpermute_b32 v33, v187, v32
	s_waitcnt lgkmcnt(0)
	v_add_f32_e32 v32, v32, v33
	ds_bpermute_b32 v33, v188, v32
	s_waitcnt lgkmcnt(0)
	v_add_f32_e32 v32, v32, v33
	ds_bpermute_b32 v33, v189, v32
	s_waitcnt lgkmcnt(0)
	v_add_f32_e32 v32, v32, v33
	v_fmamk_f32 v32, v32, 0x3a000000, v190
	v_mul_f32_e32 v33, 0x4b800000, v32
	v_cmp_gt_f32_e32 vcc, s33, v32
	s_nop 1
	v_cndmask_b32_e32 v32, v32, v33, vcc
	v_rsq_f32_e32 v32, v32
	s_nop 0
	v_mul_f32_e32 v33, 0x45800000, v32
	v_cndmask_b32_e32 v124, v32, v33, vcc
	v_pk_mul_f32 v[32:33], v[60:61], v[124:125] op_sel_hi:[1,0]
	v_pk_mul_f32 v[34:35], v[62:63], v[124:125] op_sel_hi:[1,0]
	v_pk_mul_f32 v[32:33], v[0:1], v[32:33]
	v_pk_mul_f32 v[34:35], v[2:3], v[34:35]
	global_store_dwordx4 v64, v[32:35], s[16:17]
	v_lshl_add_u64 v[60:61], s[16:17], 0, v[64:65]
	s_nop 0
	v_pk_mul_f32 v[32:33], v[56:57], v[124:125] op_sel_hi:[1,0]
	v_pk_mul_f32 v[34:35], v[58:59], v[124:125] op_sel_hi:[1,0]
.Lst_fi_64:
	s_cbranch_execz .Lst_fi_71
	v_pk_mul_f32 v[32:33], v[4:5], v[32:33]
	v_pk_mul_f32 v[34:35], v[6:7], v[34:35]
	global_store_dwordx4 v64, v[32:35], s[16:17] offset:1024
	s_nop 1
	v_pk_mul_f32 v[32:33], v[52:53], v[124:125] op_sel_hi:[1,0]
	v_pk_mul_f32 v[34:35], v[54:55], v[124:125] op_sel_hi:[1,0]
	v_pk_mul_f32 v[32:33], v[8:9], v[32:33]
	v_pk_mul_f32 v[34:35], v[10:11], v[34:35]
	global_store_dwordx4 v64, v[32:35], s[16:17] offset:2048
	s_nop 1
	v_pk_mul_f32 v[32:33], v[48:49], v[124:125] op_sel_hi:[1,0]
	v_pk_mul_f32 v[34:35], v[50:51], v[124:125] op_sel_hi:[1,0]
	v_pk_mul_f32 v[32:33], v[12:13], v[32:33]
	v_pk_mul_f32 v[34:35], v[14:15], v[34:35]
	global_store_dwordx4 v64, v[32:35], s[16:17] offset:3072
	s_nop 1
	v_pk_mul_f32 v[32:33], v[44:45], v[124:125] op_sel_hi:[1,0]
	v_pk_mul_f32 v[34:35], v[46:47], v[124:125] op_sel_hi:[1,0]
	v_add_co_u32_e32 v44, vcc, s28, v60
	v_pk_mul_f32 v[34:35], v[18:19], v[34:35]
	v_pk_mul_f32 v[32:33], v[16:17], v[32:33]
	v_addc_co_u32_e32 v45, vcc, 0, v61, vcc
	global_store_dwordx4 v[44:45], v[32:35], off
	s_nop 1
	v_pk_mul_f32 v[32:33], v[40:41], v[124:125] op_sel_hi:[1,0]
	v_pk_mul_f32 v[34:35], v[42:43], v[124:125] op_sel_hi:[1,0]
	v_pk_mul_f32 v[32:33], v[20:21], v[32:33]
.Lst_fi_65:
	s_cbranch_execz .Lst_fi_72
	v_pk_mul_f32 v[34:35], v[22:23], v[34:35]
	global_store_dwordx4 v[44:45], v[32:35], off offset:1024
	s_nop 1
	v_pk_mul_f32 v[32:33], v[36:37], v[124:125] op_sel_hi:[1,0]
	v_pk_mul_f32 v[34:35], v[38:39], v[124:125] op_sel_hi:[1,0]
	v_pk_mul_f32 v[32:33], v[24:25], v[32:33]
	v_pk_mul_f32 v[34:35], v[26:27], v[34:35]
	global_store_dwordx4 v[44:45], v[32:35], off offset:2048
	s_nop 1
	v_pk_mul_f32 v[32:33], v[122:123], v[124:125] op_sel_hi:[1,0]
	v_pk_mul_f32 v[34:35], v[120:121], v[124:125] op_sel_hi:[1,0]
	v_pk_mul_f32 v[32:33], v[28:29], v[32:33]
	v_pk_mul_f32 v[34:35], v[30:31], v[34:35]
	global_store_dwordx4 v[44:45], v[32:35], off offset:3072
	s_cbranch_scc1 .LBB0_1600
	s_ashr_i32 s15, s14, 31
	s_ashr_i32 s3, s14, 11
	s_lshl_b64 s[16:17], s[14:15], 12
	v_lshl_add_u64 v[32:33], v[68:69], 0, s[16:17]
	s_mul_i32 s16, s3, 0x3000
	s_ashr_i32 s17, s16, 31
	s_lshl_b64 s[16:17], s[16:17], 2
	s_add_u32 s16, s70, s16
	s_addc_u32 s17, s71, s17
	v_lshl_add_u64 v[34:35], s[16:17], 0, v[64:65]
	v_add_co_u32_e32 v38, vcc, s31, v34
	v_lshl_add_u64 v[36:37], v[34:35], 0, s[12:13]
	s_nop 0
	v_addc_co_u32_e32 v39, vcc, 0, v35, vcc
	v_add_co_u32_e32 v34, vcc, 0x13000, v34
	global_load_dwordx4 v[56:59], v[36:37], off offset:1024
.Lst_fi_66:
	s_cbranch_execz .Lst_fi_73
	global_load_dwordx4 v[52:55], v[36:37], off offset:2048
	global_load_dwordx2 v[150:151], v[32:33], off nt
	global_load_dwordx2 v[144:145], v[32:33], off offset:512 nt
	global_load_dwordx2 v[138:139], v[32:33], off offset:1024 nt
	global_load_dwordx2 v[132:133], v[32:33], off offset:1536 nt
	global_load_dwordx4 v[60:63], v[38:39], off
	global_load_dwordx4 v[48:51], v[36:37], off offset:3072
	v_addc_co_u32_e32 v35, vcc, 0, v35, vcc
	global_load_dwordx4 v[44:47], v[34:35], off
	global_load_dwordx4 v[40:43], v[34:35], off offset:1024
	global_load_dwordx2 v[128:129], v[32:33], off offset:2048 nt
	global_load_dwordx2 v[124:125], v[32:33], off offset:2560 nt
	global_load_dwordx2 v[122:123], v[32:33], off offset:3072 nt
	global_load_dwordx2 v[120:121], v[32:33], off offset:3584 nt
	global_load_dwordx4 v[36:39], v[34:35], off offset:2048
	s_nop 0
	global_load_dwordx4 v[32:35], v[34:35], off offset:3072
	v_cmp_lt_i32_e32 vcc, -1, v191
	s_and_b32 s24, vcc_lo, 0xffff
	s_cmp_eq_u32 s24, 0
	s_cbranch_scc1 .LBB0_1598
	s_lshl_b32 s3, s3, 8
	v_mov_b32_e32 v160, 0
	s_ashr_i32 s6, s3, 31
	v_mov_b32_e32 v161, v160
	v_mov_b32_e32 v166, v160
	v_mov_b32_e32 v167, v160
	v_mov_b32_e32 v162, v160
	v_mov_b32_e32 v163, v160
	v_mov_b32_e32 v164, v160
	v_mov_b32_e32 v165, v160
	v_mov_b32_e32 v156, v160
.Lst_fi_67:
	s_cbranch_execz .Lst_fi_74
	v_mov_b32_e32 v157, v160
	v_mov_b32_e32 v158, v160
	v_mov_b32_e32 v159, v160
	v_mov_b32_e32 v152, v160
	v_mov_b32_e32 v153, v160
	v_mov_b32_e32 v154, v160
	v_mov_b32_e32 v155, v160
	v_mov_b32_e32 v146, v160
	v_mov_b32_e32 v147, v160
	v_mov_b32_e32 v148, v160
	v_mov_b32_e32 v149, v160
	v_mov_b32_e32 v140, v160
	v_mov_b32_e32 v141, v160
	v_mov_b32_e32 v142, v160
	v_mov_b32_e32 v143, v160
	v_mov_b32_e32 v134, v160
	v_mov_b32_e32 v135, v160
	v_mov_b32_e32 v136, v160
	v_mov_b32_e32 v137, v160
	v_mov_b32_e32 v126, v160
	v_mov_b32_e32 v127, v160
	v_mov_b32_e32 v130, v160
	v_mov_b32_e32 v131, v160
	s_branch .LBB0_1681

.Lst_fi_68:
	s_cbranch_execz .Lst_fi_75
	s_mov_b32 s25, 2
	s_cmp_eq_u32 s22, 0
	s_mov_b64 s[16:17], s[4:5]
	s_cbranch_scc1 .LBB0_1684

.Lst_fi_69:
	s_cbranch_execz .Lst_fi_76
	global_load_dwordx2 v[182:183], v[168:169], off offset:512 nt
	global_load_dwordx2 v[180:181], v[168:169], off offset:1024 nt
	global_load_dwordx2 v[178:179], v[168:169], off offset:1536 nt
	global_load_dwordx2 v[176:177], v[168:169], off offset:2048 nt
	global_load_dwordx2 v[174:175], v[168:169], off offset:2560 nt
	global_load_dwordx2 v[172:173], v[168:169], off offset:3072 nt
	s_nop 0
	global_load_dwordx2 v[168:169], v[168:169], off offset:3584 nt
	s_cmp_gt_u32 s25, 1
	s_cselect_b64 s[20:21], -1, 0
	s_cmp_lt_u32 s25, 2
	v_lshlrev_b32_e32 v192, 1, v66
	s_cbranch_scc1 .LBB0_1693
	global_load_dwordx2 v[90:91], v192, s[18:19] nt
	global_load_dwordx2 v[96:97], v192, s[18:19] offset:512 nt
	global_load_dwordx2 v[102:103], v192, s[18:19] offset:1024 nt
	global_load_dwordx2 v[106:107], v192, s[18:19] offset:1536 nt
	global_load_dwordx2 v[110:111], v192, s[18:19] offset:2048 nt
	global_load_dwordx2 v[114:115], v192, s[18:19] offset:2560 nt
	global_load_dwordx2 v[116:117], v192, s[18:19] offset:3072 nt
	global_load_dwordx2 v[118:119], v192, s[18:19] offset:3584 nt
	s_cmp_gt_u32 s25, 2
	s_cselect_b64 s[18:19], -1, 0
	s_cmp_lt_u32 s25, 3
	s_cbranch_scc0 .LBB0_1694

.Lst_fi_70:
	s_cbranch_execz .Lst_fi_77
	global_load_dwordx2 v[76:77], v192, s[22:23] offset:1024 nt
	global_load_dwordx2 v[80:81], v192, s[22:23] offset:1536 nt
	global_load_dwordx2 v[84:85], v192, s[22:23] offset:2048 nt
	global_load_dwordx2 v[88:89], v192, s[22:23] offset:2560 nt
	global_load_dwordx2 v[94:95], v192, s[22:23] offset:3072 nt
	global_load_dwordx2 v[100:101], v192, s[22:23] offset:3584 nt

.Lst_fi_71:
	s_cbranch_execz .Lsc_join_fi
	s_waitcnt vmcnt(3)
	v_lshlrev_b32_e32 v178, 16, v176
	v_and_b32_e32 v179, 0xffff0000, v176
	v_lshlrev_b32_e32 v176, 16, v177
	v_and_b32_e32 v177, 0xffff0000, v177
	v_pk_add_f32 v[148:149], v[148:149], v[176:177]
	s_waitcnt vmcnt(2)
	v_lshlrev_b32_e32 v176, 16, v174
	v_and_b32_e32 v177, 0xffff0000, v174
	v_lshlrev_b32_e32 v174, 16, v175
	v_and_b32_e32 v175, 0xffff0000, v175
	v_pk_add_f32 v[142:143], v[142:143], v[174:175]
	s_waitcnt vmcnt(1)
	v_lshlrev_b32_e32 v174, 16, v172
	v_and_b32_e32 v175, 0xffff0000, v172
	v_lshlrev_b32_e32 v172, 16, v173
	v_and_b32_e32 v173, 0xffff0000, v173
	v_pk_add_f32 v[136:137], v[136:137], v[172:173]
	s_waitcnt vmcnt(0)
	v_lshlrev_b32_e32 v172, 16, v168
	v_and_b32_e32 v173, 0xffff0000, v168
	v_lshlrev_b32_e32 v168, 16, v169
	v_and_b32_e32 v169, 0xffff0000, v169
	v_pk_add_f32 v[160:161], v[160:161], v[192:193]
	v_pk_add_f32 v[162:163], v[162:163], v[184:185]
	v_pk_add_f32 v[156:157], v[156:157], v[182:183]
	v_pk_add_f32 v[152:153], v[152:153], v[180:181]
	v_pk_add_f32 v[146:147], v[146:147], v[178:179]
	v_pk_add_f32 v[140:141], v[140:141], v[176:177]
	v_pk_add_f32 v[134:135], v[134:135], v[174:175]
.Lst_fi_72:
	s_cbranch_execz .Lsc_join_fi
	v_pk_add_f32 v[126:127], v[126:127], v[172:173]
	s_andn2_b64 vcc, exec, s[20:21]
	v_pk_add_f32 v[130:131], v[130:131], v[168:169]
	s_cbranch_vccnz .LBB0_1695
	v_lshlrev_b32_e32 v168, 16, v90
	v_and_b32_e32 v169, 0xffff0000, v90
	v_pk_add_f32 v[160:161], v[160:161], v[168:169]
	v_lshlrev_b32_e32 v168, 16, v91
	v_and_b32_e32 v169, 0xffff0000, v91
	v_pk_add_f32 v[166:167], v[166:167], v[168:169]
	v_lshlrev_b32_e32 v168, 16, v96
	v_and_b32_e32 v169, 0xffff0000, v96
	v_pk_add_f32 v[162:163], v[162:163], v[168:169]
	v_lshlrev_b32_e32 v168, 16, v97
	v_and_b32_e32 v169, 0xffff0000, v97
	v_pk_add_f32 v[164:165], v[164:165], v[168:169]
	v_lshlrev_b32_e32 v168, 16, v102
	v_and_b32_e32 v169, 0xffff0000, v102
	v_pk_add_f32 v[156:157], v[156:157], v[168:169]
	v_lshlrev_b32_e32 v168, 16, v103
	v_and_b32_e32 v169, 0xffff0000, v103
	v_pk_add_f32 v[158:159], v[158:159], v[168:169]
	v_lshlrev_b32_e32 v168, 16, v106
	v_and_b32_e32 v169, 0xffff0000, v106
	v_pk_add_f32 v[152:153], v[152:153], v[168:169]
	v_lshlrev_b32_e32 v168, 16, v107
	v_and_b32_e32 v169, 0xffff0000, v107
	v_pk_add_f32 v[154:155], v[154:155], v[168:169]
	v_lshlrev_b32_e32 v168, 16, v110
	v_and_b32_e32 v169, 0xffff0000, v110
.Lst_fi_73:
	s_cbranch_execz .Lsc_join_fi
	v_pk_add_f32 v[146:147], v[146:147], v[168:169]
	v_lshlrev_b32_e32 v168, 16, v111
	v_and_b32_e32 v169, 0xffff0000, v111
	v_pk_add_f32 v[148:149], v[148:149], v[168:169]
	v_lshlrev_b32_e32 v168, 16, v114
	v_and_b32_e32 v169, 0xffff0000, v114
	v_pk_add_f32 v[140:141], v[140:141], v[168:169]
	v_lshlrev_b32_e32 v168, 16, v115
	v_and_b32_e32 v169, 0xffff0000, v115
	v_pk_add_f32 v[142:143], v[142:143], v[168:169]
	v_lshlrev_b32_e32 v168, 16, v116
	v_and_b32_e32 v169, 0xffff0000, v116
	v_pk_add_f32 v[134:135], v[134:135], v[168:169]
	v_lshlrev_b32_e32 v168, 16, v117
	v_and_b32_e32 v169, 0xffff0000, v117
	v_pk_add_f32 v[136:137], v[136:137], v[168:169]
	v_lshlrev_b32_e32 v168, 16, v118
	v_and_b32_e32 v169, 0xffff0000, v118
	v_pk_add_f32 v[126:127], v[126:127], v[168:169]
	v_lshlrev_b32_e32 v168, 16, v119
	v_and_b32_e32 v169, 0xffff0000, v119
	v_pk_add_f32 v[130:131], v[130:131], v[168:169]
	s_andn2_b64 vcc, exec, s[18:19]
	s_cbranch_vccz .LBB0_1696

.Lst_fi_74:
	s_cbranch_execz .Lsc_join_fi
	global_load_dwordx2 v[82:83], v192, s[16:17] offset:512 nt
	global_load_dwordx2 v[86:87], v192, s[16:17] offset:1024 nt
	global_load_dwordx2 v[92:93], v192, s[16:17] offset:1536 nt
	global_load_dwordx2 v[98:99], v192, s[16:17] offset:2048 nt
	global_load_dwordx2 v[104:105], v192, s[16:17] offset:2560 nt
	global_load_dwordx2 v[108:109], v192, s[16:17] offset:3072 nt
	global_load_dwordx2 v[112:113], v192, s[16:17] offset:3584 nt
	s_cmp_gt_u32 s25, 3
	s_cselect_b64 s[16:17], -1, 0
	s_cmp_lt_u32 s25, 4
	s_cbranch_scc0 .LBB0_1689
	s_branch .LBB0_1690

.Lst_fi_75:
	s_cbranch_execz .Lsc_join_fi
	v_pk_add_f32 v[158:159], v[158:159], v[168:169]
	v_lshlrev_b32_e32 v168, 16, v92
	v_and_b32_e32 v169, 0xffff0000, v92
	v_pk_add_f32 v[152:153], v[152:153], v[168:169]
	v_lshlrev_b32_e32 v168, 16, v93
	v_and_b32_e32 v169, 0xffff0000, v93
	v_pk_add_f32 v[154:155], v[154:155], v[168:169]
	v_lshlrev_b32_e32 v168, 16, v98
	v_and_b32_e32 v169, 0xffff0000, v98
	v_pk_add_f32 v[146:147], v[146:147], v[168:169]
	v_lshlrev_b32_e32 v168, 16, v99
	v_and_b32_e32 v169, 0xffff0000, v99
	v_pk_add_f32 v[148:149], v[148:149], v[168:169]
	v_lshlrev_b32_e32 v168, 16, v104
	v_and_b32_e32 v169, 0xffff0000, v104
	v_pk_add_f32 v[140:141], v[140:141], v[168:169]
	v_lshlrev_b32_e32 v168, 16, v105
	v_and_b32_e32 v169, 0xffff0000, v105
	v_pk_add_f32 v[142:143], v[142:143], v[168:169]
	v_lshlrev_b32_e32 v168, 16, v108
	v_and_b32_e32 v169, 0xffff0000, v108
	v_pk_add_f32 v[134:135], v[134:135], v[168:169]
	v_lshlrev_b32_e32 v168, 16, v109
	v_and_b32_e32 v169, 0xffff0000, v109
	v_pk_add_f32 v[136:137], v[136:137], v[168:169]
	v_lshlrev_b32_e32 v168, 16, v112
	v_and_b32_e32 v169, 0xffff0000, v112
	v_pk_add_f32 v[126:127], v[126:127], v[168:169]
	v_lshlrev_b32_e32 v168, 16, v113
.Lst_fi_76:
	s_cbranch_execz .Lsc_join_fi
	v_and_b32_e32 v169, 0xffff0000, v113
	v_pk_add_f32 v[130:131], v[130:131], v[168:169]
	s_andn2_b64 vcc, exec, s[16:17]
	s_cbranch_vccnz .LBB0_1680

.Lst_fi_77:
	s_cbranch_execz .Lsc_join_fi
	v_pk_add_f32 v[146:147], v[146:147], v[168:169]
	v_lshlrev_b32_e32 v168, 16, v85
	v_and_b32_e32 v169, 0xffff0000, v85
	v_pk_add_f32 v[148:149], v[148:149], v[168:169]
	v_lshlrev_b32_e32 v168, 16, v88
	v_and_b32_e32 v169, 0xffff0000, v88
	v_pk_add_f32 v[140:141], v[140:141], v[168:169]
	v_lshlrev_b32_e32 v168, 16, v89
	v_and_b32_e32 v169, 0xffff0000, v89
	v_pk_add_f32 v[142:143], v[142:143], v[168:169]
	v_lshlrev_b32_e32 v168, 16, v94
	v_and_b32_e32 v169, 0xffff0000, v94
	v_pk_add_f32 v[134:135], v[134:135], v[168:169]
	v_lshlrev_b32_e32 v168, 16, v95
	v_and_b32_e32 v169, 0xffff0000, v95
	v_pk_add_f32 v[136:137], v[136:137], v[168:169]
	v_lshlrev_b32_e32 v168, 16, v100
	v_and_b32_e32 v169, 0xffff0000, v100
	v_pk_add_f32 v[126:127], v[126:127], v[168:169]
	v_lshlrev_b32_e32 v168, 16, v101
	v_and_b32_e32 v169, 0xffff0000, v101
	v_pk_add_f32 v[130:131], v[130:131], v[168:169]
	s_branch .LBB0_1680

.Lsc_disp_m2:
	s_cmp_eq_u32 s80, 1
	s_cbranch_scc1 .Lst_m2_0
	s_cmp_eq_u32 s80, 2
	s_cbranch_scc1 .Lst_m2_1
	s_cmp_eq_u32 s80, 3
	s_cbranch_scc1 .Lst_m2_2
	s_cmp_eq_u32 s80, 4
	s_cbranch_scc1 .Lst_m2_3
	s_cmp_eq_u32 s80, 5
	s_cbranch_scc1 .Lst_m2_4
	s_cmp_eq_u32 s80, 6
	s_cbranch_scc1 .Lst_m2_5
	s_cmp_eq_u32 s80, 7
	s_cbranch_scc1 .Lst_m2_6
	s_branch .Lsc_join_m2
